# strategy 8: radix-8 FFT pass loops fully unrolled over two register sets, next butterfly's LDS reads issued in the shadow of the current arithmetic
# baseline (speedup 1.0000x reference)
.LBB0_758:
	v_add_u32_e32 v250, 0, v4
	v_and_b32_e32 v250, 0xffffffc0, v250
	v_lshlrev_b32_e32 v230, 3, v250
	v_add3_u32 v250, v5, v250, v230
	ds_read2_b64 v[230:233], v250 offset1:9
	ds_read2_b64 v[234:237], v250 offset0:18 offset1:27
	ds_read2_b64 v[238:241], v250 offset0:36 offset1:45
	ds_read2_b64 v[242:245], v250 offset0:54 offset1:63
	v_add_u32_e32 v38, 0x1000, v4
	v_and_b32_e32 v38, 0xffffffc0, v38
	v_lshlrev_b32_e32 v102, 3, v38
	v_add3_u32 v38, v5, v38, v102
	ds_read2_b64 v[102:105], v38 offset1:9
	ds_read2_b64 v[106:109], v38 offset0:18 offset1:27
	ds_read2_b64 v[110:113], v38 offset0:36 offset1:45
	ds_read2_b64 v[114:117], v38 offset0:54 offset1:63
	s_waitcnt lgkmcnt(5)
	v_pk_add_f32 v[246:247], v[230:231], v[238:239]
	v_pk_add_f32 v[230:231], v[230:231], v[238:239] neg_lo:[0,1] neg_hi:[0,1]
	v_pk_add_f32 v[238:239], v[232:233], v[240:241]
	v_pk_add_f32 v[232:233], v[232:233], v[240:241] neg_lo:[0,1] neg_hi:[0,1]
	v_mov_b64_e32 v[240:241], s[6:7]
	v_pk_mul_f32 v[248:249], v[232:233], v[240:241] op_sel_hi:[1,0]
	v_pk_fma_f32 v[232:233], v[232:233], v[240:241], v[248:249] op_sel:[1,1,0] op_sel_hi:[0,1,1] neg_hi:[1,0,0]
	s_waitcnt lgkmcnt(4)
	v_pk_add_f32 v[240:241], v[234:235], v[242:243]
	v_pk_add_f32 v[234:235], v[234:235], v[242:243] op_sel:[1,1] op_sel_hi:[0,0] neg_lo:[0,1] neg_hi:[1,0]
	v_pk_add_f32 v[242:243], v[236:237], v[244:245]
	v_pk_add_f32 v[236:237], v[236:237], v[244:245] neg_lo:[0,1] neg_hi:[0,1]
	v_mov_b64_e32 v[244:245], s[14:15]
	v_pk_mul_f32 v[248:249], v[236:237], v[244:245] op_sel_hi:[1,0]
	v_pk_fma_f32 v[236:237], v[236:237], v[244:245], v[248:249] op_sel:[1,1,0] op_sel_hi:[0,1,1] neg_hi:[1,0,0]
	v_pk_add_f32 v[244:245], v[246:247], v[240:241]
	v_pk_add_f32 v[240:241], v[246:247], v[240:241] neg_lo:[0,1] neg_hi:[0,1]
	v_pk_add_f32 v[246:247], v[238:239], v[242:243]
	v_pk_add_f32 v[238:239], v[238:239], v[242:243] op_sel:[1,1] op_sel_hi:[0,0] neg_lo:[0,1] neg_hi:[1,0]
	v_pk_add_f32 v[242:243], v[230:231], v[234:235]
	v_pk_add_f32 v[230:231], v[230:231], v[234:235] neg_lo:[0,1] neg_hi:[0,1]
	v_pk_add_f32 v[234:235], v[232:233], v[236:237]
	v_pk_add_f32 v[232:233], v[232:233], v[236:237] op_sel:[1,1] op_sel_hi:[0,0] neg_lo:[0,1] neg_hi:[1,0]
	v_pk_add_f32 v[236:237], v[244:245], v[246:247]
	v_pk_add_f32 v[244:245], v[244:245], v[246:247] neg_lo:[0,1] neg_hi:[0,1]
	v_pk_add_f32 v[246:247], v[240:241], v[238:239]
	v_pk_add_f32 v[238:239], v[240:241], v[238:239] neg_lo:[0,1] neg_hi:[0,1]
	v_pk_add_f32 v[240:241], v[242:243], v[234:235]
	v_pk_add_f32 v[234:235], v[242:243], v[234:235] neg_lo:[0,1] neg_hi:[0,1]
	v_pk_add_f32 v[242:243], v[230:231], v[232:233]
	v_pk_add_f32 v[230:231], v[230:231], v[232:233] neg_lo:[0,1] neg_hi:[0,1]
	v_pk_mul_f32 v[232:233], v[240:241], v[2:3] op_sel_hi:[1,0]
	v_pk_fma_f32 v[232:233], v[240:241], v[2:3], v[232:233] op_sel:[1,1,0] op_sel_hi:[0,1,1] neg_hi:[1,0,0]
	v_pk_mul_f32 v[240:241], v[2:3], v[2:3] op_sel_hi:[1,0]
	v_pk_fma_f32 v[240:241], v[2:3], v[2:3], v[240:241] op_sel:[1,1,0] op_sel_hi:[0,1,1] neg_lo:[1,0,0]
	v_pk_mul_f32 v[248:249], v[246:247], v[240:241] op_sel_hi:[1,0]
	v_pk_fma_f32 v[246:247], v[246:247], v[240:241], v[248:249] op_sel:[1,1,0] op_sel_hi:[0,1,1] neg_hi:[1,0,0]
	v_pk_mul_f32 v[248:249], v[240:241], v[2:3] op_sel_hi:[1,0]
	v_pk_fma_f32 v[240:241], v[240:241], v[2:3], v[248:249] op_sel:[1,1,0] op_sel_hi:[0,1,1] neg_lo:[1,0,0]
	v_pk_mul_f32 v[248:249], v[242:243], v[240:241] op_sel_hi:[1,0]
	v_pk_fma_f32 v[242:243], v[242:243], v[240:241], v[248:249] op_sel:[1,1,0] op_sel_hi:[0,1,1] neg_hi:[1,0,0]
	v_pk_mul_f32 v[248:249], v[240:241], v[2:3] op_sel_hi:[1,0]
	v_pk_fma_f32 v[240:241], v[240:241], v[2:3], v[248:249] op_sel:[1,1,0] op_sel_hi:[0,1,1] neg_lo:[1,0,0]
	v_pk_mul_f32 v[248:249], v[244:245], v[240:241] op_sel_hi:[1,0]
	v_pk_fma_f32 v[244:245], v[244:245], v[240:241], v[248:249] op_sel:[1,1,0] op_sel_hi:[0,1,1] neg_hi:[1,0,0]
	v_pk_mul_f32 v[248:249], v[240:241], v[2:3] op_sel_hi:[1,0]
	v_pk_fma_f32 v[240:241], v[240:241], v[2:3], v[248:249] op_sel:[1,1,0] op_sel_hi:[0,1,1] neg_lo:[1,0,0]
	v_pk_mul_f32 v[248:249], v[234:235], v[240:241] op_sel_hi:[1,0]
	v_pk_fma_f32 v[234:235], v[234:235], v[240:241], v[248:249] op_sel:[1,1,0] op_sel_hi:[0,1,1] neg_hi:[1,0,0]
	v_pk_mul_f32 v[248:249], v[240:241], v[2:3] op_sel_hi:[1,0]
	v_pk_fma_f32 v[240:241], v[240:241], v[2:3], v[248:249] op_sel:[1,1,0] op_sel_hi:[0,1,1] neg_lo:[1,0,0]
	v_pk_mul_f32 v[248:249], v[238:239], v[240:241] op_sel_hi:[1,0]
	v_pk_fma_f32 v[238:239], v[238:239], v[240:241], v[248:249] op_sel:[1,1,0] op_sel_hi:[0,1,1] neg_hi:[1,0,0]
	v_pk_mul_f32 v[248:249], v[240:241], v[2:3] op_sel_hi:[1,0]
	v_pk_fma_f32 v[240:241], v[240:241], v[2:3], v[248:249] op_sel:[1,1,0] op_sel_hi:[0,1,1] neg_lo:[1,0,0]
	v_pk_mul_f32 v[248:249], v[230:231], v[240:241] op_sel_hi:[1,0]
	v_pk_fma_f32 v[230:231], v[230:231], v[240:241], v[248:249] op_sel:[1,1,0] op_sel_hi:[0,1,1] neg_hi:[1,0,0]
	ds_write2_b64 v250, v[236:237], v[232:233] offset1:9
	ds_write2_b64 v250, v[246:247], v[242:243] offset0:18 offset1:27
	ds_write2_b64 v250, v[244:245], v[234:235] offset0:36 offset1:45
	ds_write2_b64 v250, v[238:239], v[230:231] offset0:54 offset1:63
	v_add_u32_e32 v250, 0x2000, v4
	v_and_b32_e32 v250, 0xffffffc0, v250
	v_lshlrev_b32_e32 v230, 3, v250
	v_add3_u32 v250, v5, v250, v230
	ds_read2_b64 v[230:233], v250 offset1:9
	ds_read2_b64 v[234:237], v250 offset0:18 offset1:27
	ds_read2_b64 v[238:241], v250 offset0:36 offset1:45
	ds_read2_b64 v[242:245], v250 offset0:54 offset1:63
	s_waitcnt lgkmcnt(9)
	v_pk_add_f32 v[118:119], v[102:103], v[110:111]
	v_pk_add_f32 v[102:103], v[102:103], v[110:111] neg_lo:[0,1] neg_hi:[0,1]
	v_pk_add_f32 v[110:111], v[104:105], v[112:113]
	v_pk_add_f32 v[104:105], v[104:105], v[112:113] neg_lo:[0,1] neg_hi:[0,1]
	v_mov_b64_e32 v[112:113], s[6:7]
	v_pk_mul_f32 v[120:121], v[104:105], v[112:113] op_sel_hi:[1,0]
	v_pk_fma_f32 v[104:105], v[104:105], v[112:113], v[120:121] op_sel:[1,1,0] op_sel_hi:[0,1,1] neg_hi:[1,0,0]
	s_waitcnt lgkmcnt(8)
	v_pk_add_f32 v[112:113], v[106:107], v[114:115]
	v_pk_add_f32 v[106:107], v[106:107], v[114:115] op_sel:[1,1] op_sel_hi:[0,0] neg_lo:[0,1] neg_hi:[1,0]
	v_pk_add_f32 v[114:115], v[108:109], v[116:117]
	v_pk_add_f32 v[108:109], v[108:109], v[116:117] neg_lo:[0,1] neg_hi:[0,1]
	v_mov_b64_e32 v[116:117], s[14:15]
	v_pk_mul_f32 v[120:121], v[108:109], v[116:117] op_sel_hi:[1,0]
	v_pk_fma_f32 v[108:109], v[108:109], v[116:117], v[120:121] op_sel:[1,1,0] op_sel_hi:[0,1,1] neg_hi:[1,0,0]
	v_pk_add_f32 v[116:117], v[118:119], v[112:113]
	v_pk_add_f32 v[112:113], v[118:119], v[112:113] neg_lo:[0,1] neg_hi:[0,1]
	v_pk_add_f32 v[118:119], v[110:111], v[114:115]
	v_pk_add_f32 v[110:111], v[110:111], v[114:115] op_sel:[1,1] op_sel_hi:[0,0] neg_lo:[0,1] neg_hi:[1,0]
	v_pk_add_f32 v[114:115], v[102:103], v[106:107]
	v_pk_add_f32 v[102:103], v[102:103], v[106:107] neg_lo:[0,1] neg_hi:[0,1]
	v_pk_add_f32 v[106:107], v[104:105], v[108:109]
	v_pk_add_f32 v[104:105], v[104:105], v[108:109] op_sel:[1,1] op_sel_hi:[0,0] neg_lo:[0,1] neg_hi:[1,0]
	v_pk_add_f32 v[108:109], v[116:117], v[118:119]
	v_pk_add_f32 v[116:117], v[116:117], v[118:119] neg_lo:[0,1] neg_hi:[0,1]
	v_pk_add_f32 v[118:119], v[112:113], v[110:111]
	v_pk_add_f32 v[110:111], v[112:113], v[110:111] neg_lo:[0,1] neg_hi:[0,1]
	v_pk_add_f32 v[112:113], v[114:115], v[106:107]
	v_pk_add_f32 v[106:107], v[114:115], v[106:107] neg_lo:[0,1] neg_hi:[0,1]
	v_pk_add_f32 v[114:115], v[102:103], v[104:105]
	v_pk_add_f32 v[102:103], v[102:103], v[104:105] neg_lo:[0,1] neg_hi:[0,1]
	v_pk_mul_f32 v[104:105], v[112:113], v[2:3] op_sel_hi:[1,0]
	v_pk_fma_f32 v[104:105], v[112:113], v[2:3], v[104:105] op_sel:[1,1,0] op_sel_hi:[0,1,1] neg_hi:[1,0,0]
	v_pk_mul_f32 v[112:113], v[2:3], v[2:3] op_sel_hi:[1,0]
	v_pk_fma_f32 v[112:113], v[2:3], v[2:3], v[112:113] op_sel:[1,1,0] op_sel_hi:[0,1,1] neg_lo:[1,0,0]
	v_pk_mul_f32 v[120:121], v[118:119], v[112:113] op_sel_hi:[1,0]
	v_pk_fma_f32 v[118:119], v[118:119], v[112:113], v[120:121] op_sel:[1,1,0] op_sel_hi:[0,1,1] neg_hi:[1,0,0]
	v_pk_mul_f32 v[120:121], v[112:113], v[2:3] op_sel_hi:[1,0]
	v_pk_fma_f32 v[112:113], v[112:113], v[2:3], v[120:121] op_sel:[1,1,0] op_sel_hi:[0,1,1] neg_lo:[1,0,0]
	v_pk_mul_f32 v[120:121], v[114:115], v[112:113] op_sel_hi:[1,0]
	v_pk_fma_f32 v[114:115], v[114:115], v[112:113], v[120:121] op_sel:[1,1,0] op_sel_hi:[0,1,1] neg_hi:[1,0,0]
	v_pk_mul_f32 v[120:121], v[112:113], v[2:3] op_sel_hi:[1,0]
	v_pk_fma_f32 v[112:113], v[112:113], v[2:3], v[120:121] op_sel:[1,1,0] op_sel_hi:[0,1,1] neg_lo:[1,0,0]
	v_pk_mul_f32 v[120:121], v[116:117], v[112:113] op_sel_hi:[1,0]
	v_pk_fma_f32 v[116:117], v[116:117], v[112:113], v[120:121] op_sel:[1,1,0] op_sel_hi:[0,1,1] neg_hi:[1,0,0]
	v_pk_mul_f32 v[120:121], v[112:113], v[2:3] op_sel_hi:[1,0]
	v_pk_fma_f32 v[112:113], v[112:113], v[2:3], v[120:121] op_sel:[1,1,0] op_sel_hi:[0,1,1] neg_lo:[1,0,0]
	v_pk_mul_f32 v[120:121], v[106:107], v[112:113] op_sel_hi:[1,0]
	v_pk_fma_f32 v[106:107], v[106:107], v[112:113], v[120:121] op_sel:[1,1,0] op_sel_hi:[0,1,1] neg_hi:[1,0,0]
	v_pk_mul_f32 v[120:121], v[112:113], v[2:3] op_sel_hi:[1,0]
	v_pk_fma_f32 v[112:113], v[112:113], v[2:3], v[120:121] op_sel:[1,1,0] op_sel_hi:[0,1,1] neg_lo:[1,0,0]
	v_pk_mul_f32 v[120:121], v[110:111], v[112:113] op_sel_hi:[1,0]
	v_pk_fma_f32 v[110:111], v[110:111], v[112:113], v[120:121] op_sel:[1,1,0] op_sel_hi:[0,1,1] neg_hi:[1,0,0]
	v_pk_mul_f32 v[120:121], v[112:113], v[2:3] op_sel_hi:[1,0]
	v_pk_fma_f32 v[112:113], v[112:113], v[2:3], v[120:121] op_sel:[1,1,0] op_sel_hi:[0,1,1] neg_lo:[1,0,0]
	v_pk_mul_f32 v[120:121], v[102:103], v[112:113] op_sel_hi:[1,0]
	v_pk_fma_f32 v[102:103], v[102:103], v[112:113], v[120:121] op_sel:[1,1,0] op_sel_hi:[0,1,1] neg_hi:[1,0,0]
	ds_write2_b64 v38, v[108:109], v[104:105] offset1:9
	ds_write2_b64 v38, v[118:119], v[114:115] offset0:18 offset1:27
	ds_write2_b64 v38, v[116:117], v[106:107] offset0:36 offset1:45
	ds_write2_b64 v38, v[110:111], v[102:103] offset0:54 offset1:63
	v_add_u32_e32 v38, 0x3000, v4
	v_and_b32_e32 v38, 0xffffffc0, v38
	v_lshlrev_b32_e32 v102, 3, v38
	v_add3_u32 v38, v5, v38, v102
	ds_read2_b64 v[102:105], v38 offset1:9
	ds_read2_b64 v[106:109], v38 offset0:18 offset1:27
	ds_read2_b64 v[110:113], v38 offset0:36 offset1:45
	ds_read2_b64 v[114:117], v38 offset0:54 offset1:63
	s_waitcnt lgkmcnt(9)
	v_pk_add_f32 v[246:247], v[230:231], v[238:239]
	v_pk_add_f32 v[230:231], v[230:231], v[238:239] neg_lo:[0,1] neg_hi:[0,1]
	v_pk_add_f32 v[238:239], v[232:233], v[240:241]
	v_pk_add_f32 v[232:233], v[232:233], v[240:241] neg_lo:[0,1] neg_hi:[0,1]
	v_mov_b64_e32 v[240:241], s[6:7]
	v_pk_mul_f32 v[248:249], v[232:233], v[240:241] op_sel_hi:[1,0]
	v_pk_fma_f32 v[232:233], v[232:233], v[240:241], v[248:249] op_sel:[1,1,0] op_sel_hi:[0,1,1] neg_hi:[1,0,0]
	s_waitcnt lgkmcnt(8)
	v_pk_add_f32 v[240:241], v[234:235], v[242:243]
	v_pk_add_f32 v[234:235], v[234:235], v[242:243] op_sel:[1,1] op_sel_hi:[0,0] neg_lo:[0,1] neg_hi:[1,0]
	v_pk_add_f32 v[242:243], v[236:237], v[244:245]
	v_pk_add_f32 v[236:237], v[236:237], v[244:245] neg_lo:[0,1] neg_hi:[0,1]
	v_mov_b64_e32 v[244:245], s[14:15]
	v_pk_mul_f32 v[248:249], v[236:237], v[244:245] op_sel_hi:[1,0]
	v_pk_fma_f32 v[236:237], v[236:237], v[244:245], v[248:249] op_sel:[1,1,0] op_sel_hi:[0,1,1] neg_hi:[1,0,0]
	v_pk_add_f32 v[244:245], v[246:247], v[240:241]
	v_pk_add_f32 v[240:241], v[246:247], v[240:241] neg_lo:[0,1] neg_hi:[0,1]
	v_pk_add_f32 v[246:247], v[238:239], v[242:243]
	v_pk_add_f32 v[238:239], v[238:239], v[242:243] op_sel:[1,1] op_sel_hi:[0,0] neg_lo:[0,1] neg_hi:[1,0]
	v_pk_add_f32 v[242:243], v[230:231], v[234:235]
	v_pk_add_f32 v[230:231], v[230:231], v[234:235] neg_lo:[0,1] neg_hi:[0,1]
	v_pk_add_f32 v[234:235], v[232:233], v[236:237]
	v_pk_add_f32 v[232:233], v[232:233], v[236:237] op_sel:[1,1] op_sel_hi:[0,0] neg_lo:[0,1] neg_hi:[1,0]
	v_pk_add_f32 v[236:237], v[244:245], v[246:247]
	v_pk_add_f32 v[244:245], v[244:245], v[246:247] neg_lo:[0,1] neg_hi:[0,1]
	v_pk_add_f32 v[246:247], v[240:241], v[238:239]
	v_pk_add_f32 v[238:239], v[240:241], v[238:239] neg_lo:[0,1] neg_hi:[0,1]
	v_pk_add_f32 v[240:241], v[242:243], v[234:235]
	v_pk_add_f32 v[234:235], v[242:243], v[234:235] neg_lo:[0,1] neg_hi:[0,1]
	v_pk_add_f32 v[242:243], v[230:231], v[232:233]
	v_pk_add_f32 v[230:231], v[230:231], v[232:233] neg_lo:[0,1] neg_hi:[0,1]
	v_pk_mul_f32 v[232:233], v[240:241], v[2:3] op_sel_hi:[1,0]
	v_pk_fma_f32 v[232:233], v[240:241], v[2:3], v[232:233] op_sel:[1,1,0] op_sel_hi:[0,1,1] neg_hi:[1,0,0]
	v_pk_mul_f32 v[240:241], v[2:3], v[2:3] op_sel_hi:[1,0]
	v_pk_fma_f32 v[240:241], v[2:3], v[2:3], v[240:241] op_sel:[1,1,0] op_sel_hi:[0,1,1] neg_lo:[1,0,0]
	v_pk_mul_f32 v[248:249], v[246:247], v[240:241] op_sel_hi:[1,0]
	v_pk_fma_f32 v[246:247], v[246:247], v[240:241], v[248:249] op_sel:[1,1,0] op_sel_hi:[0,1,1] neg_hi:[1,0,0]
	v_pk_mul_f32 v[248:249], v[240:241], v[2:3] op_sel_hi:[1,0]
	v_pk_fma_f32 v[240:241], v[240:241], v[2:3], v[248:249] op_sel:[1,1,0] op_sel_hi:[0,1,1] neg_lo:[1,0,0]
	v_pk_mul_f32 v[248:249], v[242:243], v[240:241] op_sel_hi:[1,0]
	v_pk_fma_f32 v[242:243], v[242:243], v[240:241], v[248:249] op_sel:[1,1,0] op_sel_hi:[0,1,1] neg_hi:[1,0,0]
	v_pk_mul_f32 v[248:249], v[240:241], v[2:3] op_sel_hi:[1,0]
	v_pk_fma_f32 v[240:241], v[240:241], v[2:3], v[248:249] op_sel:[1,1,0] op_sel_hi:[0,1,1] neg_lo:[1,0,0]
	v_pk_mul_f32 v[248:249], v[244:245], v[240:241] op_sel_hi:[1,0]
	v_pk_fma_f32 v[244:245], v[244:245], v[240:241], v[248:249] op_sel:[1,1,0] op_sel_hi:[0,1,1] neg_hi:[1,0,0]
	v_pk_mul_f32 v[248:249], v[240:241], v[2:3] op_sel_hi:[1,0]
	v_pk_fma_f32 v[240:241], v[240:241], v[2:3], v[248:249] op_sel:[1,1,0] op_sel_hi:[0,1,1] neg_lo:[1,0,0]
	v_pk_mul_f32 v[248:249], v[234:235], v[240:241] op_sel_hi:[1,0]
	v_pk_fma_f32 v[234:235], v[234:235], v[240:241], v[248:249] op_sel:[1,1,0] op_sel_hi:[0,1,1] neg_hi:[1,0,0]
	v_pk_mul_f32 v[248:249], v[240:241], v[2:3] op_sel_hi:[1,0]
	v_pk_fma_f32 v[240:241], v[240:241], v[2:3], v[248:249] op_sel:[1,1,0] op_sel_hi:[0,1,1] neg_lo:[1,0,0]
	v_pk_mul_f32 v[248:249], v[238:239], v[240:241] op_sel_hi:[1,0]
	v_pk_fma_f32 v[238:239], v[238:239], v[240:241], v[248:249] op_sel:[1,1,0] op_sel_hi:[0,1,1] neg_hi:[1,0,0]
	v_pk_mul_f32 v[248:249], v[240:241], v[2:3] op_sel_hi:[1,0]
	v_pk_fma_f32 v[240:241], v[240:241], v[2:3], v[248:249] op_sel:[1,1,0] op_sel_hi:[0,1,1] neg_lo:[1,0,0]
	v_pk_mul_f32 v[248:249], v[230:231], v[240:241] op_sel_hi:[1,0]
	v_pk_fma_f32 v[230:231], v[230:231], v[240:241], v[248:249] op_sel:[1,1,0] op_sel_hi:[0,1,1] neg_hi:[1,0,0]
	ds_write2_b64 v250, v[236:237], v[232:233] offset1:9
	ds_write2_b64 v250, v[246:247], v[242:243] offset0:18 offset1:27
	ds_write2_b64 v250, v[244:245], v[234:235] offset0:36 offset1:45
	ds_write2_b64 v250, v[238:239], v[230:231] offset0:54 offset1:63
	s_waitcnt lgkmcnt(5)
	v_pk_add_f32 v[118:119], v[102:103], v[110:111]
	v_pk_add_f32 v[102:103], v[102:103], v[110:111] neg_lo:[0,1] neg_hi:[0,1]
	v_pk_add_f32 v[110:111], v[104:105], v[112:113]
	v_pk_add_f32 v[104:105], v[104:105], v[112:113] neg_lo:[0,1] neg_hi:[0,1]
	v_mov_b64_e32 v[112:113], s[6:7]
	v_pk_mul_f32 v[120:121], v[104:105], v[112:113] op_sel_hi:[1,0]
	v_pk_fma_f32 v[104:105], v[104:105], v[112:113], v[120:121] op_sel:[1,1,0] op_sel_hi:[0,1,1] neg_hi:[1,0,0]
	s_waitcnt lgkmcnt(4)
	v_pk_add_f32 v[112:113], v[106:107], v[114:115]
	v_pk_add_f32 v[106:107], v[106:107], v[114:115] op_sel:[1,1] op_sel_hi:[0,0] neg_lo:[0,1] neg_hi:[1,0]
	v_pk_add_f32 v[114:115], v[108:109], v[116:117]
	v_pk_add_f32 v[108:109], v[108:109], v[116:117] neg_lo:[0,1] neg_hi:[0,1]
	v_mov_b64_e32 v[116:117], s[14:15]
	v_pk_mul_f32 v[120:121], v[108:109], v[116:117] op_sel_hi:[1,0]
	v_pk_fma_f32 v[108:109], v[108:109], v[116:117], v[120:121] op_sel:[1,1,0] op_sel_hi:[0,1,1] neg_hi:[1,0,0]
	v_pk_add_f32 v[116:117], v[118:119], v[112:113]
	v_pk_add_f32 v[112:113], v[118:119], v[112:113] neg_lo:[0,1] neg_hi:[0,1]
	v_pk_add_f32 v[118:119], v[110:111], v[114:115]
	v_pk_add_f32 v[110:111], v[110:111], v[114:115] op_sel:[1,1] op_sel_hi:[0,0] neg_lo:[0,1] neg_hi:[1,0]
	v_pk_add_f32 v[114:115], v[102:103], v[106:107]
	v_pk_add_f32 v[102:103], v[102:103], v[106:107] neg_lo:[0,1] neg_hi:[0,1]
	v_pk_add_f32 v[106:107], v[104:105], v[108:109]
	v_pk_add_f32 v[104:105], v[104:105], v[108:109] op_sel:[1,1] op_sel_hi:[0,0] neg_lo:[0,1] neg_hi:[1,0]
	v_pk_add_f32 v[108:109], v[116:117], v[118:119]
	v_pk_add_f32 v[116:117], v[116:117], v[118:119] neg_lo:[0,1] neg_hi:[0,1]
	v_pk_add_f32 v[118:119], v[112:113], v[110:111]
	v_pk_add_f32 v[110:111], v[112:113], v[110:111] neg_lo:[0,1] neg_hi:[0,1]
	v_pk_add_f32 v[112:113], v[114:115], v[106:107]
	v_pk_add_f32 v[106:107], v[114:115], v[106:107] neg_lo:[0,1] neg_hi:[0,1]
	v_pk_add_f32 v[114:115], v[102:103], v[104:105]
	v_pk_add_f32 v[102:103], v[102:103], v[104:105] neg_lo:[0,1] neg_hi:[0,1]
	v_pk_mul_f32 v[104:105], v[112:113], v[2:3] op_sel_hi:[1,0]
	v_pk_fma_f32 v[104:105], v[112:113], v[2:3], v[104:105] op_sel:[1,1,0] op_sel_hi:[0,1,1] neg_hi:[1,0,0]
	v_pk_mul_f32 v[112:113], v[2:3], v[2:3] op_sel_hi:[1,0]
	v_pk_fma_f32 v[112:113], v[2:3], v[2:3], v[112:113] op_sel:[1,1,0] op_sel_hi:[0,1,1] neg_lo:[1,0,0]
	v_pk_mul_f32 v[120:121], v[118:119], v[112:113] op_sel_hi:[1,0]
	v_pk_fma_f32 v[118:119], v[118:119], v[112:113], v[120:121] op_sel:[1,1,0] op_sel_hi:[0,1,1] neg_hi:[1,0,0]
	v_pk_mul_f32 v[120:121], v[112:113], v[2:3] op_sel_hi:[1,0]
	v_pk_fma_f32 v[112:113], v[112:113], v[2:3], v[120:121] op_sel:[1,1,0] op_sel_hi:[0,1,1] neg_lo:[1,0,0]
	v_pk_mul_f32 v[120:121], v[114:115], v[112:113] op_sel_hi:[1,0]
	v_pk_fma_f32 v[114:115], v[114:115], v[112:113], v[120:121] op_sel:[1,1,0] op_sel_hi:[0,1,1] neg_hi:[1,0,0]
	v_pk_mul_f32 v[120:121], v[112:113], v[2:3] op_sel_hi:[1,0]
	v_pk_fma_f32 v[112:113], v[112:113], v[2:3], v[120:121] op_sel:[1,1,0] op_sel_hi:[0,1,1] neg_lo:[1,0,0]
	v_pk_mul_f32 v[120:121], v[116:117], v[112:113] op_sel_hi:[1,0]
	v_pk_fma_f32 v[116:117], v[116:117], v[112:113], v[120:121] op_sel:[1,1,0] op_sel_hi:[0,1,1] neg_hi:[1,0,0]
	v_pk_mul_f32 v[120:121], v[112:113], v[2:3] op_sel_hi:[1,0]
	v_pk_fma_f32 v[112:113], v[112:113], v[2:3], v[120:121] op_sel:[1,1,0] op_sel_hi:[0,1,1] neg_lo:[1,0,0]
	v_pk_mul_f32 v[120:121], v[106:107], v[112:113] op_sel_hi:[1,0]
	v_pk_fma_f32 v[106:107], v[106:107], v[112:113], v[120:121] op_sel:[1,1,0] op_sel_hi:[0,1,1] neg_hi:[1,0,0]
	v_pk_mul_f32 v[120:121], v[112:113], v[2:3] op_sel_hi:[1,0]
	v_pk_fma_f32 v[112:113], v[112:113], v[2:3], v[120:121] op_sel:[1,1,0] op_sel_hi:[0,1,1] neg_lo:[1,0,0]
	v_pk_mul_f32 v[120:121], v[110:111], v[112:113] op_sel_hi:[1,0]
	v_pk_fma_f32 v[110:111], v[110:111], v[112:113], v[120:121] op_sel:[1,1,0] op_sel_hi:[0,1,1] neg_hi:[1,0,0]
	v_pk_mul_f32 v[120:121], v[112:113], v[2:3] op_sel_hi:[1,0]
	v_pk_fma_f32 v[112:113], v[112:113], v[2:3], v[120:121] op_sel:[1,1,0] op_sel_hi:[0,1,1] neg_lo:[1,0,0]
	v_pk_mul_f32 v[120:121], v[102:103], v[112:113] op_sel_hi:[1,0]
	v_pk_fma_f32 v[102:103], v[102:103], v[112:113], v[120:121] op_sel:[1,1,0] op_sel_hi:[0,1,1] neg_hi:[1,0,0]
	ds_write2_b64 v38, v[108:109], v[104:105] offset1:9
	ds_write2_b64 v38, v[118:119], v[114:115] offset0:18 offset1:27
	ds_write2_b64 v38, v[116:117], v[106:107] offset0:36 offset1:45
	ds_write2_b64 v38, v[110:111], v[102:103] offset0:54 offset1:63
	s_mov_b32 s84, 0x4000
	s_cmpk_lg_i32 s84, 0x4000
	v_mov_b32_e32 v2, v204
	s_waitcnt lgkmcnt(0)
	s_barrier
	s_mov_b32 s84, 0
	v_mul_lo_u32 v2, v2, s33
	v_add_u32_e32 v2, 0, v2
.LBB0_760:
	v_add_u32_e32 v248, 0, v2
	ds_read2_b64 v[230:233], v248 offset1:1
	ds_read2_b64 v[234:237], v248 offset0:2 offset1:3
	ds_read2_b64 v[238:241], v248 offset0:4 offset1:5
	ds_read2_b64 v[242:245], v248 offset0:6 offset1:7
	v_add_u32_e32 v3, 0x9000, v2
	ds_read2_b64 v[102:105], v3 offset1:1
	ds_read2_b64 v[106:109], v3 offset0:2 offset1:3
	ds_read2_b64 v[110:113], v3 offset0:4 offset1:5
	ds_read2_b64 v[114:117], v3 offset0:6 offset1:7
	s_waitcnt lgkmcnt(5)
	v_pk_add_f32 v[250:251], v[230:231], v[238:239]
	v_pk_add_f32 v[230:231], v[230:231], v[238:239] neg_lo:[0,1] neg_hi:[0,1]
	v_pk_add_f32 v[238:239], v[232:233], v[240:241]
	v_pk_add_f32 v[232:233], v[232:233], v[240:241] neg_lo:[0,1] neg_hi:[0,1]
	v_mov_b64_e32 v[240:241], s[6:7]
	v_pk_mul_f32 v[246:247], v[232:233], v[240:241] op_sel_hi:[1,0]
	v_pk_fma_f32 v[232:233], v[232:233], v[240:241], v[246:247] op_sel:[1,1,0] op_sel_hi:[0,1,1] neg_hi:[1,0,0]
	s_waitcnt lgkmcnt(4)
	v_pk_add_f32 v[240:241], v[234:235], v[242:243]
	v_pk_add_f32 v[234:235], v[234:235], v[242:243] op_sel:[1,1] op_sel_hi:[0,0] neg_lo:[0,1] neg_hi:[1,0]
	v_pk_add_f32 v[242:243], v[236:237], v[244:245]
	v_pk_add_f32 v[236:237], v[236:237], v[244:245] neg_lo:[0,1] neg_hi:[0,1]
	v_mov_b64_e32 v[244:245], s[14:15]
	v_pk_mul_f32 v[246:247], v[236:237], v[244:245] op_sel_hi:[1,0]
	v_pk_fma_f32 v[236:237], v[236:237], v[244:245], v[246:247] op_sel:[1,1,0] op_sel_hi:[0,1,1] neg_hi:[1,0,0]
	v_pk_add_f32 v[244:245], v[250:251], v[240:241]
	v_pk_add_f32 v[250:251], v[250:251], v[240:241] neg_lo:[0,1] neg_hi:[0,1]
	v_pk_add_f32 v[240:241], v[238:239], v[242:243]
	v_pk_add_f32 v[238:239], v[238:239], v[242:243] op_sel:[1,1] op_sel_hi:[0,0] neg_lo:[0,1] neg_hi:[1,0]
	v_pk_add_f32 v[242:243], v[230:231], v[234:235]
	v_pk_add_f32 v[230:231], v[230:231], v[234:235] neg_lo:[0,1] neg_hi:[0,1]
	v_pk_add_f32 v[234:235], v[232:233], v[236:237]
	v_pk_add_f32 v[232:233], v[232:233], v[236:237] op_sel:[1,1] op_sel_hi:[0,0] neg_lo:[0,1] neg_hi:[1,0]
	v_pk_add_f32 v[236:237], v[244:245], v[240:241]
	v_pk_add_f32 v[240:241], v[244:245], v[240:241] neg_lo:[0,1] neg_hi:[0,1]
	v_pk_add_f32 v[244:245], v[250:251], v[238:239]
	v_pk_add_f32 v[250:251], v[250:251], v[238:239] neg_lo:[0,1] neg_hi:[0,1]
	v_pk_add_f32 v[238:239], v[242:243], v[234:235]
	v_pk_add_f32 v[234:235], v[242:243], v[234:235] neg_lo:[0,1] neg_hi:[0,1]
	v_pk_add_f32 v[242:243], v[230:231], v[232:233]
	v_pk_add_f32 v[230:231], v[230:231], v[232:233] neg_lo:[0,1] neg_hi:[0,1]
	ds_write2_b64 v248, v[236:237], v[238:239] offset1:1
	ds_write2_b64 v248, v[244:245], v[242:243] offset0:2 offset1:3
	ds_write2_b64 v248, v[240:241], v[234:235] offset0:4 offset1:5
	ds_write2_b64 v248, v[250:251], v[230:231] offset0:6 offset1:7
	v_add_u32_e32 v248, 0x12000, v2
	ds_read2_b64 v[230:233], v248 offset1:1
	ds_read2_b64 v[234:237], v248 offset0:2 offset1:3
	ds_read2_b64 v[238:241], v248 offset0:4 offset1:5
	ds_read2_b64 v[242:245], v248 offset0:6 offset1:7
	s_waitcnt lgkmcnt(9)
	v_pk_add_f32 v[4:5], v[102:103], v[110:111]
	v_pk_add_f32 v[102:103], v[102:103], v[110:111] neg_lo:[0,1] neg_hi:[0,1]
	v_pk_add_f32 v[110:111], v[104:105], v[112:113]
	v_pk_add_f32 v[104:105], v[104:105], v[112:113] neg_lo:[0,1] neg_hi:[0,1]
	v_mov_b64_e32 v[112:113], s[6:7]
	v_pk_mul_f32 v[118:119], v[104:105], v[112:113] op_sel_hi:[1,0]
	v_pk_fma_f32 v[104:105], v[104:105], v[112:113], v[118:119] op_sel:[1,1,0] op_sel_hi:[0,1,1] neg_hi:[1,0,0]
	s_waitcnt lgkmcnt(8)
	v_pk_add_f32 v[112:113], v[106:107], v[114:115]
	v_pk_add_f32 v[106:107], v[106:107], v[114:115] op_sel:[1,1] op_sel_hi:[0,0] neg_lo:[0,1] neg_hi:[1,0]
	v_pk_add_f32 v[114:115], v[108:109], v[116:117]
	v_pk_add_f32 v[108:109], v[108:109], v[116:117] neg_lo:[0,1] neg_hi:[0,1]
	v_mov_b64_e32 v[116:117], s[14:15]
	v_pk_mul_f32 v[118:119], v[108:109], v[116:117] op_sel_hi:[1,0]
	v_pk_fma_f32 v[108:109], v[108:109], v[116:117], v[118:119] op_sel:[1,1,0] op_sel_hi:[0,1,1] neg_hi:[1,0,0]
	v_pk_add_f32 v[116:117], v[4:5], v[112:113]
	v_pk_add_f32 v[4:5], v[4:5], v[112:113] neg_lo:[0,1] neg_hi:[0,1]
	v_pk_add_f32 v[112:113], v[110:111], v[114:115]
	v_pk_add_f32 v[110:111], v[110:111], v[114:115] op_sel:[1,1] op_sel_hi:[0,0] neg_lo:[0,1] neg_hi:[1,0]
	v_pk_add_f32 v[114:115], v[102:103], v[106:107]
	v_pk_add_f32 v[102:103], v[102:103], v[106:107] neg_lo:[0,1] neg_hi:[0,1]
	v_pk_add_f32 v[106:107], v[104:105], v[108:109]
	v_pk_add_f32 v[104:105], v[104:105], v[108:109] op_sel:[1,1] op_sel_hi:[0,0] neg_lo:[0,1] neg_hi:[1,0]
	v_pk_add_f32 v[108:109], v[116:117], v[112:113]
	v_pk_add_f32 v[112:113], v[116:117], v[112:113] neg_lo:[0,1] neg_hi:[0,1]
	v_pk_add_f32 v[116:117], v[4:5], v[110:111]
	v_pk_add_f32 v[4:5], v[4:5], v[110:111] neg_lo:[0,1] neg_hi:[0,1]
	v_pk_add_f32 v[110:111], v[114:115], v[106:107]
	v_pk_add_f32 v[106:107], v[114:115], v[106:107] neg_lo:[0,1] neg_hi:[0,1]
	v_pk_add_f32 v[114:115], v[102:103], v[104:105]
	v_pk_add_f32 v[102:103], v[102:103], v[104:105] neg_lo:[0,1] neg_hi:[0,1]
	ds_write2_b64 v3, v[108:109], v[110:111] offset1:1
	ds_write2_b64 v3, v[116:117], v[114:115] offset0:2 offset1:3
	ds_write2_b64 v3, v[112:113], v[106:107] offset0:4 offset1:5
	ds_write2_b64 v3, v[4:5], v[102:103] offset0:6 offset1:7
	v_add_u32_e32 v3, 0x1b000, v2
	ds_read2_b64 v[102:105], v3 offset1:1
	ds_read2_b64 v[106:109], v3 offset0:2 offset1:3
	ds_read2_b64 v[110:113], v3 offset0:4 offset1:5
	ds_read2_b64 v[114:117], v3 offset0:6 offset1:7
	s_waitcnt lgkmcnt(9)
	v_pk_add_f32 v[250:251], v[230:231], v[238:239]
	v_pk_add_f32 v[230:231], v[230:231], v[238:239] neg_lo:[0,1] neg_hi:[0,1]
	v_pk_add_f32 v[238:239], v[232:233], v[240:241]
	v_pk_add_f32 v[232:233], v[232:233], v[240:241] neg_lo:[0,1] neg_hi:[0,1]
	v_mov_b64_e32 v[240:241], s[6:7]
	v_pk_mul_f32 v[246:247], v[232:233], v[240:241] op_sel_hi:[1,0]
	v_pk_fma_f32 v[232:233], v[232:233], v[240:241], v[246:247] op_sel:[1,1,0] op_sel_hi:[0,1,1] neg_hi:[1,0,0]
	s_waitcnt lgkmcnt(8)
	v_pk_add_f32 v[240:241], v[234:235], v[242:243]
	v_pk_add_f32 v[234:235], v[234:235], v[242:243] op_sel:[1,1] op_sel_hi:[0,0] neg_lo:[0,1] neg_hi:[1,0]
	v_pk_add_f32 v[242:243], v[236:237], v[244:245]
	v_pk_add_f32 v[236:237], v[236:237], v[244:245] neg_lo:[0,1] neg_hi:[0,1]
	v_mov_b64_e32 v[244:245], s[14:15]
	v_pk_mul_f32 v[246:247], v[236:237], v[244:245] op_sel_hi:[1,0]
	v_pk_fma_f32 v[236:237], v[236:237], v[244:245], v[246:247] op_sel:[1,1,0] op_sel_hi:[0,1,1] neg_hi:[1,0,0]
	v_pk_add_f32 v[244:245], v[250:251], v[240:241]
	v_pk_add_f32 v[250:251], v[250:251], v[240:241] neg_lo:[0,1] neg_hi:[0,1]
	v_pk_add_f32 v[240:241], v[238:239], v[242:243]
	v_pk_add_f32 v[238:239], v[238:239], v[242:243] op_sel:[1,1] op_sel_hi:[0,0] neg_lo:[0,1] neg_hi:[1,0]
	v_pk_add_f32 v[242:243], v[230:231], v[234:235]
	v_pk_add_f32 v[230:231], v[230:231], v[234:235] neg_lo:[0,1] neg_hi:[0,1]
	v_pk_add_f32 v[234:235], v[232:233], v[236:237]
	v_pk_add_f32 v[232:233], v[232:233], v[236:237] op_sel:[1,1] op_sel_hi:[0,0] neg_lo:[0,1] neg_hi:[1,0]
	v_pk_add_f32 v[236:237], v[244:245], v[240:241]
	v_pk_add_f32 v[240:241], v[244:245], v[240:241] neg_lo:[0,1] neg_hi:[0,1]
	v_pk_add_f32 v[244:245], v[250:251], v[238:239]
	v_pk_add_f32 v[250:251], v[250:251], v[238:239] neg_lo:[0,1] neg_hi:[0,1]
	v_pk_add_f32 v[238:239], v[242:243], v[234:235]
	v_pk_add_f32 v[234:235], v[242:243], v[234:235] neg_lo:[0,1] neg_hi:[0,1]
	v_pk_add_f32 v[242:243], v[230:231], v[232:233]
	v_pk_add_f32 v[230:231], v[230:231], v[232:233] neg_lo:[0,1] neg_hi:[0,1]
	ds_write2_b64 v248, v[236:237], v[238:239] offset1:1
	ds_write2_b64 v248, v[244:245], v[242:243] offset0:2 offset1:3
	ds_write2_b64 v248, v[240:241], v[234:235] offset0:4 offset1:5
	ds_write2_b64 v248, v[250:251], v[230:231] offset0:6 offset1:7
	s_waitcnt lgkmcnt(5)
	v_pk_add_f32 v[4:5], v[102:103], v[110:111]
	v_pk_add_f32 v[102:103], v[102:103], v[110:111] neg_lo:[0,1] neg_hi:[0,1]
	v_pk_add_f32 v[110:111], v[104:105], v[112:113]
	v_pk_add_f32 v[104:105], v[104:105], v[112:113] neg_lo:[0,1] neg_hi:[0,1]
	v_mov_b64_e32 v[112:113], s[6:7]
	v_pk_mul_f32 v[118:119], v[104:105], v[112:113] op_sel_hi:[1,0]
	v_pk_fma_f32 v[104:105], v[104:105], v[112:113], v[118:119] op_sel:[1,1,0] op_sel_hi:[0,1,1] neg_hi:[1,0,0]
	s_waitcnt lgkmcnt(4)
	v_pk_add_f32 v[112:113], v[106:107], v[114:115]
	v_pk_add_f32 v[106:107], v[106:107], v[114:115] op_sel:[1,1] op_sel_hi:[0,0] neg_lo:[0,1] neg_hi:[1,0]
	v_pk_add_f32 v[114:115], v[108:109], v[116:117]
	v_pk_add_f32 v[108:109], v[108:109], v[116:117] neg_lo:[0,1] neg_hi:[0,1]
	v_mov_b64_e32 v[116:117], s[14:15]
	v_pk_mul_f32 v[118:119], v[108:109], v[116:117] op_sel_hi:[1,0]
	v_pk_fma_f32 v[108:109], v[108:109], v[116:117], v[118:119] op_sel:[1,1,0] op_sel_hi:[0,1,1] neg_hi:[1,0,0]
	v_pk_add_f32 v[116:117], v[4:5], v[112:113]
	v_pk_add_f32 v[4:5], v[4:5], v[112:113] neg_lo:[0,1] neg_hi:[0,1]
	v_pk_add_f32 v[112:113], v[110:111], v[114:115]
	v_pk_add_f32 v[110:111], v[110:111], v[114:115] op_sel:[1,1] op_sel_hi:[0,0] neg_lo:[0,1] neg_hi:[1,0]
	v_pk_add_f32 v[114:115], v[102:103], v[106:107]
	v_pk_add_f32 v[102:103], v[102:103], v[106:107] neg_lo:[0,1] neg_hi:[0,1]
	v_pk_add_f32 v[106:107], v[104:105], v[108:109]
	v_pk_add_f32 v[104:105], v[104:105], v[108:109] op_sel:[1,1] op_sel_hi:[0,0] neg_lo:[0,1] neg_hi:[1,0]
	v_pk_add_f32 v[108:109], v[116:117], v[112:113]
	v_pk_add_f32 v[112:113], v[116:117], v[112:113] neg_lo:[0,1] neg_hi:[0,1]
	v_pk_add_f32 v[116:117], v[4:5], v[110:111]
	v_pk_add_f32 v[4:5], v[4:5], v[110:111] neg_lo:[0,1] neg_hi:[0,1]
	v_pk_add_f32 v[110:111], v[114:115], v[106:107]
	v_pk_add_f32 v[106:107], v[114:115], v[106:107] neg_lo:[0,1] neg_hi:[0,1]
	v_pk_add_f32 v[114:115], v[102:103], v[104:105]
	v_pk_add_f32 v[102:103], v[102:103], v[104:105] neg_lo:[0,1] neg_hi:[0,1]
	ds_write2_b64 v3, v[108:109], v[110:111] offset1:1
	ds_write2_b64 v3, v[116:117], v[114:115] offset0:2 offset1:3
	ds_write2_b64 v3, v[112:113], v[106:107] offset0:4 offset1:5
	ds_write2_b64 v3, v[4:5], v[102:103] offset0:6 offset1:7
	s_mov_b32 s84, 0x24000
	s_cmp_lg_u32 s84, 0x24000
	v_mov_b32_e32 v209, v208
	s_waitcnt lgkmcnt(0)
	s_barrier
	s_nop 0
	v_lshlrev_b32_e32 v3, 10, v209
	v_lshlrev_b32_e32 v4, 2, v209
	v_lshrrev_b32_e32 v5, 5, v209
	v_ashrrev_i32_e32 v38, 11, v209
	v_sub_u32_e32 v2, 0, v209
	v_and_b32_e32 v3, 0x3c00, v3
	v_and_b32_e32 v5, 56, v5
	v_and_or_b32 v4, v4, s9, v38
	v_or3_b32 v3, v4, v3, v5
	v_lshlrev_b32_e32 v4, 10, v2
	v_lshlrev_b32_e32 v5, 2, v2
	v_lshrrev_b32_e32 v38, 5, v2
	v_bfe_u32 v2, v2, 11, 3
	v_and_b32_e32 v4, 0x3c00, v4
	v_and_b32_e32 v5, 0x3c0, v5
	v_and_or_b32 v2, v38, 56, v2
	v_or3_b32 v2, v2, v5, v4
	v_add_u32_e32 v4, 1, v209
	v_lshlrev_b32_e32 v38, 10, v4
	v_lshlrev_b32_e32 v102, 2, v4
	v_lshrrev_b32_e32 v103, 5, v4
	v_ashrrev_i32_e32 v4, 11, v4
	v_not_b32_e32 v5, v209
	v_and_b32_e32 v38, 0x3c00, v38
	v_and_b32_e32 v103, 56, v103
	v_and_or_b32 v4, v102, s9, v4
	v_or3_b32 v4, v4, v38, v103
	v_lshlrev_b32_e32 v38, 10, v5
	v_lshlrev_b32_e32 v102, 2, v5
	v_lshrrev_b32_e32 v103, 5, v5
	v_bfe_u32 v5, v5, 11, 3
	v_and_b32_e32 v38, 0x3c00, v38
	v_and_b32_e32 v102, 0x3c0, v102
	v_and_or_b32 v5, v103, 56, v5
	v_mul_i32_i24_e32 v3, 9, v3
	v_mul_u32_u24_e32 v2, 9, v2
	v_or3_b32 v5, v5, v102, v38
	v_and_b32_e32 v3, -8, v3
	v_and_b32_e32 v2, 0x3fff8, v2
	v_mul_i32_i24_e32 v4, 9, v4
	v_mul_u32_u24_e32 v5, 9, v5
	v_add_u32_e32 v3, 0, v3
	v_add_u32_e32 v2, 0, v2
	v_and_b32_e32 v4, -8, v4
	v_and_b32_e32 v5, 0x3fff8, v5
	v_add_u32_e32 v4, 0, v4
	v_add_u32_e32 v5, 0, v5
	ds_read_b64 v[158:159], v3
	ds_read_b64 v[160:161], v2
	ds_read_b64 v[154:155], v4
	ds_read_b64 v[156:157], v5
	v_add_u32_e32 v2, 2, v209
	v_lshlrev_b32_e32 v4, 10, v2
	v_lshlrev_b32_e32 v5, 2, v2
	v_lshrrev_b32_e32 v38, 5, v2
	v_ashrrev_i32_e32 v2, 11, v2
	v_sub_u32_e32 v3, -2, v209
	v_and_b32_e32 v4, 0x3c00, v4
	v_and_b32_e32 v38, 56, v38
	v_and_or_b32 v2, v5, s9, v2
	v_or3_b32 v2, v2, v4, v38
	v_lshlrev_b32_e32 v4, 10, v3
	v_lshlrev_b32_e32 v5, 2, v3
	v_lshrrev_b32_e32 v38, 5, v3
	v_bfe_u32 v3, v3, 11, 3
	v_and_b32_e32 v4, 0x3c00, v4
	v_and_b32_e32 v5, 0x3c0, v5
	v_and_or_b32 v3, v38, 56, v3
	v_or3_b32 v3, v3, v5, v4
	v_add_u32_e32 v4, 3, v209
	v_lshlrev_b32_e32 v38, 10, v4
	v_lshlrev_b32_e32 v102, 2, v4
	v_lshrrev_b32_e32 v103, 5, v4
	v_ashrrev_i32_e32 v4, 11, v4
	v_sub_u32_e32 v5, -3, v209
	v_and_b32_e32 v38, 0x3c00, v38
	v_and_b32_e32 v103, 56, v103
	v_and_or_b32 v4, v102, s9, v4
	v_or3_b32 v4, v4, v38, v103
	v_lshlrev_b32_e32 v38, 10, v5
	v_lshlrev_b32_e32 v102, 2, v5
	v_lshrrev_b32_e32 v103, 5, v5
	v_bfe_u32 v5, v5, 11, 3
	v_and_b32_e32 v38, 0x3c00, v38
	v_and_b32_e32 v102, 0x3c0, v102
	v_and_or_b32 v5, v103, 56, v5
	v_mul_i32_i24_e32 v2, 9, v2
	v_or3_b32 v5, v5, v102, v38
	v_and_b32_e32 v2, -8, v2
	v_mul_u32_u24_e32 v3, 9, v3
	v_mul_i32_i24_e32 v4, 9, v4
	v_mul_u32_u24_e32 v5, 9, v5
	v_add_u32_e32 v2, 0, v2
	v_and_b32_e32 v3, 0x3fff8, v3
	v_and_b32_e32 v4, -8, v4
	v_and_b32_e32 v5, 0x3fff8, v5
	v_add_u32_e32 v3, 0, v3
	v_add_u32_e32 v4, 0, v4
	v_add_u32_e32 v5, 0, v5
	ds_read_b64 v[150:151], v2
	ds_read_b64 v[152:153], v3
	ds_read_b64 v[146:147], v4
	ds_read_b64 v[148:149], v5
	v_add_u32_e32 v2, 4, v209
	v_lshlrev_b32_e32 v4, 10, v2
	v_lshlrev_b32_e32 v5, 2, v2
	v_lshrrev_b32_e32 v38, 5, v2
	v_ashrrev_i32_e32 v2, 11, v2
	v_sub_u32_e32 v3, -4, v209
	v_and_b32_e32 v4, 0x3c00, v4
	v_and_b32_e32 v38, 56, v38
	v_and_or_b32 v2, v5, s9, v2
	v_or3_b32 v2, v2, v4, v38
	v_lshlrev_b32_e32 v4, 10, v3
	v_lshlrev_b32_e32 v5, 2, v3
	v_lshrrev_b32_e32 v38, 5, v3
	v_bfe_u32 v3, v3, 11, 3
	v_and_b32_e32 v4, 0x3c00, v4
	v_and_b32_e32 v5, 0x3c0, v5
	v_and_or_b32 v3, v38, 56, v3
	v_or3_b32 v3, v3, v5, v4
	v_add_u32_e32 v4, 5, v209
	v_lshlrev_b32_e32 v38, 10, v4
	v_lshlrev_b32_e32 v102, 2, v4
	v_lshrrev_b32_e32 v103, 5, v4
	v_ashrrev_i32_e32 v4, 11, v4
	v_sub_u32_e32 v5, -5, v209
	v_and_b32_e32 v38, 0x3c00, v38
	v_and_b32_e32 v103, 56, v103
	v_and_or_b32 v4, v102, s9, v4
	v_or3_b32 v4, v4, v38, v103
	v_lshlrev_b32_e32 v38, 10, v5
	v_lshlrev_b32_e32 v102, 2, v5
	v_lshrrev_b32_e32 v103, 5, v5
	v_bfe_u32 v5, v5, 11, 3
	v_and_b32_e32 v38, 0x3c00, v38
	v_and_b32_e32 v102, 0x3c0, v102
	v_and_or_b32 v5, v103, 56, v5
	v_mul_i32_i24_e32 v2, 9, v2
	v_or3_b32 v5, v5, v102, v38
	v_and_b32_e32 v2, -8, v2
	v_mul_u32_u24_e32 v3, 9, v3
	v_mul_i32_i24_e32 v4, 9, v4
	v_mul_u32_u24_e32 v5, 9, v5
	v_add_u32_e32 v2, 0, v2
	v_and_b32_e32 v3, 0x3fff8, v3
	v_and_b32_e32 v4, -8, v4
	v_and_b32_e32 v5, 0x3fff8, v5
	v_add_u32_e32 v3, 0, v3
	v_add_u32_e32 v4, 0, v4
	v_add_u32_e32 v5, 0, v5
	ds_read_b64 v[142:143], v2
	ds_read_b64 v[144:145], v3
	ds_read_b64 v[138:139], v4
	ds_read_b64 v[140:141], v5
	v_add_u32_e32 v2, 6, v209
	v_lshlrev_b32_e32 v4, 10, v2
	v_lshlrev_b32_e32 v5, 2, v2
	v_lshrrev_b32_e32 v38, 5, v2
	v_ashrrev_i32_e32 v2, 11, v2
	v_sub_u32_e32 v3, -6, v209
	v_and_b32_e32 v4, 0x3c00, v4
	v_and_b32_e32 v38, 56, v38
	v_and_or_b32 v2, v5, s9, v2
	v_or3_b32 v2, v2, v4, v38
	v_lshlrev_b32_e32 v4, 10, v3
	v_lshlrev_b32_e32 v5, 2, v3
	v_lshrrev_b32_e32 v38, 5, v3
	v_bfe_u32 v3, v3, 11, 3
	v_and_b32_e32 v4, 0x3c00, v4
	v_and_b32_e32 v5, 0x3c0, v5
	v_and_or_b32 v3, v38, 56, v3
	v_or3_b32 v3, v3, v5, v4
	v_add_u32_e32 v4, 7, v209
	v_lshlrev_b32_e32 v38, 10, v4
	v_lshlrev_b32_e32 v102, 2, v4
	v_lshrrev_b32_e32 v103, 5, v4
	v_ashrrev_i32_e32 v4, 11, v4
	v_sub_u32_e32 v5, -7, v209
	v_and_b32_e32 v38, 0x3c00, v38
	v_and_b32_e32 v103, 56, v103
	v_and_or_b32 v4, v102, s9, v4
	v_or3_b32 v4, v4, v38, v103
	v_lshlrev_b32_e32 v38, 10, v5
	v_lshlrev_b32_e32 v102, 2, v5
	v_lshrrev_b32_e32 v103, 5, v5
	v_bfe_u32 v5, v5, 11, 3
	v_and_b32_e32 v38, 0x3c00, v38
	v_and_b32_e32 v102, 0x3c0, v102
	v_and_or_b32 v5, v103, 56, v5
	v_mul_i32_i24_e32 v2, 9, v2
	v_or3_b32 v5, v5, v102, v38
	v_and_b32_e32 v2, -8, v2
	v_mul_u32_u24_e32 v3, 9, v3
	v_mul_i32_i24_e32 v4, 9, v4
	v_mul_u32_u24_e32 v5, 9, v5
	v_add_u32_e32 v2, 0, v2
	v_and_b32_e32 v3, 0x3fff8, v3
	v_and_b32_e32 v4, -8, v4
	v_and_b32_e32 v5, 0x3fff8, v5
	v_add_u32_e32 v3, 0, v3
	v_add_u32_e32 v4, 0, v4
	v_add_u32_e32 v5, 0, v5
	ds_read_b64 v[134:135], v2
	ds_read_b64 v[136:137], v3
	ds_read_b64 v[130:131], v4
	ds_read_b64 v[132:133], v5
	v_add_u32_e32 v2, 8, v209
	v_lshlrev_b32_e32 v4, 10, v2
	v_lshlrev_b32_e32 v5, 2, v2
	v_lshrrev_b32_e32 v38, 5, v2
	v_ashrrev_i32_e32 v2, 11, v2
	v_sub_u32_e32 v3, -8, v209
	v_and_b32_e32 v4, 0x3c00, v4
	v_and_b32_e32 v38, 56, v38
	v_and_or_b32 v2, v5, s9, v2
	v_or3_b32 v2, v2, v4, v38
	v_lshlrev_b32_e32 v4, 10, v3
	v_lshlrev_b32_e32 v5, 2, v3
	v_lshrrev_b32_e32 v38, 5, v3
	v_bfe_u32 v3, v3, 11, 3
	v_and_b32_e32 v4, 0x3c00, v4
	v_and_b32_e32 v5, 0x3c0, v5
	v_and_or_b32 v3, v38, 56, v3
	v_or3_b32 v3, v3, v5, v4
	v_add_u32_e32 v4, 9, v209
	v_lshlrev_b32_e32 v38, 10, v4
	v_lshlrev_b32_e32 v102, 2, v4
	v_lshrrev_b32_e32 v103, 5, v4
	v_ashrrev_i32_e32 v4, 11, v4
	v_sub_u32_e32 v5, -9, v209
	v_and_b32_e32 v38, 0x3c00, v38
	v_and_b32_e32 v103, 56, v103
	v_and_or_b32 v4, v102, s9, v4
	v_or3_b32 v4, v4, v38, v103
	v_lshlrev_b32_e32 v38, 10, v5
	v_lshlrev_b32_e32 v102, 2, v5
	v_lshrrev_b32_e32 v103, 5, v5
	v_bfe_u32 v5, v5, 11, 3
	v_and_b32_e32 v38, 0x3c00, v38
	v_and_b32_e32 v102, 0x3c0, v102
	v_and_or_b32 v5, v103, 56, v5
	v_mul_i32_i24_e32 v2, 9, v2
	v_or3_b32 v5, v5, v102, v38
	v_and_b32_e32 v2, -8, v2
	v_mul_u32_u24_e32 v3, 9, v3
	v_mul_i32_i24_e32 v4, 9, v4
	v_mul_u32_u24_e32 v5, 9, v5
	v_add_u32_e32 v2, 0, v2
	v_and_b32_e32 v3, 0x3fff8, v3
	v_and_b32_e32 v4, -8, v4
	v_and_b32_e32 v5, 0x3fff8, v5
	v_add_u32_e32 v3, 0, v3
	v_add_u32_e32 v4, 0, v4
	v_add_u32_e32 v5, 0, v5
	ds_read_b64 v[126:127], v2
	ds_read_b64 v[128:129], v3
	ds_read_b64 v[122:123], v4
	ds_read_b64 v[124:125], v5
	v_add_u32_e32 v2, 10, v209
	v_lshlrev_b32_e32 v4, 10, v2
	v_lshlrev_b32_e32 v5, 2, v2
	v_lshrrev_b32_e32 v38, 5, v2
	v_ashrrev_i32_e32 v2, 11, v2
	v_sub_u32_e32 v3, -10, v209
	v_and_b32_e32 v4, 0x3c00, v4
	v_and_b32_e32 v38, 56, v38
	v_and_or_b32 v2, v5, s9, v2
	v_or3_b32 v2, v2, v4, v38
	v_lshlrev_b32_e32 v4, 10, v3
	v_lshlrev_b32_e32 v5, 2, v3
	v_lshrrev_b32_e32 v38, 5, v3
	v_bfe_u32 v3, v3, 11, 3
	v_and_b32_e32 v4, 0x3c00, v4
	v_and_b32_e32 v5, 0x3c0, v5
	v_and_or_b32 v3, v38, 56, v3
	v_or3_b32 v3, v3, v5, v4
	v_add_u32_e32 v4, 11, v209
	v_lshlrev_b32_e32 v38, 10, v4
	v_lshlrev_b32_e32 v102, 2, v4
	v_lshrrev_b32_e32 v103, 5, v4
	v_ashrrev_i32_e32 v4, 11, v4
	v_sub_u32_e32 v5, -11, v209
	v_and_b32_e32 v38, 0x3c00, v38
	v_and_b32_e32 v103, 56, v103
	v_and_or_b32 v4, v102, s9, v4
	v_or3_b32 v4, v4, v38, v103
	v_lshlrev_b32_e32 v38, 10, v5
	v_lshlrev_b32_e32 v102, 2, v5
	v_lshrrev_b32_e32 v103, 5, v5
	v_bfe_u32 v5, v5, 11, 3
	v_and_b32_e32 v38, 0x3c00, v38
	v_and_b32_e32 v102, 0x3c0, v102
	v_and_or_b32 v5, v103, 56, v5
	v_mul_i32_i24_e32 v2, 9, v2
	v_or3_b32 v5, v5, v102, v38
	v_and_b32_e32 v2, -8, v2
	v_mul_u32_u24_e32 v3, 9, v3
	v_mul_i32_i24_e32 v4, 9, v4
	v_mul_u32_u24_e32 v5, 9, v5
	v_add_u32_e32 v2, 0, v2
	v_and_b32_e32 v3, 0x3fff8, v3
	v_and_b32_e32 v4, -8, v4
	v_and_b32_e32 v5, 0x3fff8, v5
	v_add_u32_e32 v3, 0, v3
	v_add_u32_e32 v4, 0, v4
	v_add_u32_e32 v5, 0, v5
	ds_read_b64 v[118:119], v2
	ds_read_b64 v[120:121], v3
	ds_read_b64 v[114:115], v4
	ds_read_b64 v[116:117], v5
	v_add_u32_e32 v2, 12, v209
	v_lshlrev_b32_e32 v4, 10, v2
	v_lshlrev_b32_e32 v5, 2, v2
	v_lshrrev_b32_e32 v38, 5, v2
	v_ashrrev_i32_e32 v2, 11, v2
	v_sub_u32_e32 v3, -12, v209
	v_and_b32_e32 v4, 0x3c00, v4
	v_and_b32_e32 v38, 56, v38
	v_and_or_b32 v2, v5, s9, v2
	v_or3_b32 v2, v2, v4, v38
	v_lshlrev_b32_e32 v4, 10, v3
	v_lshlrev_b32_e32 v5, 2, v3
	v_lshrrev_b32_e32 v38, 5, v3
	v_bfe_u32 v3, v3, 11, 3
	v_and_b32_e32 v4, 0x3c00, v4
	v_and_b32_e32 v5, 0x3c0, v5
	v_and_or_b32 v3, v38, 56, v3
	v_or3_b32 v3, v3, v5, v4
	v_add_u32_e32 v4, 13, v209
	v_lshlrev_b32_e32 v38, 10, v4
	v_lshlrev_b32_e32 v102, 2, v4
	v_lshrrev_b32_e32 v103, 5, v4
	v_ashrrev_i32_e32 v4, 11, v4
	v_sub_u32_e32 v5, -13, v209
	v_and_b32_e32 v38, 0x3c00, v38
	v_and_b32_e32 v103, 56, v103
	v_and_or_b32 v4, v102, s9, v4
	v_or3_b32 v4, v4, v38, v103
	v_lshlrev_b32_e32 v38, 10, v5
	v_lshlrev_b32_e32 v102, 2, v5
	v_lshrrev_b32_e32 v103, 5, v5
	v_bfe_u32 v5, v5, 11, 3
	v_and_b32_e32 v38, 0x3c00, v38
	v_and_b32_e32 v102, 0x3c0, v102
	v_and_or_b32 v5, v103, 56, v5
	v_mul_i32_i24_e32 v2, 9, v2
	v_or3_b32 v5, v5, v102, v38
	v_and_b32_e32 v2, -8, v2
	v_mul_u32_u24_e32 v3, 9, v3
	v_mul_i32_i24_e32 v4, 9, v4
	v_mul_u32_u24_e32 v5, 9, v5
	v_add_u32_e32 v2, 0, v2
	v_and_b32_e32 v3, 0x3fff8, v3
	v_and_b32_e32 v4, -8, v4
	v_and_b32_e32 v5, 0x3fff8, v5
	v_add_u32_e32 v3, 0, v3
	v_add_u32_e32 v4, 0, v4
	v_add_u32_e32 v5, 0, v5
	ds_read_b64 v[110:111], v2
	ds_read_b64 v[112:113], v3
	ds_read_b64 v[106:107], v4
	ds_read_b64 v[108:109], v5
	v_add_u32_e32 v2, 14, v209
	v_lshlrev_b32_e32 v4, 10, v2
	v_lshlrev_b32_e32 v5, 2, v2
	v_lshrrev_b32_e32 v38, 5, v2
	v_ashrrev_i32_e32 v2, 11, v2
	v_sub_u32_e32 v3, -14, v209
	v_and_b32_e32 v4, 0x3c00, v4
	v_and_b32_e32 v38, 56, v38
	v_and_or_b32 v2, v5, s9, v2
	v_or3_b32 v2, v2, v4, v38
	v_lshlrev_b32_e32 v4, 10, v3
	v_lshlrev_b32_e32 v5, 2, v3
	v_lshrrev_b32_e32 v38, 5, v3
	v_bfe_u32 v3, v3, 11, 3
	v_and_b32_e32 v4, 0x3c00, v4
	v_and_b32_e32 v5, 0x3c0, v5
	v_and_or_b32 v3, v38, 56, v3
	v_or3_b32 v3, v3, v5, v4
	v_add_u32_e32 v4, 15, v209
	v_lshlrev_b32_e32 v38, 10, v4
	v_lshlrev_b32_e32 v102, 2, v4
	v_lshrrev_b32_e32 v103, 5, v4
	v_ashrrev_i32_e32 v4, 11, v4
	v_sub_u32_e32 v5, -15, v209
	v_and_b32_e32 v38, 0x3c00, v38
	v_and_b32_e32 v103, 56, v103
	v_and_or_b32 v4, v102, s9, v4
	v_or3_b32 v4, v4, v38, v103
	v_lshlrev_b32_e32 v38, 10, v5
	v_lshlrev_b32_e32 v102, 2, v5
	v_lshrrev_b32_e32 v103, 5, v5
	v_bfe_u32 v5, v5, 11, 3
	v_and_b32_e32 v38, 0x3c00, v38
	v_and_b32_e32 v102, 0x3c0, v102
	v_and_or_b32 v5, v103, 56, v5
	v_or3_b32 v5, v5, v102, v38
	v_mul_i32_i24_e32 v2, 9, v2
	v_mul_u32_u24_e32 v3, 9, v3
	v_mul_i32_i24_e32 v4, 9, v4
	v_mul_u32_u24_e32 v5, 9, v5
	v_and_b32_e32 v2, -8, v2
	v_and_b32_e32 v3, 0x3fff8, v3
	v_and_b32_e32 v4, -8, v4
	v_and_b32_e32 v5, 0x3fff8, v5
	v_add_u32_e32 v2, 0, v2
	v_add_u32_e32 v3, 0, v3
	v_add_u32_e32 v4, 0, v4
	v_add_u32_e32 v5, 0, v5
	ds_read_b64 v[102:103], v2
	ds_read_b64 v[104:105], v3
	ds_read_b64 v[2:3], v4
	ds_read_b64 v[4:5], v5
	s_and_saveexec_b64 s[84:85], s[0:1]
	s_cbranch_execz .LBB0_763
	ds_read_b64 v[162:163], v203 offset:32
	v_mov_b32_e32 v38, s94
	s_waitcnt lgkmcnt(0)
	ds_write_b64 v38, v[162:163]

.LBB0_766:
	v_add_u32_e32 v250, 0, v38
	v_and_b32_e32 v250, 0xffffffc0, v250
	v_lshlrev_b32_e32 v230, 3, v250
	v_add3_u32 v250, v164, v250, v230
	ds_read2_b64 v[230:233], v250 offset1:9
	ds_read2_b64 v[234:237], v250 offset0:18 offset1:27
	ds_read2_b64 v[238:241], v250 offset0:36 offset1:45
	ds_read2_b64 v[242:245], v250 offset0:54 offset1:63
	v_add_u32_e32 v165, 0x1000, v38
	v_and_b32_e32 v165, 0xffffffc0, v165
	v_lshlrev_b32_e32 v166, 3, v165
	v_add3_u32 v165, v164, v165, v166
	ds_read2_b64 v[166:169], v165 offset1:9
	ds_read2_b64 v[170:173], v165 offset0:18 offset1:27
	ds_read2_b64 v[174:177], v165 offset0:36 offset1:45
	ds_read2_b64 v[178:181], v165 offset0:54 offset1:63
	s_waitcnt lgkmcnt(5)
	v_pk_add_f32 v[246:247], v[230:231], v[238:239]
	v_pk_add_f32 v[230:231], v[230:231], v[238:239] neg_lo:[0,1] neg_hi:[0,1]
	v_pk_add_f32 v[238:239], v[232:233], v[240:241]
	v_pk_add_f32 v[232:233], v[232:233], v[240:241] neg_lo:[0,1] neg_hi:[0,1]
	v_mov_b64_e32 v[240:241], s[6:7]
	v_pk_mul_f32 v[248:249], v[232:233], v[240:241] op_sel_hi:[1,0]
	v_pk_fma_f32 v[232:233], v[232:233], v[240:241], v[248:249] op_sel:[1,1,0] op_sel_hi:[0,1,1] neg_hi:[1,0,0]
	s_waitcnt lgkmcnt(4)
	v_pk_add_f32 v[240:241], v[234:235], v[242:243]
	v_pk_add_f32 v[234:235], v[234:235], v[242:243] op_sel:[1,1] op_sel_hi:[0,0] neg_lo:[0,1] neg_hi:[1,0]
	v_pk_add_f32 v[242:243], v[236:237], v[244:245]
	v_pk_add_f32 v[236:237], v[236:237], v[244:245] neg_lo:[0,1] neg_hi:[0,1]
	v_mov_b64_e32 v[244:245], s[14:15]
	v_pk_mul_f32 v[248:249], v[236:237], v[244:245] op_sel_hi:[1,0]
	v_pk_fma_f32 v[236:237], v[236:237], v[244:245], v[248:249] op_sel:[1,1,0] op_sel_hi:[0,1,1] neg_hi:[1,0,0]
	v_pk_add_f32 v[244:245], v[246:247], v[240:241]
	v_pk_add_f32 v[240:241], v[246:247], v[240:241] neg_lo:[0,1] neg_hi:[0,1]
	v_pk_add_f32 v[246:247], v[238:239], v[242:243]
	v_pk_add_f32 v[238:239], v[238:239], v[242:243] op_sel:[1,1] op_sel_hi:[0,0] neg_lo:[0,1] neg_hi:[1,0]
	v_pk_add_f32 v[242:243], v[230:231], v[234:235]
	v_pk_add_f32 v[230:231], v[230:231], v[234:235] neg_lo:[0,1] neg_hi:[0,1]
	v_pk_add_f32 v[234:235], v[232:233], v[236:237]
	v_pk_add_f32 v[232:233], v[232:233], v[236:237] op_sel:[1,1] op_sel_hi:[0,0] neg_lo:[0,1] neg_hi:[1,0]
	v_pk_add_f32 v[236:237], v[244:245], v[246:247]
	v_pk_add_f32 v[244:245], v[244:245], v[246:247] neg_lo:[0,1] neg_hi:[0,1]
	v_pk_add_f32 v[246:247], v[240:241], v[238:239]
	v_pk_add_f32 v[238:239], v[240:241], v[238:239] neg_lo:[0,1] neg_hi:[0,1]
	v_pk_add_f32 v[240:241], v[242:243], v[234:235]
	v_pk_add_f32 v[234:235], v[242:243], v[234:235] neg_lo:[0,1] neg_hi:[0,1]
	v_pk_add_f32 v[242:243], v[230:231], v[232:233]
	v_pk_add_f32 v[230:231], v[230:231], v[232:233] neg_lo:[0,1] neg_hi:[0,1]
	v_pk_mul_f32 v[232:233], v[240:241], v[162:163] op_sel_hi:[1,0]
	v_pk_fma_f32 v[232:233], v[240:241], v[162:163], v[232:233] op_sel:[1,1,0] op_sel_hi:[0,1,1] neg_hi:[1,0,0]
	v_pk_mul_f32 v[240:241], v[162:163], v[162:163] op_sel_hi:[1,0]
	v_pk_fma_f32 v[240:241], v[162:163], v[162:163], v[240:241] op_sel:[1,1,0] op_sel_hi:[0,1,1] neg_lo:[1,0,0]
	v_pk_mul_f32 v[248:249], v[246:247], v[240:241] op_sel_hi:[1,0]
	v_pk_fma_f32 v[246:247], v[246:247], v[240:241], v[248:249] op_sel:[1,1,0] op_sel_hi:[0,1,1] neg_hi:[1,0,0]
	v_pk_mul_f32 v[248:249], v[240:241], v[162:163] op_sel_hi:[1,0]
	v_pk_fma_f32 v[240:241], v[240:241], v[162:163], v[248:249] op_sel:[1,1,0] op_sel_hi:[0,1,1] neg_lo:[1,0,0]
	v_pk_mul_f32 v[248:249], v[242:243], v[240:241] op_sel_hi:[1,0]
	v_pk_fma_f32 v[242:243], v[242:243], v[240:241], v[248:249] op_sel:[1,1,0] op_sel_hi:[0,1,1] neg_hi:[1,0,0]
	v_pk_mul_f32 v[248:249], v[240:241], v[162:163] op_sel_hi:[1,0]
	v_pk_fma_f32 v[240:241], v[240:241], v[162:163], v[248:249] op_sel:[1,1,0] op_sel_hi:[0,1,1] neg_lo:[1,0,0]
	v_pk_mul_f32 v[248:249], v[244:245], v[240:241] op_sel_hi:[1,0]
	v_pk_fma_f32 v[244:245], v[244:245], v[240:241], v[248:249] op_sel:[1,1,0] op_sel_hi:[0,1,1] neg_hi:[1,0,0]
	v_pk_mul_f32 v[248:249], v[240:241], v[162:163] op_sel_hi:[1,0]
	v_pk_fma_f32 v[240:241], v[240:241], v[162:163], v[248:249] op_sel:[1,1,0] op_sel_hi:[0,1,1] neg_lo:[1,0,0]
	v_pk_mul_f32 v[248:249], v[234:235], v[240:241] op_sel_hi:[1,0]
	v_pk_fma_f32 v[234:235], v[234:235], v[240:241], v[248:249] op_sel:[1,1,0] op_sel_hi:[0,1,1] neg_hi:[1,0,0]
	v_pk_mul_f32 v[248:249], v[240:241], v[162:163] op_sel_hi:[1,0]
	v_pk_fma_f32 v[240:241], v[240:241], v[162:163], v[248:249] op_sel:[1,1,0] op_sel_hi:[0,1,1] neg_lo:[1,0,0]
	v_pk_mul_f32 v[248:249], v[238:239], v[240:241] op_sel_hi:[1,0]
	v_pk_fma_f32 v[238:239], v[238:239], v[240:241], v[248:249] op_sel:[1,1,0] op_sel_hi:[0,1,1] neg_hi:[1,0,0]
	v_pk_mul_f32 v[248:249], v[240:241], v[162:163] op_sel_hi:[1,0]
	v_pk_fma_f32 v[240:241], v[240:241], v[162:163], v[248:249] op_sel:[1,1,0] op_sel_hi:[0,1,1] neg_lo:[1,0,0]
	v_pk_mul_f32 v[248:249], v[230:231], v[240:241] op_sel_hi:[1,0]
	v_pk_fma_f32 v[230:231], v[230:231], v[240:241], v[248:249] op_sel:[1,1,0] op_sel_hi:[0,1,1] neg_hi:[1,0,0]
	ds_write2_b64 v250, v[236:237], v[232:233] offset1:9
	ds_write2_b64 v250, v[246:247], v[242:243] offset0:18 offset1:27
	ds_write2_b64 v250, v[244:245], v[234:235] offset0:36 offset1:45
	ds_write2_b64 v250, v[238:239], v[230:231] offset0:54 offset1:63
	v_add_u32_e32 v250, 0x2000, v38
	v_and_b32_e32 v250, 0xffffffc0, v250
	v_lshlrev_b32_e32 v230, 3, v250
	v_add3_u32 v250, v164, v250, v230
	ds_read2_b64 v[230:233], v250 offset1:9
	ds_read2_b64 v[234:237], v250 offset0:18 offset1:27
	ds_read2_b64 v[238:241], v250 offset0:36 offset1:45
	ds_read2_b64 v[242:245], v250 offset0:54 offset1:63
	s_waitcnt lgkmcnt(9)
	v_pk_add_f32 v[182:183], v[166:167], v[174:175]
	v_pk_add_f32 v[166:167], v[166:167], v[174:175] neg_lo:[0,1] neg_hi:[0,1]
	v_pk_add_f32 v[174:175], v[168:169], v[176:177]
	v_pk_add_f32 v[168:169], v[168:169], v[176:177] neg_lo:[0,1] neg_hi:[0,1]
	v_mov_b64_e32 v[176:177], s[6:7]
	v_pk_mul_f32 v[184:185], v[168:169], v[176:177] op_sel_hi:[1,0]
	v_pk_fma_f32 v[168:169], v[168:169], v[176:177], v[184:185] op_sel:[1,1,0] op_sel_hi:[0,1,1] neg_hi:[1,0,0]
	s_waitcnt lgkmcnt(8)
	v_pk_add_f32 v[176:177], v[170:171], v[178:179]
	v_pk_add_f32 v[170:171], v[170:171], v[178:179] op_sel:[1,1] op_sel_hi:[0,0] neg_lo:[0,1] neg_hi:[1,0]
	v_pk_add_f32 v[178:179], v[172:173], v[180:181]
	v_pk_add_f32 v[172:173], v[172:173], v[180:181] neg_lo:[0,1] neg_hi:[0,1]
	v_mov_b64_e32 v[180:181], s[14:15]
	v_pk_mul_f32 v[184:185], v[172:173], v[180:181] op_sel_hi:[1,0]
	v_pk_fma_f32 v[172:173], v[172:173], v[180:181], v[184:185] op_sel:[1,1,0] op_sel_hi:[0,1,1] neg_hi:[1,0,0]
	v_pk_add_f32 v[180:181], v[182:183], v[176:177]
	v_pk_add_f32 v[176:177], v[182:183], v[176:177] neg_lo:[0,1] neg_hi:[0,1]
	v_pk_add_f32 v[182:183], v[174:175], v[178:179]
	v_pk_add_f32 v[174:175], v[174:175], v[178:179] op_sel:[1,1] op_sel_hi:[0,0] neg_lo:[0,1] neg_hi:[1,0]
	v_pk_add_f32 v[178:179], v[166:167], v[170:171]
	v_pk_add_f32 v[166:167], v[166:167], v[170:171] neg_lo:[0,1] neg_hi:[0,1]
	v_pk_add_f32 v[170:171], v[168:169], v[172:173]
	v_pk_add_f32 v[168:169], v[168:169], v[172:173] op_sel:[1,1] op_sel_hi:[0,0] neg_lo:[0,1] neg_hi:[1,0]
	v_pk_add_f32 v[172:173], v[180:181], v[182:183]
	v_pk_add_f32 v[180:181], v[180:181], v[182:183] neg_lo:[0,1] neg_hi:[0,1]
	v_pk_add_f32 v[182:183], v[176:177], v[174:175]
	v_pk_add_f32 v[174:175], v[176:177], v[174:175] neg_lo:[0,1] neg_hi:[0,1]
	v_pk_add_f32 v[176:177], v[178:179], v[170:171]
	v_pk_add_f32 v[170:171], v[178:179], v[170:171] neg_lo:[0,1] neg_hi:[0,1]
	v_pk_add_f32 v[178:179], v[166:167], v[168:169]
	v_pk_add_f32 v[166:167], v[166:167], v[168:169] neg_lo:[0,1] neg_hi:[0,1]
	v_pk_mul_f32 v[168:169], v[176:177], v[162:163] op_sel_hi:[1,0]
	v_pk_fma_f32 v[168:169], v[176:177], v[162:163], v[168:169] op_sel:[1,1,0] op_sel_hi:[0,1,1] neg_hi:[1,0,0]
	v_pk_mul_f32 v[176:177], v[162:163], v[162:163] op_sel_hi:[1,0]
	v_pk_fma_f32 v[176:177], v[162:163], v[162:163], v[176:177] op_sel:[1,1,0] op_sel_hi:[0,1,1] neg_lo:[1,0,0]
	v_pk_mul_f32 v[184:185], v[182:183], v[176:177] op_sel_hi:[1,0]
	v_pk_fma_f32 v[182:183], v[182:183], v[176:177], v[184:185] op_sel:[1,1,0] op_sel_hi:[0,1,1] neg_hi:[1,0,0]
	v_pk_mul_f32 v[184:185], v[176:177], v[162:163] op_sel_hi:[1,0]
	v_pk_fma_f32 v[176:177], v[176:177], v[162:163], v[184:185] op_sel:[1,1,0] op_sel_hi:[0,1,1] neg_lo:[1,0,0]
	v_pk_mul_f32 v[184:185], v[178:179], v[176:177] op_sel_hi:[1,0]
	v_pk_fma_f32 v[178:179], v[178:179], v[176:177], v[184:185] op_sel:[1,1,0] op_sel_hi:[0,1,1] neg_hi:[1,0,0]
	v_pk_mul_f32 v[184:185], v[176:177], v[162:163] op_sel_hi:[1,0]
	v_pk_fma_f32 v[176:177], v[176:177], v[162:163], v[184:185] op_sel:[1,1,0] op_sel_hi:[0,1,1] neg_lo:[1,0,0]
	v_pk_mul_f32 v[184:185], v[180:181], v[176:177] op_sel_hi:[1,0]
	v_pk_fma_f32 v[180:181], v[180:181], v[176:177], v[184:185] op_sel:[1,1,0] op_sel_hi:[0,1,1] neg_hi:[1,0,0]
	v_pk_mul_f32 v[184:185], v[176:177], v[162:163] op_sel_hi:[1,0]
	v_pk_fma_f32 v[176:177], v[176:177], v[162:163], v[184:185] op_sel:[1,1,0] op_sel_hi:[0,1,1] neg_lo:[1,0,0]
	v_pk_mul_f32 v[184:185], v[170:171], v[176:177] op_sel_hi:[1,0]
	v_pk_fma_f32 v[170:171], v[170:171], v[176:177], v[184:185] op_sel:[1,1,0] op_sel_hi:[0,1,1] neg_hi:[1,0,0]
	v_pk_mul_f32 v[184:185], v[176:177], v[162:163] op_sel_hi:[1,0]
	v_pk_fma_f32 v[176:177], v[176:177], v[162:163], v[184:185] op_sel:[1,1,0] op_sel_hi:[0,1,1] neg_lo:[1,0,0]
	v_pk_mul_f32 v[184:185], v[174:175], v[176:177] op_sel_hi:[1,0]
	v_pk_fma_f32 v[174:175], v[174:175], v[176:177], v[184:185] op_sel:[1,1,0] op_sel_hi:[0,1,1] neg_hi:[1,0,0]
	v_pk_mul_f32 v[184:185], v[176:177], v[162:163] op_sel_hi:[1,0]
	v_pk_fma_f32 v[176:177], v[176:177], v[162:163], v[184:185] op_sel:[1,1,0] op_sel_hi:[0,1,1] neg_lo:[1,0,0]
	v_pk_mul_f32 v[184:185], v[166:167], v[176:177] op_sel_hi:[1,0]
	v_pk_fma_f32 v[166:167], v[166:167], v[176:177], v[184:185] op_sel:[1,1,0] op_sel_hi:[0,1,1] neg_hi:[1,0,0]
	ds_write2_b64 v165, v[172:173], v[168:169] offset1:9
	ds_write2_b64 v165, v[182:183], v[178:179] offset0:18 offset1:27
	ds_write2_b64 v165, v[180:181], v[170:171] offset0:36 offset1:45
	ds_write2_b64 v165, v[174:175], v[166:167] offset0:54 offset1:63
	v_add_u32_e32 v165, 0x3000, v38
	v_and_b32_e32 v165, 0xffffffc0, v165
	v_lshlrev_b32_e32 v166, 3, v165
	v_add3_u32 v165, v164, v165, v166
	ds_read2_b64 v[166:169], v165 offset1:9
	ds_read2_b64 v[170:173], v165 offset0:18 offset1:27
	ds_read2_b64 v[174:177], v165 offset0:36 offset1:45
	ds_read2_b64 v[178:181], v165 offset0:54 offset1:63
	s_waitcnt lgkmcnt(9)
	v_pk_add_f32 v[246:247], v[230:231], v[238:239]
	v_pk_add_f32 v[230:231], v[230:231], v[238:239] neg_lo:[0,1] neg_hi:[0,1]
	v_pk_add_f32 v[238:239], v[232:233], v[240:241]
	v_pk_add_f32 v[232:233], v[232:233], v[240:241] neg_lo:[0,1] neg_hi:[0,1]
	v_mov_b64_e32 v[240:241], s[6:7]
	v_pk_mul_f32 v[248:249], v[232:233], v[240:241] op_sel_hi:[1,0]
	v_pk_fma_f32 v[232:233], v[232:233], v[240:241], v[248:249] op_sel:[1,1,0] op_sel_hi:[0,1,1] neg_hi:[1,0,0]
	s_waitcnt lgkmcnt(8)
	v_pk_add_f32 v[240:241], v[234:235], v[242:243]
	v_pk_add_f32 v[234:235], v[234:235], v[242:243] op_sel:[1,1] op_sel_hi:[0,0] neg_lo:[0,1] neg_hi:[1,0]
	v_pk_add_f32 v[242:243], v[236:237], v[244:245]
	v_pk_add_f32 v[236:237], v[236:237], v[244:245] neg_lo:[0,1] neg_hi:[0,1]
	v_mov_b64_e32 v[244:245], s[14:15]
	v_pk_mul_f32 v[248:249], v[236:237], v[244:245] op_sel_hi:[1,0]
	v_pk_fma_f32 v[236:237], v[236:237], v[244:245], v[248:249] op_sel:[1,1,0] op_sel_hi:[0,1,1] neg_hi:[1,0,0]
	v_pk_add_f32 v[244:245], v[246:247], v[240:241]
	v_pk_add_f32 v[240:241], v[246:247], v[240:241] neg_lo:[0,1] neg_hi:[0,1]
	v_pk_add_f32 v[246:247], v[238:239], v[242:243]
	v_pk_add_f32 v[238:239], v[238:239], v[242:243] op_sel:[1,1] op_sel_hi:[0,0] neg_lo:[0,1] neg_hi:[1,0]
	v_pk_add_f32 v[242:243], v[230:231], v[234:235]
	v_pk_add_f32 v[230:231], v[230:231], v[234:235] neg_lo:[0,1] neg_hi:[0,1]
	v_pk_add_f32 v[234:235], v[232:233], v[236:237]
	v_pk_add_f32 v[232:233], v[232:233], v[236:237] op_sel:[1,1] op_sel_hi:[0,0] neg_lo:[0,1] neg_hi:[1,0]
	v_pk_add_f32 v[236:237], v[244:245], v[246:247]
	v_pk_add_f32 v[244:245], v[244:245], v[246:247] neg_lo:[0,1] neg_hi:[0,1]
	v_pk_add_f32 v[246:247], v[240:241], v[238:239]
	v_pk_add_f32 v[238:239], v[240:241], v[238:239] neg_lo:[0,1] neg_hi:[0,1]
	v_pk_add_f32 v[240:241], v[242:243], v[234:235]
	v_pk_add_f32 v[234:235], v[242:243], v[234:235] neg_lo:[0,1] neg_hi:[0,1]
	v_pk_add_f32 v[242:243], v[230:231], v[232:233]
	v_pk_add_f32 v[230:231], v[230:231], v[232:233] neg_lo:[0,1] neg_hi:[0,1]
	v_pk_mul_f32 v[232:233], v[240:241], v[162:163] op_sel_hi:[1,0]
	v_pk_fma_f32 v[232:233], v[240:241], v[162:163], v[232:233] op_sel:[1,1,0] op_sel_hi:[0,1,1] neg_hi:[1,0,0]
	v_pk_mul_f32 v[240:241], v[162:163], v[162:163] op_sel_hi:[1,0]
	v_pk_fma_f32 v[240:241], v[162:163], v[162:163], v[240:241] op_sel:[1,1,0] op_sel_hi:[0,1,1] neg_lo:[1,0,0]
	v_pk_mul_f32 v[248:249], v[246:247], v[240:241] op_sel_hi:[1,0]
	v_pk_fma_f32 v[246:247], v[246:247], v[240:241], v[248:249] op_sel:[1,1,0] op_sel_hi:[0,1,1] neg_hi:[1,0,0]
	v_pk_mul_f32 v[248:249], v[240:241], v[162:163] op_sel_hi:[1,0]
	v_pk_fma_f32 v[240:241], v[240:241], v[162:163], v[248:249] op_sel:[1,1,0] op_sel_hi:[0,1,1] neg_lo:[1,0,0]
	v_pk_mul_f32 v[248:249], v[242:243], v[240:241] op_sel_hi:[1,0]
	v_pk_fma_f32 v[242:243], v[242:243], v[240:241], v[248:249] op_sel:[1,1,0] op_sel_hi:[0,1,1] neg_hi:[1,0,0]
	v_pk_mul_f32 v[248:249], v[240:241], v[162:163] op_sel_hi:[1,0]
	v_pk_fma_f32 v[240:241], v[240:241], v[162:163], v[248:249] op_sel:[1,1,0] op_sel_hi:[0,1,1] neg_lo:[1,0,0]
	v_pk_mul_f32 v[248:249], v[244:245], v[240:241] op_sel_hi:[1,0]
	v_pk_fma_f32 v[244:245], v[244:245], v[240:241], v[248:249] op_sel:[1,1,0] op_sel_hi:[0,1,1] neg_hi:[1,0,0]
	v_pk_mul_f32 v[248:249], v[240:241], v[162:163] op_sel_hi:[1,0]
	v_pk_fma_f32 v[240:241], v[240:241], v[162:163], v[248:249] op_sel:[1,1,0] op_sel_hi:[0,1,1] neg_lo:[1,0,0]
	v_pk_mul_f32 v[248:249], v[234:235], v[240:241] op_sel_hi:[1,0]
	v_pk_fma_f32 v[234:235], v[234:235], v[240:241], v[248:249] op_sel:[1,1,0] op_sel_hi:[0,1,1] neg_hi:[1,0,0]
	v_pk_mul_f32 v[248:249], v[240:241], v[162:163] op_sel_hi:[1,0]
	v_pk_fma_f32 v[240:241], v[240:241], v[162:163], v[248:249] op_sel:[1,1,0] op_sel_hi:[0,1,1] neg_lo:[1,0,0]
	v_pk_mul_f32 v[248:249], v[238:239], v[240:241] op_sel_hi:[1,0]
	v_pk_fma_f32 v[238:239], v[238:239], v[240:241], v[248:249] op_sel:[1,1,0] op_sel_hi:[0,1,1] neg_hi:[1,0,0]
	v_pk_mul_f32 v[248:249], v[240:241], v[162:163] op_sel_hi:[1,0]
	v_pk_fma_f32 v[240:241], v[240:241], v[162:163], v[248:249] op_sel:[1,1,0] op_sel_hi:[0,1,1] neg_lo:[1,0,0]
	v_pk_mul_f32 v[248:249], v[230:231], v[240:241] op_sel_hi:[1,0]
	v_pk_fma_f32 v[230:231], v[230:231], v[240:241], v[248:249] op_sel:[1,1,0] op_sel_hi:[0,1,1] neg_hi:[1,0,0]
	ds_write2_b64 v250, v[236:237], v[232:233] offset1:9
	ds_write2_b64 v250, v[246:247], v[242:243] offset0:18 offset1:27
	ds_write2_b64 v250, v[244:245], v[234:235] offset0:36 offset1:45
	ds_write2_b64 v250, v[238:239], v[230:231] offset0:54 offset1:63
	s_waitcnt lgkmcnt(5)
	v_pk_add_f32 v[182:183], v[166:167], v[174:175]
	v_pk_add_f32 v[166:167], v[166:167], v[174:175] neg_lo:[0,1] neg_hi:[0,1]
	v_pk_add_f32 v[174:175], v[168:169], v[176:177]
	v_pk_add_f32 v[168:169], v[168:169], v[176:177] neg_lo:[0,1] neg_hi:[0,1]
	v_mov_b64_e32 v[176:177], s[6:7]
	v_pk_mul_f32 v[184:185], v[168:169], v[176:177] op_sel_hi:[1,0]
	v_pk_fma_f32 v[168:169], v[168:169], v[176:177], v[184:185] op_sel:[1,1,0] op_sel_hi:[0,1,1] neg_hi:[1,0,0]
	s_waitcnt lgkmcnt(4)
	v_pk_add_f32 v[176:177], v[170:171], v[178:179]
	v_pk_add_f32 v[170:171], v[170:171], v[178:179] op_sel:[1,1] op_sel_hi:[0,0] neg_lo:[0,1] neg_hi:[1,0]
	v_pk_add_f32 v[178:179], v[172:173], v[180:181]
	v_pk_add_f32 v[172:173], v[172:173], v[180:181] neg_lo:[0,1] neg_hi:[0,1]
	v_mov_b64_e32 v[180:181], s[14:15]
	v_pk_mul_f32 v[184:185], v[172:173], v[180:181] op_sel_hi:[1,0]
	v_pk_fma_f32 v[172:173], v[172:173], v[180:181], v[184:185] op_sel:[1,1,0] op_sel_hi:[0,1,1] neg_hi:[1,0,0]
	v_pk_add_f32 v[180:181], v[182:183], v[176:177]
	v_pk_add_f32 v[176:177], v[182:183], v[176:177] neg_lo:[0,1] neg_hi:[0,1]
	v_pk_add_f32 v[182:183], v[174:175], v[178:179]
	v_pk_add_f32 v[174:175], v[174:175], v[178:179] op_sel:[1,1] op_sel_hi:[0,0] neg_lo:[0,1] neg_hi:[1,0]
	v_pk_add_f32 v[178:179], v[166:167], v[170:171]
	v_pk_add_f32 v[166:167], v[166:167], v[170:171] neg_lo:[0,1] neg_hi:[0,1]
	v_pk_add_f32 v[170:171], v[168:169], v[172:173]
	v_pk_add_f32 v[168:169], v[168:169], v[172:173] op_sel:[1,1] op_sel_hi:[0,0] neg_lo:[0,1] neg_hi:[1,0]
	v_pk_add_f32 v[172:173], v[180:181], v[182:183]
	v_pk_add_f32 v[180:181], v[180:181], v[182:183] neg_lo:[0,1] neg_hi:[0,1]
	v_pk_add_f32 v[182:183], v[176:177], v[174:175]
	v_pk_add_f32 v[174:175], v[176:177], v[174:175] neg_lo:[0,1] neg_hi:[0,1]
	v_pk_add_f32 v[176:177], v[178:179], v[170:171]
	v_pk_add_f32 v[170:171], v[178:179], v[170:171] neg_lo:[0,1] neg_hi:[0,1]
	v_pk_add_f32 v[178:179], v[166:167], v[168:169]
	v_pk_add_f32 v[166:167], v[166:167], v[168:169] neg_lo:[0,1] neg_hi:[0,1]
	v_pk_mul_f32 v[168:169], v[176:177], v[162:163] op_sel_hi:[1,0]
	v_pk_fma_f32 v[168:169], v[176:177], v[162:163], v[168:169] op_sel:[1,1,0] op_sel_hi:[0,1,1] neg_hi:[1,0,0]
	v_pk_mul_f32 v[176:177], v[162:163], v[162:163] op_sel_hi:[1,0]
	v_pk_fma_f32 v[176:177], v[162:163], v[162:163], v[176:177] op_sel:[1,1,0] op_sel_hi:[0,1,1] neg_lo:[1,0,0]
	v_pk_mul_f32 v[184:185], v[182:183], v[176:177] op_sel_hi:[1,0]
	v_pk_fma_f32 v[182:183], v[182:183], v[176:177], v[184:185] op_sel:[1,1,0] op_sel_hi:[0,1,1] neg_hi:[1,0,0]
	v_pk_mul_f32 v[184:185], v[176:177], v[162:163] op_sel_hi:[1,0]
	v_pk_fma_f32 v[176:177], v[176:177], v[162:163], v[184:185] op_sel:[1,1,0] op_sel_hi:[0,1,1] neg_lo:[1,0,0]
	v_pk_mul_f32 v[184:185], v[178:179], v[176:177] op_sel_hi:[1,0]
	v_pk_fma_f32 v[178:179], v[178:179], v[176:177], v[184:185] op_sel:[1,1,0] op_sel_hi:[0,1,1] neg_hi:[1,0,0]
	v_pk_mul_f32 v[184:185], v[176:177], v[162:163] op_sel_hi:[1,0]
	v_pk_fma_f32 v[176:177], v[176:177], v[162:163], v[184:185] op_sel:[1,1,0] op_sel_hi:[0,1,1] neg_lo:[1,0,0]
	v_pk_mul_f32 v[184:185], v[180:181], v[176:177] op_sel_hi:[1,0]
	v_pk_fma_f32 v[180:181], v[180:181], v[176:177], v[184:185] op_sel:[1,1,0] op_sel_hi:[0,1,1] neg_hi:[1,0,0]
	v_pk_mul_f32 v[184:185], v[176:177], v[162:163] op_sel_hi:[1,0]
	v_pk_fma_f32 v[176:177], v[176:177], v[162:163], v[184:185] op_sel:[1,1,0] op_sel_hi:[0,1,1] neg_lo:[1,0,0]
	v_pk_mul_f32 v[184:185], v[170:171], v[176:177] op_sel_hi:[1,0]
	v_pk_fma_f32 v[170:171], v[170:171], v[176:177], v[184:185] op_sel:[1,1,0] op_sel_hi:[0,1,1] neg_hi:[1,0,0]
	v_pk_mul_f32 v[184:185], v[176:177], v[162:163] op_sel_hi:[1,0]
	v_pk_fma_f32 v[176:177], v[176:177], v[162:163], v[184:185] op_sel:[1,1,0] op_sel_hi:[0,1,1] neg_lo:[1,0,0]
	v_pk_mul_f32 v[184:185], v[174:175], v[176:177] op_sel_hi:[1,0]
	v_pk_fma_f32 v[174:175], v[174:175], v[176:177], v[184:185] op_sel:[1,1,0] op_sel_hi:[0,1,1] neg_hi:[1,0,0]
	v_pk_mul_f32 v[184:185], v[176:177], v[162:163] op_sel_hi:[1,0]
	v_pk_fma_f32 v[176:177], v[176:177], v[162:163], v[184:185] op_sel:[1,1,0] op_sel_hi:[0,1,1] neg_lo:[1,0,0]
	v_pk_mul_f32 v[184:185], v[166:167], v[176:177] op_sel_hi:[1,0]
	v_pk_fma_f32 v[166:167], v[166:167], v[176:177], v[184:185] op_sel:[1,1,0] op_sel_hi:[0,1,1] neg_hi:[1,0,0]
	ds_write2_b64 v165, v[172:173], v[168:169] offset1:9
	ds_write2_b64 v165, v[182:183], v[178:179] offset0:18 offset1:27
	ds_write2_b64 v165, v[180:181], v[170:171] offset0:36 offset1:45
	ds_write2_b64 v165, v[174:175], v[166:167] offset0:54 offset1:63
	s_mov_b32 s84, 0x4000
	s_cmpk_lg_i32 s84, 0x4000
	v_mov_b32_e32 v38, v204
	s_waitcnt lgkmcnt(0)
	s_barrier
	s_mov_b32 s84, 0
	v_mul_lo_u32 v38, v38, s33
	v_add_u32_e32 v38, 0, v38
.LBB0_768:
	v_add_u32_e32 v250, 0, v38
	ds_read2_b64 v[230:233], v250 offset1:1
	ds_read2_b64 v[234:237], v250 offset0:2 offset1:3
	ds_read2_b64 v[238:241], v250 offset0:4 offset1:5
	ds_read2_b64 v[242:245], v250 offset0:6 offset1:7
	v_add_u32_e32 v182, 0x9000, v38
	ds_read2_b64 v[162:165], v182 offset1:1
	ds_read2_b64 v[166:169], v182 offset0:2 offset1:3
	ds_read2_b64 v[170:173], v182 offset0:4 offset1:5
	ds_read2_b64 v[174:177], v182 offset0:6 offset1:7
	s_waitcnt lgkmcnt(5)
	v_pk_add_f32 v[246:247], v[230:231], v[238:239]
	v_pk_add_f32 v[230:231], v[230:231], v[238:239] neg_lo:[0,1] neg_hi:[0,1]
	v_pk_add_f32 v[238:239], v[232:233], v[240:241]
	v_pk_add_f32 v[232:233], v[232:233], v[240:241] neg_lo:[0,1] neg_hi:[0,1]
	v_mov_b64_e32 v[240:241], s[6:7]
	v_pk_mul_f32 v[248:249], v[232:233], v[240:241] op_sel_hi:[1,0]
	v_pk_fma_f32 v[232:233], v[232:233], v[240:241], v[248:249] op_sel:[1,1,0] op_sel_hi:[0,1,1] neg_hi:[1,0,0]
	s_waitcnt lgkmcnt(4)
	v_pk_add_f32 v[240:241], v[234:235], v[242:243]
	v_pk_add_f32 v[234:235], v[234:235], v[242:243] op_sel:[1,1] op_sel_hi:[0,0] neg_lo:[0,1] neg_hi:[1,0]
	v_pk_add_f32 v[242:243], v[236:237], v[244:245]
	v_pk_add_f32 v[236:237], v[236:237], v[244:245] neg_lo:[0,1] neg_hi:[0,1]
	v_mov_b64_e32 v[244:245], s[14:15]
	v_pk_mul_f32 v[248:249], v[236:237], v[244:245] op_sel_hi:[1,0]
	v_pk_fma_f32 v[236:237], v[236:237], v[244:245], v[248:249] op_sel:[1,1,0] op_sel_hi:[0,1,1] neg_hi:[1,0,0]
	v_pk_add_f32 v[244:245], v[246:247], v[240:241]
	v_pk_add_f32 v[240:241], v[246:247], v[240:241] neg_lo:[0,1] neg_hi:[0,1]
	v_pk_add_f32 v[246:247], v[238:239], v[242:243]
	v_pk_add_f32 v[238:239], v[238:239], v[242:243] op_sel:[1,1] op_sel_hi:[0,0] neg_lo:[0,1] neg_hi:[1,0]
	v_pk_add_f32 v[242:243], v[230:231], v[234:235]
	v_pk_add_f32 v[230:231], v[230:231], v[234:235] neg_lo:[0,1] neg_hi:[0,1]
	v_pk_add_f32 v[234:235], v[232:233], v[236:237]
	v_pk_add_f32 v[232:233], v[232:233], v[236:237] op_sel:[1,1] op_sel_hi:[0,0] neg_lo:[0,1] neg_hi:[1,0]
	v_pk_add_f32 v[236:237], v[244:245], v[246:247]
	v_pk_add_f32 v[244:245], v[244:245], v[246:247] neg_lo:[0,1] neg_hi:[0,1]
	v_pk_add_f32 v[246:247], v[240:241], v[238:239]
	v_pk_add_f32 v[238:239], v[240:241], v[238:239] neg_lo:[0,1] neg_hi:[0,1]
	v_pk_add_f32 v[240:241], v[242:243], v[234:235]
	v_pk_add_f32 v[234:235], v[242:243], v[234:235] neg_lo:[0,1] neg_hi:[0,1]
	v_pk_add_f32 v[242:243], v[230:231], v[232:233]
	v_pk_add_f32 v[230:231], v[230:231], v[232:233] neg_lo:[0,1] neg_hi:[0,1]
	ds_write2_b64 v250, v[236:237], v[240:241] offset1:1
	ds_write2_b64 v250, v[246:247], v[242:243] offset0:2 offset1:3
	ds_write2_b64 v250, v[244:245], v[234:235] offset0:4 offset1:5
	ds_write2_b64 v250, v[238:239], v[230:231] offset0:6 offset1:7
	v_add_u32_e32 v250, 0x12000, v38
	ds_read2_b64 v[230:233], v250 offset1:1
	ds_read2_b64 v[234:237], v250 offset0:2 offset1:3
	ds_read2_b64 v[238:241], v250 offset0:4 offset1:5
	ds_read2_b64 v[242:245], v250 offset0:6 offset1:7
	s_waitcnt lgkmcnt(9)
	v_pk_add_f32 v[178:179], v[162:163], v[170:171]
	v_pk_add_f32 v[162:163], v[162:163], v[170:171] neg_lo:[0,1] neg_hi:[0,1]
	v_pk_add_f32 v[170:171], v[164:165], v[172:173]
	v_pk_add_f32 v[164:165], v[164:165], v[172:173] neg_lo:[0,1] neg_hi:[0,1]
	v_mov_b64_e32 v[172:173], s[6:7]
	v_pk_mul_f32 v[180:181], v[164:165], v[172:173] op_sel_hi:[1,0]
	v_pk_fma_f32 v[164:165], v[164:165], v[172:173], v[180:181] op_sel:[1,1,0] op_sel_hi:[0,1,1] neg_hi:[1,0,0]
	s_waitcnt lgkmcnt(8)
	v_pk_add_f32 v[172:173], v[166:167], v[174:175]
	v_pk_add_f32 v[166:167], v[166:167], v[174:175] op_sel:[1,1] op_sel_hi:[0,0] neg_lo:[0,1] neg_hi:[1,0]
	v_pk_add_f32 v[174:175], v[168:169], v[176:177]
	v_pk_add_f32 v[168:169], v[168:169], v[176:177] neg_lo:[0,1] neg_hi:[0,1]
	v_mov_b64_e32 v[176:177], s[14:15]
	v_pk_mul_f32 v[180:181], v[168:169], v[176:177] op_sel_hi:[1,0]
	v_pk_fma_f32 v[168:169], v[168:169], v[176:177], v[180:181] op_sel:[1,1,0] op_sel_hi:[0,1,1] neg_hi:[1,0,0]
	v_pk_add_f32 v[176:177], v[178:179], v[172:173]
	v_pk_add_f32 v[172:173], v[178:179], v[172:173] neg_lo:[0,1] neg_hi:[0,1]
	v_pk_add_f32 v[178:179], v[170:171], v[174:175]
	v_pk_add_f32 v[170:171], v[170:171], v[174:175] op_sel:[1,1] op_sel_hi:[0,0] neg_lo:[0,1] neg_hi:[1,0]
	v_pk_add_f32 v[174:175], v[162:163], v[166:167]
	v_pk_add_f32 v[162:163], v[162:163], v[166:167] neg_lo:[0,1] neg_hi:[0,1]
	v_pk_add_f32 v[166:167], v[164:165], v[168:169]
	v_pk_add_f32 v[164:165], v[164:165], v[168:169] op_sel:[1,1] op_sel_hi:[0,0] neg_lo:[0,1] neg_hi:[1,0]
	v_pk_add_f32 v[168:169], v[176:177], v[178:179]
	v_pk_add_f32 v[176:177], v[176:177], v[178:179] neg_lo:[0,1] neg_hi:[0,1]
	v_pk_add_f32 v[178:179], v[172:173], v[170:171]
	v_pk_add_f32 v[170:171], v[172:173], v[170:171] neg_lo:[0,1] neg_hi:[0,1]
	v_pk_add_f32 v[172:173], v[174:175], v[166:167]
	v_pk_add_f32 v[166:167], v[174:175], v[166:167] neg_lo:[0,1] neg_hi:[0,1]
	v_pk_add_f32 v[174:175], v[162:163], v[164:165]
	v_pk_add_f32 v[162:163], v[162:163], v[164:165] neg_lo:[0,1] neg_hi:[0,1]
	ds_write2_b64 v182, v[168:169], v[172:173] offset1:1
	ds_write2_b64 v182, v[178:179], v[174:175] offset0:2 offset1:3
	ds_write2_b64 v182, v[176:177], v[166:167] offset0:4 offset1:5
	ds_write2_b64 v182, v[170:171], v[162:163] offset0:6 offset1:7
	v_add_u32_e32 v182, 0x1b000, v38
	ds_read2_b64 v[162:165], v182 offset1:1
	ds_read2_b64 v[166:169], v182 offset0:2 offset1:3
	ds_read2_b64 v[170:173], v182 offset0:4 offset1:5
	ds_read2_b64 v[174:177], v182 offset0:6 offset1:7
	s_waitcnt lgkmcnt(9)
	v_pk_add_f32 v[246:247], v[230:231], v[238:239]
	v_pk_add_f32 v[230:231], v[230:231], v[238:239] neg_lo:[0,1] neg_hi:[0,1]
	v_pk_add_f32 v[238:239], v[232:233], v[240:241]
	v_pk_add_f32 v[232:233], v[232:233], v[240:241] neg_lo:[0,1] neg_hi:[0,1]
	v_mov_b64_e32 v[240:241], s[6:7]
	v_pk_mul_f32 v[248:249], v[232:233], v[240:241] op_sel_hi:[1,0]
	v_pk_fma_f32 v[232:233], v[232:233], v[240:241], v[248:249] op_sel:[1,1,0] op_sel_hi:[0,1,1] neg_hi:[1,0,0]
	s_waitcnt lgkmcnt(8)
	v_pk_add_f32 v[240:241], v[234:235], v[242:243]
	v_pk_add_f32 v[234:235], v[234:235], v[242:243] op_sel:[1,1] op_sel_hi:[0,0] neg_lo:[0,1] neg_hi:[1,0]
	v_pk_add_f32 v[242:243], v[236:237], v[244:245]
	v_pk_add_f32 v[236:237], v[236:237], v[244:245] neg_lo:[0,1] neg_hi:[0,1]
	v_mov_b64_e32 v[244:245], s[14:15]
	v_pk_mul_f32 v[248:249], v[236:237], v[244:245] op_sel_hi:[1,0]
	v_pk_fma_f32 v[236:237], v[236:237], v[244:245], v[248:249] op_sel:[1,1,0] op_sel_hi:[0,1,1] neg_hi:[1,0,0]
	v_pk_add_f32 v[244:245], v[246:247], v[240:241]
	v_pk_add_f32 v[240:241], v[246:247], v[240:241] neg_lo:[0,1] neg_hi:[0,1]
	v_pk_add_f32 v[246:247], v[238:239], v[242:243]
	v_pk_add_f32 v[238:239], v[238:239], v[242:243] op_sel:[1,1] op_sel_hi:[0,0] neg_lo:[0,1] neg_hi:[1,0]
	v_pk_add_f32 v[242:243], v[230:231], v[234:235]
	v_pk_add_f32 v[230:231], v[230:231], v[234:235] neg_lo:[0,1] neg_hi:[0,1]
	v_pk_add_f32 v[234:235], v[232:233], v[236:237]
	v_pk_add_f32 v[232:233], v[232:233], v[236:237] op_sel:[1,1] op_sel_hi:[0,0] neg_lo:[0,1] neg_hi:[1,0]
	v_pk_add_f32 v[236:237], v[244:245], v[246:247]
	v_pk_add_f32 v[244:245], v[244:245], v[246:247] neg_lo:[0,1] neg_hi:[0,1]
	v_pk_add_f32 v[246:247], v[240:241], v[238:239]
	v_pk_add_f32 v[238:239], v[240:241], v[238:239] neg_lo:[0,1] neg_hi:[0,1]
	v_pk_add_f32 v[240:241], v[242:243], v[234:235]
	v_pk_add_f32 v[234:235], v[242:243], v[234:235] neg_lo:[0,1] neg_hi:[0,1]
	v_pk_add_f32 v[242:243], v[230:231], v[232:233]
	v_pk_add_f32 v[230:231], v[230:231], v[232:233] neg_lo:[0,1] neg_hi:[0,1]
	ds_write2_b64 v250, v[236:237], v[240:241] offset1:1
	ds_write2_b64 v250, v[246:247], v[242:243] offset0:2 offset1:3
	ds_write2_b64 v250, v[244:245], v[234:235] offset0:4 offset1:5
	ds_write2_b64 v250, v[238:239], v[230:231] offset0:6 offset1:7
	s_waitcnt lgkmcnt(5)
	v_pk_add_f32 v[178:179], v[162:163], v[170:171]
	v_pk_add_f32 v[162:163], v[162:163], v[170:171] neg_lo:[0,1] neg_hi:[0,1]
	v_pk_add_f32 v[170:171], v[164:165], v[172:173]
	v_pk_add_f32 v[164:165], v[164:165], v[172:173] neg_lo:[0,1] neg_hi:[0,1]
	v_mov_b64_e32 v[172:173], s[6:7]
	v_pk_mul_f32 v[180:181], v[164:165], v[172:173] op_sel_hi:[1,0]
	v_pk_fma_f32 v[164:165], v[164:165], v[172:173], v[180:181] op_sel:[1,1,0] op_sel_hi:[0,1,1] neg_hi:[1,0,0]
	s_waitcnt lgkmcnt(4)
	v_pk_add_f32 v[172:173], v[166:167], v[174:175]
	v_pk_add_f32 v[166:167], v[166:167], v[174:175] op_sel:[1,1] op_sel_hi:[0,0] neg_lo:[0,1] neg_hi:[1,0]
	v_pk_add_f32 v[174:175], v[168:169], v[176:177]
	v_pk_add_f32 v[168:169], v[168:169], v[176:177] neg_lo:[0,1] neg_hi:[0,1]
	v_mov_b64_e32 v[176:177], s[14:15]
	v_pk_mul_f32 v[180:181], v[168:169], v[176:177] op_sel_hi:[1,0]
	v_pk_fma_f32 v[168:169], v[168:169], v[176:177], v[180:181] op_sel:[1,1,0] op_sel_hi:[0,1,1] neg_hi:[1,0,0]
	v_pk_add_f32 v[176:177], v[178:179], v[172:173]
	v_pk_add_f32 v[172:173], v[178:179], v[172:173] neg_lo:[0,1] neg_hi:[0,1]
	v_pk_add_f32 v[178:179], v[170:171], v[174:175]
	v_pk_add_f32 v[170:171], v[170:171], v[174:175] op_sel:[1,1] op_sel_hi:[0,0] neg_lo:[0,1] neg_hi:[1,0]
	v_pk_add_f32 v[174:175], v[162:163], v[166:167]
	v_pk_add_f32 v[162:163], v[162:163], v[166:167] neg_lo:[0,1] neg_hi:[0,1]
	v_pk_add_f32 v[166:167], v[164:165], v[168:169]
	v_pk_add_f32 v[164:165], v[164:165], v[168:169] op_sel:[1,1] op_sel_hi:[0,0] neg_lo:[0,1] neg_hi:[1,0]
	v_pk_add_f32 v[168:169], v[176:177], v[178:179]
	v_pk_add_f32 v[176:177], v[176:177], v[178:179] neg_lo:[0,1] neg_hi:[0,1]
	v_pk_add_f32 v[178:179], v[172:173], v[170:171]
	v_pk_add_f32 v[170:171], v[172:173], v[170:171] neg_lo:[0,1] neg_hi:[0,1]
	v_pk_add_f32 v[172:173], v[174:175], v[166:167]
	v_pk_add_f32 v[166:167], v[174:175], v[166:167] neg_lo:[0,1] neg_hi:[0,1]
	v_pk_add_f32 v[174:175], v[162:163], v[164:165]
	v_pk_add_f32 v[162:163], v[162:163], v[164:165] neg_lo:[0,1] neg_hi:[0,1]
	ds_write2_b64 v182, v[168:169], v[172:173] offset1:1
	ds_write2_b64 v182, v[178:179], v[174:175] offset0:2 offset1:3
	ds_write2_b64 v182, v[176:177], v[166:167] offset0:4 offset1:5
	ds_write2_b64 v182, v[170:171], v[162:163] offset0:6 offset1:7
	s_mov_b32 s84, 0x24000
	s_cmp_lg_u32 s84, 0x24000
	s_waitcnt lgkmcnt(0)
	s_barrier
	s_nop 0
	v_cvt_f32_i32_e32 v38, v209
	v_lshlrev_b32_e32 v165, 2, v209
	v_lshrrev_b32_e32 v166, 5, v209
	v_ashrrev_i32_e32 v167, 11, v209
	v_mul_f32_e32 v38, 0x38800000, v38
	v_cos_f32_e32 v163, v38
	v_sin_f32_e32 v162, v38
	v_lshlrev_b32_e32 v38, 10, v209
	v_sub_u32_e32 v164, 0, v209
	v_and_b32_e32 v38, 0x3c00, v38
	v_and_b32_e32 v166, 56, v166
	v_and_or_b32 v165, v165, s9, v167
	v_or3_b32 v38, v165, v38, v166
	v_lshlrev_b32_e32 v165, 10, v164
	v_lshlrev_b32_e32 v166, 2, v164
	v_lshrrev_b32_e32 v167, 5, v164
	v_bfe_u32 v164, v164, 11, 3
	v_and_b32_e32 v165, 0x3c00, v165
	v_and_b32_e32 v166, 0x3c0, v166
	v_and_or_b32 v164, v167, 56, v164
	v_mul_i32_i24_e32 v38, 9, v38
	v_or3_b32 v164, v164, v166, v165
	v_and_b32_e32 v38, -8, v38
	v_mul_u32_u24_e32 v164, 9, v164
	v_add_u32_e32 v38, 0, v38
	v_and_b32_e32 v164, 0x3fff8, v164
	v_add_u32_e32 v176, 0, v164
	ds_read_b64 v[164:165], v38
	ds_read_b64 v[166:167], v176
	v_pk_fma_f32 v[168:169], v[162:163], 0, v[162:163] op_sel:[0,0,1] op_sel_hi:[1,0,0] neg_lo:[1,0,0] neg_hi:[1,0,0]
	v_pk_fma_f32 v[170:171], v[162:163], 0, v[162:163] op_sel:[0,0,1] op_sel_hi:[1,0,0]
	s_nop 0
	v_mov_b32_e32 v169, v171
	s_waitcnt lgkmcnt(0)
	v_pk_add_f32 v[170:171], v[164:165], v[166:167] neg_hi:[0,1]
	v_pk_add_f32 v[164:165], v[164:165], v[166:167] op_sel:[1,1] op_sel_hi:[0,0] neg_hi:[1,0]
	v_pk_add_f32 v[166:167], v[158:159], v[160:161] neg_hi:[0,1]
	v_pk_add_f32 v[158:159], v[158:159], v[160:161] op_sel:[1,1] op_sel_hi:[0,0] neg_hi:[1,0]
	v_pk_mul_f32 v[160:161], v[170:171], v[166:167] op_sel_hi:[1,0]
	v_pk_mul_f32 v[172:173], v[164:165], v[158:159] op_sel_hi:[1,0]
	v_pk_fma_f32 v[160:161], v[170:171], v[166:167], v[160:161] op_sel:[1,1,0] op_sel_hi:[0,1,1] neg_lo:[1,0,0]
	v_pk_fma_f32 v[172:173], v[164:165], v[158:159], v[172:173] op_sel:[1,1,0] op_sel_hi:[0,1,1] neg_lo:[1,0,0]
	v_pk_mul_f32 v[174:175], v[172:173], v[168:169] op_sel_hi:[1,0]
	v_pk_fma_f32 v[168:169], v[172:173], v[168:169], v[174:175] op_sel:[1,1,0] op_sel_hi:[0,1,1] neg_hi:[1,0,0]
	v_pk_add_f32 v[160:161], v[160:161], v[168:169]
	v_pk_mul_f32 v[168:169], v[170:171], v[158:159] op_sel_hi:[1,0]
	v_pk_fma_f32 v[158:159], v[170:171], v[158:159], v[168:169] op_sel:[1,1,0] op_sel_hi:[0,1,1] neg_lo:[1,0,0]
	v_pk_mul_f32 v[168:169], v[164:165], v[166:167] op_sel_hi:[1,0]
	v_pk_fma_f32 v[164:165], v[164:165], v[166:167], v[168:169] op_sel:[1,1,0] op_sel_hi:[0,1,1] neg_lo:[1,0,0]
	v_pk_add_f32 v[158:159], v[158:159], v[164:165]
	s_nop 0
	v_pk_add_f32 v[164:165], v[160:161], v[158:159] op_sel:[0,1] op_sel_hi:[1,0] neg_lo:[0,1]
	v_pk_add_f32 v[158:159], v[160:161], v[158:159] op_sel:[0,1] op_sel_hi:[1,0] neg_hi:[1,0]
	ds_write_b64 v38, v[164:165]
	ds_write_b64 v176, v[158:159]
	v_add_u32_e32 v158, 1, v209
	v_lshlrev_b32_e32 v164, 10, v158
	v_lshlrev_b32_e32 v165, 2, v158
	v_lshrrev_b32_e32 v166, 5, v158
	v_ashrrev_i32_e32 v158, 11, v158
	v_and_b32_e32 v164, 0x3c00, v164
	v_and_b32_e32 v166, 56, v166
	v_and_or_b32 v158, v165, s9, v158
	v_or3_b32 v158, v158, v164, v166
	v_mul_i32_i24_e32 v158, 9, v158
	v_not_b32_e32 v159, v209
	v_and_b32_e32 v158, -8, v158
	v_add_u32_e32 v174, 0, v158
	v_lshlrev_b32_e32 v158, 10, v159
	v_lshlrev_b32_e32 v164, 2, v159
	v_lshrrev_b32_e32 v165, 5, v159
	v_bfe_u32 v159, v159, 11, 3
	v_and_b32_e32 v158, 0x3c00, v158
	v_and_b32_e32 v164, 0x3c0, v164
	v_and_or_b32 v159, v165, 56, v159
	v_or3_b32 v158, v159, v164, v158
	v_mul_u32_u24_e32 v158, 9, v158
	v_and_b32_e32 v158, 0x3fff8, v158
	v_add_u32_e32 v159, 0, v158
	ds_read_b64 v[164:165], v159
	ds_read_b64 v[166:167], v174
	v_pk_mul_f32 v[160:161], v[162:163], s[20:21] op_sel_hi:[0,1]
	v_mov_b32_e32 v38, v163
	v_mov_b32_e32 v158, v163
	v_pk_fma_f32 v[168:169], v[38:39], s[22:23], v[160:161] neg_lo:[0,0,1] neg_hi:[0,0,1]
	v_pk_fma_f32 v[160:161], v[158:159], s[22:23], v[160:161] op_sel_hi:[0,1,1]
	v_mov_b32_e32 v169, v161
	s_waitcnt lgkmcnt(0)
	v_pk_add_f32 v[160:161], v[166:167], v[164:165] neg_hi:[0,1]
	v_pk_add_f32 v[164:165], v[166:167], v[164:165] op_sel:[1,1] op_sel_hi:[0,0] neg_hi:[1,0]
	v_pk_add_f32 v[166:167], v[154:155], v[156:157] neg_hi:[0,1]
	v_pk_add_f32 v[154:155], v[154:155], v[156:157] op_sel:[1,1] op_sel_hi:[0,0] neg_hi:[1,0]
	v_pk_mul_f32 v[156:157], v[160:161], v[166:167] op_sel_hi:[1,0]
	v_pk_mul_f32 v[170:171], v[164:165], v[154:155] op_sel_hi:[1,0]
	v_pk_fma_f32 v[156:157], v[160:161], v[166:167], v[156:157] op_sel:[1,1,0] op_sel_hi:[0,1,1] neg_lo:[1,0,0]
	v_pk_fma_f32 v[170:171], v[164:165], v[154:155], v[170:171] op_sel:[1,1,0] op_sel_hi:[0,1,1] neg_lo:[1,0,0]
	v_pk_mul_f32 v[172:173], v[170:171], v[168:169] op_sel_hi:[1,0]
	v_pk_fma_f32 v[168:169], v[170:171], v[168:169], v[172:173] op_sel:[1,1,0] op_sel_hi:[0,1,1] neg_hi:[1,0,0]
	v_pk_add_f32 v[156:157], v[156:157], v[168:169]
	v_pk_mul_f32 v[168:169], v[160:161], v[154:155] op_sel_hi:[1,0]
	v_pk_fma_f32 v[154:155], v[160:161], v[154:155], v[168:169] op_sel:[1,1,0] op_sel_hi:[0,1,1] neg_lo:[1,0,0]
	v_pk_mul_f32 v[160:161], v[164:165], v[166:167] op_sel_hi:[1,0]
	v_pk_fma_f32 v[160:161], v[164:165], v[166:167], v[160:161] op_sel:[1,1,0] op_sel_hi:[0,1,1] neg_lo:[1,0,0]
	v_pk_add_f32 v[154:155], v[154:155], v[160:161]
	s_nop 0
	v_pk_add_f32 v[160:161], v[156:157], v[154:155] op_sel:[0,1] op_sel_hi:[1,0] neg_lo:[0,1]
	v_pk_add_f32 v[154:155], v[156:157], v[154:155] op_sel:[0,1] op_sel_hi:[1,0] neg_hi:[1,0]
	ds_write_b64 v174, v[160:161]
	ds_write_b64 v159, v[154:155]
	v_add_u32_e32 v154, 2, v209
	v_lshlrev_b32_e32 v156, 10, v154
	v_lshlrev_b32_e32 v157, 2, v154
	v_lshrrev_b32_e32 v159, 5, v154
	v_ashrrev_i32_e32 v154, 11, v154
	v_and_b32_e32 v156, 0x3c00, v156
	v_and_b32_e32 v159, 56, v159
	v_and_or_b32 v154, v157, s9, v154
	v_or3_b32 v154, v154, v156, v159
	v_mul_i32_i24_e32 v154, 9, v154
	v_sub_u32_e32 v155, -2, v209
	v_and_b32_e32 v154, -8, v154
	v_add_u32_e32 v159, 0, v154
	v_lshlrev_b32_e32 v154, 10, v155
	v_lshlrev_b32_e32 v156, 2, v155
	v_lshrrev_b32_e32 v157, 5, v155
	v_bfe_u32 v155, v155, 11, 3
	v_and_b32_e32 v154, 0x3c00, v154
	v_and_b32_e32 v156, 0x3c0, v156
	v_and_or_b32 v155, v157, 56, v155
	v_or3_b32 v154, v155, v156, v154
	v_mul_u32_u24_e32 v154, 9, v154
	v_and_b32_e32 v154, 0x3fff8, v154
	v_add_u32_e32 v163, 0, v154
	ds_read_b64 v[154:155], v159
	ds_read_b64 v[156:157], v163
	v_pk_mul_f32 v[160:161], v[162:163], s[24:25] op_sel_hi:[0,1]
	v_pk_fma_f32 v[164:165], v[38:39], s[26:27], v[160:161] neg_lo:[0,0,1] neg_hi:[0,0,1]
	v_pk_fma_f32 v[160:161], v[158:159], s[26:27], v[160:161] op_sel_hi:[0,1,1]
	v_mov_b32_e32 v165, v161
	s_waitcnt lgkmcnt(0)
	v_pk_add_f32 v[160:161], v[154:155], v[156:157] neg_hi:[0,1]
	v_pk_add_f32 v[154:155], v[154:155], v[156:157] op_sel:[1,1] op_sel_hi:[0,0] neg_hi:[1,0]
	v_pk_add_f32 v[156:157], v[150:151], v[152:153] neg_hi:[0,1]
	v_pk_add_f32 v[150:151], v[150:151], v[152:153] op_sel:[1,1] op_sel_hi:[0,0] neg_hi:[1,0]
	v_pk_mul_f32 v[152:153], v[160:161], v[156:157] op_sel_hi:[1,0]
	v_pk_mul_f32 v[166:167], v[154:155], v[150:151] op_sel_hi:[1,0]
	v_pk_fma_f32 v[152:153], v[160:161], v[156:157], v[152:153] op_sel:[1,1,0] op_sel_hi:[0,1,1] neg_lo:[1,0,0]
	v_pk_fma_f32 v[166:167], v[154:155], v[150:151], v[166:167] op_sel:[1,1,0] op_sel_hi:[0,1,1] neg_lo:[1,0,0]
	v_pk_mul_f32 v[168:169], v[166:167], v[164:165] op_sel_hi:[1,0]
	v_pk_fma_f32 v[164:165], v[166:167], v[164:165], v[168:169] op_sel:[1,1,0] op_sel_hi:[0,1,1] neg_hi:[1,0,0]
	v_pk_add_f32 v[152:153], v[152:153], v[164:165]
	v_pk_mul_f32 v[164:165], v[160:161], v[150:151] op_sel_hi:[1,0]
	v_pk_fma_f32 v[150:151], v[160:161], v[150:151], v[164:165] op_sel:[1,1,0] op_sel_hi:[0,1,1] neg_lo:[1,0,0]
	v_pk_mul_f32 v[160:161], v[154:155], v[156:157] op_sel_hi:[1,0]
	v_pk_fma_f32 v[154:155], v[154:155], v[156:157], v[160:161] op_sel:[1,1,0] op_sel_hi:[0,1,1] neg_lo:[1,0,0]
	v_pk_add_f32 v[150:151], v[150:151], v[154:155]
	s_nop 0
	v_pk_add_f32 v[154:155], v[152:153], v[150:151] op_sel:[0,1] op_sel_hi:[1,0] neg_lo:[0,1]
	v_pk_add_f32 v[150:151], v[152:153], v[150:151] op_sel:[0,1] op_sel_hi:[1,0] neg_hi:[1,0]
	ds_write_b64 v159, v[154:155]
	ds_write_b64 v163, v[150:151]
	v_add_u32_e32 v150, 3, v209
	v_lshlrev_b32_e32 v152, 10, v150
	v_lshlrev_b32_e32 v153, 2, v150
	v_lshrrev_b32_e32 v154, 5, v150
	v_ashrrev_i32_e32 v150, 11, v150
	v_and_b32_e32 v152, 0x3c00, v152
	v_and_b32_e32 v154, 56, v154
	v_and_or_b32 v150, v153, s9, v150
	v_or3_b32 v150, v150, v152, v154
	v_mul_i32_i24_e32 v150, 9, v150
	v_sub_u32_e32 v151, -3, v209
	v_and_b32_e32 v150, -8, v150
	v_add_u32_e32 v159, 0, v150
	v_lshlrev_b32_e32 v150, 10, v151
	v_lshlrev_b32_e32 v152, 2, v151
	v_lshrrev_b32_e32 v153, 5, v151
	v_bfe_u32 v151, v151, 11, 3
	v_and_b32_e32 v150, 0x3c00, v150
	v_and_b32_e32 v152, 0x3c0, v152
	v_and_or_b32 v151, v153, 56, v151
	v_or3_b32 v150, v151, v152, v150
	v_mul_u32_u24_e32 v150, 9, v150
	v_and_b32_e32 v150, 0x3fff8, v150
	v_add_u32_e32 v163, 0, v150
	ds_read_b64 v[150:151], v159
	ds_read_b64 v[152:153], v163
	v_pk_mul_f32 v[154:155], v[162:163], s[28:29] op_sel_hi:[0,1]
	v_pk_fma_f32 v[156:157], v[38:39], s[30:31], v[154:155] neg_lo:[0,0,1] neg_hi:[0,0,1]
	v_pk_fma_f32 v[154:155], v[158:159], s[30:31], v[154:155] op_sel_hi:[0,1,1]
	v_mov_b32_e32 v157, v155
	s_waitcnt lgkmcnt(0)
	v_pk_add_f32 v[154:155], v[150:151], v[152:153] neg_hi:[0,1]
	v_pk_add_f32 v[150:151], v[150:151], v[152:153] op_sel:[1,1] op_sel_hi:[0,0] neg_hi:[1,0]
	v_pk_add_f32 v[152:153], v[146:147], v[148:149] neg_hi:[0,1]
	v_pk_add_f32 v[146:147], v[146:147], v[148:149] op_sel:[1,1] op_sel_hi:[0,0] neg_hi:[1,0]
	v_pk_mul_f32 v[148:149], v[154:155], v[152:153] op_sel_hi:[1,0]
	v_pk_mul_f32 v[160:161], v[150:151], v[146:147] op_sel_hi:[1,0]
	v_pk_fma_f32 v[148:149], v[154:155], v[152:153], v[148:149] op_sel:[1,1,0] op_sel_hi:[0,1,1] neg_lo:[1,0,0]
	v_pk_fma_f32 v[160:161], v[150:151], v[146:147], v[160:161] op_sel:[1,1,0] op_sel_hi:[0,1,1] neg_lo:[1,0,0]
	v_pk_mul_f32 v[164:165], v[160:161], v[156:157] op_sel_hi:[1,0]
	v_pk_fma_f32 v[156:157], v[160:161], v[156:157], v[164:165] op_sel:[1,1,0] op_sel_hi:[0,1,1] neg_hi:[1,0,0]
	v_pk_add_f32 v[148:149], v[148:149], v[156:157]
	v_pk_mul_f32 v[156:157], v[154:155], v[146:147] op_sel_hi:[1,0]
	v_pk_fma_f32 v[146:147], v[154:155], v[146:147], v[156:157] op_sel:[1,1,0] op_sel_hi:[0,1,1] neg_lo:[1,0,0]
	v_pk_mul_f32 v[154:155], v[150:151], v[152:153] op_sel_hi:[1,0]
	v_pk_fma_f32 v[150:151], v[150:151], v[152:153], v[154:155] op_sel:[1,1,0] op_sel_hi:[0,1,1] neg_lo:[1,0,0]
	v_pk_add_f32 v[146:147], v[146:147], v[150:151]
	s_nop 0
	v_pk_add_f32 v[150:151], v[148:149], v[146:147] op_sel:[0,1] op_sel_hi:[1,0] neg_lo:[0,1]
	v_pk_add_f32 v[146:147], v[148:149], v[146:147] op_sel:[0,1] op_sel_hi:[1,0] neg_hi:[1,0]
	ds_write_b64 v159, v[150:151]
	ds_write_b64 v163, v[146:147]
	v_add_u32_e32 v146, 4, v209
	v_lshlrev_b32_e32 v148, 10, v146
	v_lshlrev_b32_e32 v149, 2, v146
	v_lshrrev_b32_e32 v150, 5, v146
	v_ashrrev_i32_e32 v146, 11, v146
	v_and_b32_e32 v148, 0x3c00, v148
	v_and_b32_e32 v150, 56, v150
	v_and_or_b32 v146, v149, s9, v146
	v_or3_b32 v146, v146, v148, v150
	v_mul_i32_i24_e32 v146, 9, v146
	v_sub_u32_e32 v147, -4, v209
	v_and_b32_e32 v146, -8, v146
	v_add_u32_e32 v159, 0, v146
	v_lshlrev_b32_e32 v146, 10, v147
	v_lshlrev_b32_e32 v148, 2, v147
	v_lshrrev_b32_e32 v149, 5, v147
	v_bfe_u32 v147, v147, 11, 3
	v_and_b32_e32 v146, 0x3c00, v146
	v_and_b32_e32 v148, 0x3c0, v148
	v_and_or_b32 v147, v149, 56, v147
	v_or3_b32 v146, v147, v148, v146
	v_mul_u32_u24_e32 v146, 9, v146
	v_and_b32_e32 v146, 0x3fff8, v146
	v_add_u32_e32 v160, 0, v146
	ds_read_b64 v[146:147], v159
	ds_read_b64 v[148:149], v160
	v_pk_mul_f32 v[150:151], v[162:163], s[34:35] op_sel_hi:[0,1]
	v_pk_fma_f32 v[152:153], v[38:39], s[36:37], v[150:151] neg_lo:[0,0,1] neg_hi:[0,0,1]
	v_pk_fma_f32 v[150:151], v[158:159], s[36:37], v[150:151] op_sel_hi:[0,1,1]
	v_mov_b32_e32 v153, v151
	s_waitcnt lgkmcnt(0)
	v_pk_add_f32 v[150:151], v[146:147], v[148:149] neg_hi:[0,1]
	v_pk_add_f32 v[146:147], v[146:147], v[148:149] op_sel:[1,1] op_sel_hi:[0,0] neg_hi:[1,0]
	v_pk_add_f32 v[148:149], v[142:143], v[144:145] neg_hi:[0,1]
	v_pk_add_f32 v[142:143], v[142:143], v[144:145] op_sel:[1,1] op_sel_hi:[0,0] neg_hi:[1,0]
	v_pk_mul_f32 v[144:145], v[150:151], v[148:149] op_sel_hi:[1,0]
	v_pk_mul_f32 v[154:155], v[146:147], v[142:143] op_sel_hi:[1,0]
	v_pk_fma_f32 v[144:145], v[150:151], v[148:149], v[144:145] op_sel:[1,1,0] op_sel_hi:[0,1,1] neg_lo:[1,0,0]
	v_pk_fma_f32 v[154:155], v[146:147], v[142:143], v[154:155] op_sel:[1,1,0] op_sel_hi:[0,1,1] neg_lo:[1,0,0]
	v_pk_mul_f32 v[156:157], v[154:155], v[152:153] op_sel_hi:[1,0]
	v_pk_fma_f32 v[152:153], v[154:155], v[152:153], v[156:157] op_sel:[1,1,0] op_sel_hi:[0,1,1] neg_hi:[1,0,0]
	v_pk_add_f32 v[144:145], v[144:145], v[152:153]
	v_pk_mul_f32 v[152:153], v[150:151], v[142:143] op_sel_hi:[1,0]
	v_pk_fma_f32 v[142:143], v[150:151], v[142:143], v[152:153] op_sel:[1,1,0] op_sel_hi:[0,1,1] neg_lo:[1,0,0]
	v_pk_mul_f32 v[150:151], v[146:147], v[148:149] op_sel_hi:[1,0]
	v_pk_fma_f32 v[146:147], v[146:147], v[148:149], v[150:151] op_sel:[1,1,0] op_sel_hi:[0,1,1] neg_lo:[1,0,0]
	v_pk_add_f32 v[142:143], v[142:143], v[146:147]
	s_nop 0
	v_pk_add_f32 v[146:147], v[144:145], v[142:143] op_sel:[0,1] op_sel_hi:[1,0] neg_lo:[0,1]
	v_pk_add_f32 v[142:143], v[144:145], v[142:143] op_sel:[0,1] op_sel_hi:[1,0] neg_hi:[1,0]
	ds_write_b64 v159, v[146:147]
	ds_write_b64 v160, v[142:143]
	v_add_u32_e32 v142, 5, v209
	v_lshlrev_b32_e32 v144, 10, v142
	v_lshlrev_b32_e32 v145, 2, v142
	v_lshrrev_b32_e32 v146, 5, v142
	v_ashrrev_i32_e32 v142, 11, v142
	v_and_b32_e32 v144, 0x3c00, v144
	v_and_b32_e32 v146, 56, v146
	v_and_or_b32 v142, v145, s9, v142
	v_or3_b32 v142, v142, v144, v146
	v_mul_i32_i24_e32 v142, 9, v142
	v_sub_u32_e32 v143, -5, v209
	v_and_b32_e32 v142, -8, v142
	v_add_u32_e32 v154, 0, v142
	v_lshlrev_b32_e32 v142, 10, v143
	v_lshlrev_b32_e32 v144, 2, v143
	v_lshrrev_b32_e32 v145, 5, v143
	v_bfe_u32 v143, v143, 11, 3
	v_and_b32_e32 v142, 0x3c00, v142
	v_and_b32_e32 v144, 0x3c0, v144
	v_and_or_b32 v143, v145, 56, v143
	v_or3_b32 v142, v143, v144, v142
	v_mul_u32_u24_e32 v142, 9, v142
	v_and_b32_e32 v142, 0x3fff8, v142
	v_add_u32_e32 v155, 0, v142
	ds_read_b64 v[142:143], v154
	ds_read_b64 v[144:145], v155
	v_pk_mul_f32 v[146:147], v[162:163], s[38:39] op_sel_hi:[0,1]
	v_pk_fma_f32 v[148:149], v[38:39], s[40:41], v[146:147] neg_lo:[0,0,1] neg_hi:[0,0,1]
	v_pk_fma_f32 v[146:147], v[158:159], s[40:41], v[146:147] op_sel_hi:[0,1,1]
	v_mov_b32_e32 v149, v147
	s_waitcnt lgkmcnt(0)
	v_pk_add_f32 v[146:147], v[142:143], v[144:145] neg_hi:[0,1]
	v_pk_add_f32 v[142:143], v[142:143], v[144:145] op_sel:[1,1] op_sel_hi:[0,0] neg_hi:[1,0]
	v_pk_add_f32 v[144:145], v[138:139], v[140:141] neg_hi:[0,1]
	v_pk_add_f32 v[138:139], v[138:139], v[140:141] op_sel:[1,1] op_sel_hi:[0,0] neg_hi:[1,0]
	v_pk_mul_f32 v[140:141], v[146:147], v[144:145] op_sel_hi:[1,0]
	v_pk_mul_f32 v[150:151], v[142:143], v[138:139] op_sel_hi:[1,0]
	v_pk_fma_f32 v[140:141], v[146:147], v[144:145], v[140:141] op_sel:[1,1,0] op_sel_hi:[0,1,1] neg_lo:[1,0,0]
	v_pk_fma_f32 v[150:151], v[142:143], v[138:139], v[150:151] op_sel:[1,1,0] op_sel_hi:[0,1,1] neg_lo:[1,0,0]
	v_pk_mul_f32 v[152:153], v[150:151], v[148:149] op_sel_hi:[1,0]
	v_pk_fma_f32 v[148:149], v[150:151], v[148:149], v[152:153] op_sel:[1,1,0] op_sel_hi:[0,1,1] neg_hi:[1,0,0]
	v_pk_add_f32 v[140:141], v[140:141], v[148:149]
	v_pk_mul_f32 v[148:149], v[146:147], v[138:139] op_sel_hi:[1,0]
	v_pk_fma_f32 v[138:139], v[146:147], v[138:139], v[148:149] op_sel:[1,1,0] op_sel_hi:[0,1,1] neg_lo:[1,0,0]
	v_pk_mul_f32 v[146:147], v[142:143], v[144:145] op_sel_hi:[1,0]
	v_pk_fma_f32 v[142:143], v[142:143], v[144:145], v[146:147] op_sel:[1,1,0] op_sel_hi:[0,1,1] neg_lo:[1,0,0]
	v_pk_add_f32 v[138:139], v[138:139], v[142:143]
	s_nop 0
	v_pk_add_f32 v[142:143], v[140:141], v[138:139] op_sel:[0,1] op_sel_hi:[1,0] neg_lo:[0,1]
	v_pk_add_f32 v[138:139], v[140:141], v[138:139] op_sel:[0,1] op_sel_hi:[1,0] neg_hi:[1,0]
	ds_write_b64 v154, v[142:143]
	ds_write_b64 v155, v[138:139]
	v_add_u32_e32 v138, 6, v209
	v_lshlrev_b32_e32 v140, 10, v138
	v_lshlrev_b32_e32 v141, 2, v138
	v_lshrrev_b32_e32 v142, 5, v138
	v_ashrrev_i32_e32 v138, 11, v138
	v_and_b32_e32 v140, 0x3c00, v140
	v_and_b32_e32 v142, 56, v142
	v_and_or_b32 v138, v141, s9, v138
	v_or3_b32 v138, v138, v140, v142
	v_mul_i32_i24_e32 v138, 9, v138
	v_sub_u32_e32 v139, -6, v209
	v_and_b32_e32 v138, -8, v138
	v_add_u32_e32 v150, 0, v138
	v_lshlrev_b32_e32 v138, 10, v139
	v_lshlrev_b32_e32 v140, 2, v139
	v_lshrrev_b32_e32 v141, 5, v139
	v_bfe_u32 v139, v139, 11, 3
	v_and_b32_e32 v138, 0x3c00, v138
	v_and_b32_e32 v140, 0x3c0, v140
	v_and_or_b32 v139, v141, 56, v139
	v_or3_b32 v138, v139, v140, v138
	v_mul_u32_u24_e32 v138, 9, v138
	v_and_b32_e32 v138, 0x3fff8, v138
	v_add_u32_e32 v151, 0, v138
	ds_read_b64 v[138:139], v150
	ds_read_b64 v[140:141], v151
	v_pk_mul_f32 v[142:143], v[162:163], s[42:43] op_sel_hi:[0,1]
	v_pk_fma_f32 v[144:145], v[38:39], s[44:45], v[142:143] neg_lo:[0,0,1] neg_hi:[0,0,1]
	v_pk_fma_f32 v[142:143], v[158:159], s[44:45], v[142:143] op_sel_hi:[0,1,1]
	v_mov_b32_e32 v145, v143
	s_waitcnt lgkmcnt(0)
	v_pk_add_f32 v[142:143], v[138:139], v[140:141] neg_hi:[0,1]
	v_pk_add_f32 v[138:139], v[138:139], v[140:141] op_sel:[1,1] op_sel_hi:[0,0] neg_hi:[1,0]
	v_pk_add_f32 v[140:141], v[134:135], v[136:137] neg_hi:[0,1]
	v_pk_add_f32 v[134:135], v[134:135], v[136:137] op_sel:[1,1] op_sel_hi:[0,0] neg_hi:[1,0]
	v_pk_mul_f32 v[136:137], v[142:143], v[140:141] op_sel_hi:[1,0]
	v_pk_mul_f32 v[146:147], v[138:139], v[134:135] op_sel_hi:[1,0]
	v_pk_fma_f32 v[136:137], v[142:143], v[140:141], v[136:137] op_sel:[1,1,0] op_sel_hi:[0,1,1] neg_lo:[1,0,0]
	v_pk_fma_f32 v[146:147], v[138:139], v[134:135], v[146:147] op_sel:[1,1,0] op_sel_hi:[0,1,1] neg_lo:[1,0,0]
	v_pk_mul_f32 v[148:149], v[146:147], v[144:145] op_sel_hi:[1,0]
	v_pk_fma_f32 v[144:145], v[146:147], v[144:145], v[148:149] op_sel:[1,1,0] op_sel_hi:[0,1,1] neg_hi:[1,0,0]
	v_pk_add_f32 v[136:137], v[136:137], v[144:145]
	v_pk_mul_f32 v[144:145], v[142:143], v[134:135] op_sel_hi:[1,0]
	v_pk_fma_f32 v[134:135], v[142:143], v[134:135], v[144:145] op_sel:[1,1,0] op_sel_hi:[0,1,1] neg_lo:[1,0,0]
	v_pk_mul_f32 v[142:143], v[138:139], v[140:141] op_sel_hi:[1,0]
	v_pk_fma_f32 v[138:139], v[138:139], v[140:141], v[142:143] op_sel:[1,1,0] op_sel_hi:[0,1,1] neg_lo:[1,0,0]
	v_pk_add_f32 v[134:135], v[134:135], v[138:139]
	s_nop 0
	v_pk_add_f32 v[138:139], v[136:137], v[134:135] op_sel:[0,1] op_sel_hi:[1,0] neg_lo:[0,1]
	v_pk_add_f32 v[134:135], v[136:137], v[134:135] op_sel:[0,1] op_sel_hi:[1,0] neg_hi:[1,0]
	ds_write_b64 v150, v[138:139]
	ds_write_b64 v151, v[134:135]
	v_add_u32_e32 v134, 7, v209
	v_lshlrev_b32_e32 v136, 10, v134
	v_lshlrev_b32_e32 v137, 2, v134
	v_lshrrev_b32_e32 v138, 5, v134
	v_ashrrev_i32_e32 v134, 11, v134
	v_and_b32_e32 v136, 0x3c00, v136
	v_and_b32_e32 v138, 56, v138
	v_and_or_b32 v134, v137, s9, v134
	v_or3_b32 v134, v134, v136, v138
	v_mul_i32_i24_e32 v134, 9, v134
	v_sub_u32_e32 v135, -7, v209
	v_and_b32_e32 v134, -8, v134
	v_add_u32_e32 v146, 0, v134
	v_lshlrev_b32_e32 v134, 10, v135
	v_lshlrev_b32_e32 v136, 2, v135
	v_lshrrev_b32_e32 v137, 5, v135
	v_bfe_u32 v135, v135, 11, 3
	v_and_b32_e32 v134, 0x3c00, v134
	v_and_b32_e32 v136, 0x3c0, v136
	v_and_or_b32 v135, v137, 56, v135
	v_or3_b32 v134, v135, v136, v134
	v_mul_u32_u24_e32 v134, 9, v134
	v_and_b32_e32 v134, 0x3fff8, v134
	v_add_u32_e32 v147, 0, v134
	ds_read_b64 v[134:135], v146
	ds_read_b64 v[136:137], v147
	v_pk_mul_f32 v[138:139], v[162:163], s[46:47] op_sel_hi:[0,1]
	v_pk_fma_f32 v[140:141], v[38:39], s[48:49], v[138:139] neg_lo:[0,0,1] neg_hi:[0,0,1]
	v_pk_fma_f32 v[138:139], v[158:159], s[48:49], v[138:139] op_sel_hi:[0,1,1]
	v_mov_b32_e32 v141, v139
	s_waitcnt lgkmcnt(0)
	v_pk_add_f32 v[138:139], v[134:135], v[136:137] neg_hi:[0,1]
	v_pk_add_f32 v[134:135], v[134:135], v[136:137] op_sel:[1,1] op_sel_hi:[0,0] neg_hi:[1,0]
	v_pk_add_f32 v[136:137], v[130:131], v[132:133] neg_hi:[0,1]
	v_pk_add_f32 v[130:131], v[130:131], v[132:133] op_sel:[1,1] op_sel_hi:[0,0] neg_hi:[1,0]
	v_pk_mul_f32 v[132:133], v[138:139], v[136:137] op_sel_hi:[1,0]
	v_pk_mul_f32 v[142:143], v[134:135], v[130:131] op_sel_hi:[1,0]
	v_pk_fma_f32 v[132:133], v[138:139], v[136:137], v[132:133] op_sel:[1,1,0] op_sel_hi:[0,1,1] neg_lo:[1,0,0]
	v_pk_fma_f32 v[142:143], v[134:135], v[130:131], v[142:143] op_sel:[1,1,0] op_sel_hi:[0,1,1] neg_lo:[1,0,0]
	v_pk_mul_f32 v[144:145], v[142:143], v[140:141] op_sel_hi:[1,0]
	v_pk_fma_f32 v[140:141], v[142:143], v[140:141], v[144:145] op_sel:[1,1,0] op_sel_hi:[0,1,1] neg_hi:[1,0,0]
	v_pk_add_f32 v[132:133], v[132:133], v[140:141]
	v_pk_mul_f32 v[140:141], v[138:139], v[130:131] op_sel_hi:[1,0]
	v_pk_fma_f32 v[130:131], v[138:139], v[130:131], v[140:141] op_sel:[1,1,0] op_sel_hi:[0,1,1] neg_lo:[1,0,0]
	v_pk_mul_f32 v[138:139], v[134:135], v[136:137] op_sel_hi:[1,0]
	v_pk_fma_f32 v[134:135], v[134:135], v[136:137], v[138:139] op_sel:[1,1,0] op_sel_hi:[0,1,1] neg_lo:[1,0,0]
	v_pk_add_f32 v[130:131], v[130:131], v[134:135]
	s_nop 0
	v_pk_add_f32 v[134:135], v[132:133], v[130:131] op_sel:[0,1] op_sel_hi:[1,0] neg_lo:[0,1]
	v_pk_add_f32 v[130:131], v[132:133], v[130:131] op_sel:[0,1] op_sel_hi:[1,0] neg_hi:[1,0]
	ds_write_b64 v146, v[134:135]
	ds_write_b64 v147, v[130:131]
	v_add_u32_e32 v130, 8, v209
	v_lshlrev_b32_e32 v132, 10, v130
	v_lshlrev_b32_e32 v133, 2, v130
	v_lshrrev_b32_e32 v134, 5, v130
	v_ashrrev_i32_e32 v130, 11, v130
	v_and_b32_e32 v132, 0x3c00, v132
	v_and_b32_e32 v134, 56, v134
	v_and_or_b32 v130, v133, s9, v130
	v_or3_b32 v130, v130, v132, v134
	v_mul_i32_i24_e32 v130, 9, v130
	v_sub_u32_e32 v131, -8, v209
	v_and_b32_e32 v130, -8, v130
	v_add_u32_e32 v142, 0, v130
	v_lshlrev_b32_e32 v130, 10, v131
	v_lshlrev_b32_e32 v132, 2, v131
	v_lshrrev_b32_e32 v133, 5, v131
	v_bfe_u32 v131, v131, 11, 3
	v_and_b32_e32 v130, 0x3c00, v130
	v_and_b32_e32 v132, 0x3c0, v132
	v_and_or_b32 v131, v133, 56, v131
	v_or3_b32 v130, v131, v132, v130
	v_mul_u32_u24_e32 v130, 9, v130
	v_and_b32_e32 v130, 0x3fff8, v130
	v_add_u32_e32 v143, 0, v130
	ds_read_b64 v[130:131], v142
	ds_read_b64 v[132:133], v143
	v_pk_mul_f32 v[134:135], v[162:163], s[50:51] op_sel_hi:[0,1]
	v_pk_fma_f32 v[136:137], v[38:39], s[52:53], v[134:135] neg_lo:[0,0,1] neg_hi:[0,0,1]
	v_pk_fma_f32 v[134:135], v[158:159], s[52:53], v[134:135] op_sel_hi:[0,1,1]
	v_mov_b32_e32 v137, v135
	s_waitcnt lgkmcnt(0)
	v_pk_add_f32 v[134:135], v[130:131], v[132:133] neg_hi:[0,1]
	v_pk_add_f32 v[130:131], v[130:131], v[132:133] op_sel:[1,1] op_sel_hi:[0,0] neg_hi:[1,0]
	v_pk_add_f32 v[132:133], v[126:127], v[128:129] neg_hi:[0,1]
	v_pk_add_f32 v[126:127], v[126:127], v[128:129] op_sel:[1,1] op_sel_hi:[0,0] neg_hi:[1,0]
	v_pk_mul_f32 v[128:129], v[134:135], v[132:133] op_sel_hi:[1,0]
	v_pk_mul_f32 v[138:139], v[130:131], v[126:127] op_sel_hi:[1,0]
	v_pk_fma_f32 v[128:129], v[134:135], v[132:133], v[128:129] op_sel:[1,1,0] op_sel_hi:[0,1,1] neg_lo:[1,0,0]
	v_pk_fma_f32 v[138:139], v[130:131], v[126:127], v[138:139] op_sel:[1,1,0] op_sel_hi:[0,1,1] neg_lo:[1,0,0]
	v_pk_mul_f32 v[140:141], v[138:139], v[136:137] op_sel_hi:[1,0]
	v_pk_fma_f32 v[136:137], v[138:139], v[136:137], v[140:141] op_sel:[1,1,0] op_sel_hi:[0,1,1] neg_hi:[1,0,0]
	v_pk_add_f32 v[128:129], v[128:129], v[136:137]
	v_pk_mul_f32 v[136:137], v[134:135], v[126:127] op_sel_hi:[1,0]
	v_pk_fma_f32 v[126:127], v[134:135], v[126:127], v[136:137] op_sel:[1,1,0] op_sel_hi:[0,1,1] neg_lo:[1,0,0]
	v_pk_mul_f32 v[134:135], v[130:131], v[132:133] op_sel_hi:[1,0]
	v_pk_fma_f32 v[130:131], v[130:131], v[132:133], v[134:135] op_sel:[1,1,0] op_sel_hi:[0,1,1] neg_lo:[1,0,0]
	v_pk_add_f32 v[126:127], v[126:127], v[130:131]
	s_nop 0
	v_pk_add_f32 v[130:131], v[128:129], v[126:127] op_sel:[0,1] op_sel_hi:[1,0] neg_lo:[0,1]
	v_pk_add_f32 v[126:127], v[128:129], v[126:127] op_sel:[0,1] op_sel_hi:[1,0] neg_hi:[1,0]
	ds_write_b64 v142, v[130:131]
	ds_write_b64 v143, v[126:127]
	v_add_u32_e32 v126, 9, v209
	v_lshlrev_b32_e32 v128, 10, v126
	v_lshlrev_b32_e32 v129, 2, v126
	v_lshrrev_b32_e32 v130, 5, v126
	v_ashrrev_i32_e32 v126, 11, v126
	v_and_b32_e32 v128, 0x3c00, v128
	v_and_b32_e32 v130, 56, v130
	v_and_or_b32 v126, v129, s9, v126
	v_or3_b32 v126, v126, v128, v130
	v_mul_i32_i24_e32 v126, 9, v126
	v_sub_u32_e32 v127, -9, v209
	v_and_b32_e32 v126, -8, v126
	v_add_u32_e32 v138, 0, v126
	v_lshlrev_b32_e32 v126, 10, v127
	v_lshlrev_b32_e32 v128, 2, v127
	v_lshrrev_b32_e32 v129, 5, v127
	v_bfe_u32 v127, v127, 11, 3
	v_and_b32_e32 v126, 0x3c00, v126
	v_and_b32_e32 v128, 0x3c0, v128
	v_and_or_b32 v127, v129, 56, v127
	v_or3_b32 v126, v127, v128, v126
	v_mul_u32_u24_e32 v126, 9, v126
	v_and_b32_e32 v126, 0x3fff8, v126
	v_add_u32_e32 v139, 0, v126
	ds_read_b64 v[126:127], v138
	ds_read_b64 v[128:129], v139
	v_pk_mul_f32 v[130:131], v[162:163], s[54:55] op_sel_hi:[0,1]
	v_pk_fma_f32 v[132:133], v[38:39], s[56:57], v[130:131] neg_lo:[0,0,1] neg_hi:[0,0,1]
	v_pk_fma_f32 v[130:131], v[158:159], s[56:57], v[130:131] op_sel_hi:[0,1,1]
	v_mov_b32_e32 v133, v131
	s_waitcnt lgkmcnt(0)
	v_pk_add_f32 v[130:131], v[126:127], v[128:129] neg_hi:[0,1]
	v_pk_add_f32 v[126:127], v[126:127], v[128:129] op_sel:[1,1] op_sel_hi:[0,0] neg_hi:[1,0]
	v_pk_add_f32 v[128:129], v[122:123], v[124:125] neg_hi:[0,1]
	v_pk_add_f32 v[122:123], v[122:123], v[124:125] op_sel:[1,1] op_sel_hi:[0,0] neg_hi:[1,0]
	v_pk_mul_f32 v[124:125], v[130:131], v[128:129] op_sel_hi:[1,0]
	v_pk_mul_f32 v[134:135], v[126:127], v[122:123] op_sel_hi:[1,0]
	v_pk_fma_f32 v[124:125], v[130:131], v[128:129], v[124:125] op_sel:[1,1,0] op_sel_hi:[0,1,1] neg_lo:[1,0,0]
	v_pk_fma_f32 v[134:135], v[126:127], v[122:123], v[134:135] op_sel:[1,1,0] op_sel_hi:[0,1,1] neg_lo:[1,0,0]
	v_pk_mul_f32 v[136:137], v[134:135], v[132:133] op_sel_hi:[1,0]
	v_pk_fma_f32 v[132:133], v[134:135], v[132:133], v[136:137] op_sel:[1,1,0] op_sel_hi:[0,1,1] neg_hi:[1,0,0]
	v_pk_add_f32 v[124:125], v[124:125], v[132:133]
	v_pk_mul_f32 v[132:133], v[130:131], v[122:123] op_sel_hi:[1,0]
	v_pk_fma_f32 v[122:123], v[130:131], v[122:123], v[132:133] op_sel:[1,1,0] op_sel_hi:[0,1,1] neg_lo:[1,0,0]
	v_pk_mul_f32 v[130:131], v[126:127], v[128:129] op_sel_hi:[1,0]
	v_pk_fma_f32 v[126:127], v[126:127], v[128:129], v[130:131] op_sel:[1,1,0] op_sel_hi:[0,1,1] neg_lo:[1,0,0]
	v_pk_add_f32 v[122:123], v[122:123], v[126:127]
	s_nop 0
	v_pk_add_f32 v[126:127], v[124:125], v[122:123] op_sel:[0,1] op_sel_hi:[1,0] neg_lo:[0,1]
	v_pk_add_f32 v[122:123], v[124:125], v[122:123] op_sel:[0,1] op_sel_hi:[1,0] neg_hi:[1,0]
	ds_write_b64 v138, v[126:127]
	ds_write_b64 v139, v[122:123]
	v_add_u32_e32 v122, 10, v209
	v_lshlrev_b32_e32 v124, 10, v122
	v_lshlrev_b32_e32 v125, 2, v122
	v_lshrrev_b32_e32 v126, 5, v122
	v_ashrrev_i32_e32 v122, 11, v122
	v_and_b32_e32 v124, 0x3c00, v124
	v_and_b32_e32 v126, 56, v126
	v_and_or_b32 v122, v125, s9, v122
	v_or3_b32 v122, v122, v124, v126
	v_mul_i32_i24_e32 v122, 9, v122
	v_sub_u32_e32 v123, -10, v209
	v_and_b32_e32 v122, -8, v122
	v_add_u32_e32 v134, 0, v122
	v_lshlrev_b32_e32 v122, 10, v123
	v_lshlrev_b32_e32 v124, 2, v123
	v_lshrrev_b32_e32 v125, 5, v123
	v_bfe_u32 v123, v123, 11, 3
	v_and_b32_e32 v122, 0x3c00, v122
	v_and_b32_e32 v124, 0x3c0, v124
	v_and_or_b32 v123, v125, 56, v123
	v_or3_b32 v122, v123, v124, v122
	v_mul_u32_u24_e32 v122, 9, v122
	v_and_b32_e32 v122, 0x3fff8, v122
	v_add_u32_e32 v135, 0, v122
	ds_read_b64 v[122:123], v134
	ds_read_b64 v[124:125], v135
	v_pk_mul_f32 v[126:127], v[162:163], s[58:59] op_sel_hi:[0,1]
	v_pk_fma_f32 v[128:129], v[38:39], s[60:61], v[126:127] neg_lo:[0,0,1] neg_hi:[0,0,1]
	v_pk_fma_f32 v[126:127], v[158:159], s[60:61], v[126:127] op_sel_hi:[0,1,1]
	v_mov_b32_e32 v129, v127
	s_waitcnt lgkmcnt(0)
	v_pk_add_f32 v[126:127], v[122:123], v[124:125] neg_hi:[0,1]
	v_pk_add_f32 v[122:123], v[122:123], v[124:125] op_sel:[1,1] op_sel_hi:[0,0] neg_hi:[1,0]
	v_pk_add_f32 v[124:125], v[118:119], v[120:121] neg_hi:[0,1]
	v_pk_add_f32 v[118:119], v[118:119], v[120:121] op_sel:[1,1] op_sel_hi:[0,0] neg_hi:[1,0]
	v_pk_mul_f32 v[120:121], v[126:127], v[124:125] op_sel_hi:[1,0]
	v_pk_mul_f32 v[130:131], v[122:123], v[118:119] op_sel_hi:[1,0]
	v_pk_fma_f32 v[120:121], v[126:127], v[124:125], v[120:121] op_sel:[1,1,0] op_sel_hi:[0,1,1] neg_lo:[1,0,0]
	v_pk_fma_f32 v[130:131], v[122:123], v[118:119], v[130:131] op_sel:[1,1,0] op_sel_hi:[0,1,1] neg_lo:[1,0,0]
	v_pk_mul_f32 v[132:133], v[130:131], v[128:129] op_sel_hi:[1,0]
	v_pk_fma_f32 v[128:129], v[130:131], v[128:129], v[132:133] op_sel:[1,1,0] op_sel_hi:[0,1,1] neg_hi:[1,0,0]
	v_pk_add_f32 v[120:121], v[120:121], v[128:129]
	v_pk_mul_f32 v[128:129], v[126:127], v[118:119] op_sel_hi:[1,0]
	v_pk_fma_f32 v[118:119], v[126:127], v[118:119], v[128:129] op_sel:[1,1,0] op_sel_hi:[0,1,1] neg_lo:[1,0,0]
	v_pk_mul_f32 v[126:127], v[122:123], v[124:125] op_sel_hi:[1,0]
	v_pk_fma_f32 v[122:123], v[122:123], v[124:125], v[126:127] op_sel:[1,1,0] op_sel_hi:[0,1,1] neg_lo:[1,0,0]
	v_pk_add_f32 v[118:119], v[118:119], v[122:123]
	s_nop 0
	v_pk_add_f32 v[122:123], v[120:121], v[118:119] op_sel:[0,1] op_sel_hi:[1,0] neg_lo:[0,1]
	v_pk_add_f32 v[118:119], v[120:121], v[118:119] op_sel:[0,1] op_sel_hi:[1,0] neg_hi:[1,0]
	ds_write_b64 v134, v[122:123]
	ds_write_b64 v135, v[118:119]
	v_add_u32_e32 v118, 11, v209
	v_lshlrev_b32_e32 v120, 10, v118
	v_lshlrev_b32_e32 v121, 2, v118
	v_lshrrev_b32_e32 v122, 5, v118
	v_ashrrev_i32_e32 v118, 11, v118
	v_and_b32_e32 v120, 0x3c00, v120
	v_and_b32_e32 v122, 56, v122
	v_and_or_b32 v118, v121, s9, v118
	v_or3_b32 v118, v118, v120, v122
	v_mul_i32_i24_e32 v118, 9, v118
	v_sub_u32_e32 v119, -11, v209
	v_and_b32_e32 v118, -8, v118
	v_add_u32_e32 v130, 0, v118
	v_lshlrev_b32_e32 v118, 10, v119
	v_lshlrev_b32_e32 v120, 2, v119
	v_lshrrev_b32_e32 v121, 5, v119
	v_bfe_u32 v119, v119, 11, 3
	v_and_b32_e32 v118, 0x3c00, v118
	v_and_b32_e32 v120, 0x3c0, v120
	v_and_or_b32 v119, v121, 56, v119
	v_or3_b32 v118, v119, v120, v118
	v_mul_u32_u24_e32 v118, 9, v118
	v_and_b32_e32 v118, 0x3fff8, v118
	v_add_u32_e32 v131, 0, v118
	ds_read_b64 v[118:119], v130
	ds_read_b64 v[120:121], v131
	v_pk_mul_f32 v[122:123], v[162:163], s[62:63] op_sel_hi:[0,1]
	v_pk_fma_f32 v[124:125], v[38:39], s[64:65], v[122:123] neg_lo:[0,0,1] neg_hi:[0,0,1]
	v_pk_fma_f32 v[122:123], v[158:159], s[64:65], v[122:123] op_sel_hi:[0,1,1]
	v_mov_b32_e32 v125, v123
	s_waitcnt lgkmcnt(0)
	v_pk_add_f32 v[122:123], v[118:119], v[120:121] neg_hi:[0,1]
	v_pk_add_f32 v[118:119], v[118:119], v[120:121] op_sel:[1,1] op_sel_hi:[0,0] neg_hi:[1,0]
	v_pk_add_f32 v[120:121], v[114:115], v[116:117] neg_hi:[0,1]
	v_pk_add_f32 v[114:115], v[114:115], v[116:117] op_sel:[1,1] op_sel_hi:[0,0] neg_hi:[1,0]
	v_pk_mul_f32 v[116:117], v[122:123], v[120:121] op_sel_hi:[1,0]
	v_pk_mul_f32 v[126:127], v[118:119], v[114:115] op_sel_hi:[1,0]
	v_pk_fma_f32 v[116:117], v[122:123], v[120:121], v[116:117] op_sel:[1,1,0] op_sel_hi:[0,1,1] neg_lo:[1,0,0]
	v_pk_fma_f32 v[126:127], v[118:119], v[114:115], v[126:127] op_sel:[1,1,0] op_sel_hi:[0,1,1] neg_lo:[1,0,0]
	v_pk_mul_f32 v[128:129], v[126:127], v[124:125] op_sel_hi:[1,0]
	v_pk_fma_f32 v[124:125], v[126:127], v[124:125], v[128:129] op_sel:[1,1,0] op_sel_hi:[0,1,1] neg_hi:[1,0,0]
	v_pk_add_f32 v[116:117], v[116:117], v[124:125]
	v_pk_mul_f32 v[124:125], v[122:123], v[114:115] op_sel_hi:[1,0]
	v_pk_fma_f32 v[114:115], v[122:123], v[114:115], v[124:125] op_sel:[1,1,0] op_sel_hi:[0,1,1] neg_lo:[1,0,0]
	v_pk_mul_f32 v[122:123], v[118:119], v[120:121] op_sel_hi:[1,0]
	v_pk_fma_f32 v[118:119], v[118:119], v[120:121], v[122:123] op_sel:[1,1,0] op_sel_hi:[0,1,1] neg_lo:[1,0,0]
	v_pk_add_f32 v[114:115], v[114:115], v[118:119]
	s_nop 0
	v_pk_add_f32 v[118:119], v[116:117], v[114:115] op_sel:[0,1] op_sel_hi:[1,0] neg_lo:[0,1]
	v_pk_add_f32 v[114:115], v[116:117], v[114:115] op_sel:[0,1] op_sel_hi:[1,0] neg_hi:[1,0]
	ds_write_b64 v130, v[118:119]
	ds_write_b64 v131, v[114:115]
	v_add_u32_e32 v114, 12, v209
	v_lshlrev_b32_e32 v116, 10, v114
	v_lshlrev_b32_e32 v117, 2, v114
	v_lshrrev_b32_e32 v118, 5, v114
	v_ashrrev_i32_e32 v114, 11, v114
	v_and_b32_e32 v116, 0x3c00, v116
	v_and_b32_e32 v118, 56, v118
	v_and_or_b32 v114, v117, s9, v114
	v_or3_b32 v114, v114, v116, v118
	v_mul_i32_i24_e32 v114, 9, v114
	v_sub_u32_e32 v115, -12, v209
	v_and_b32_e32 v114, -8, v114
	v_add_u32_e32 v126, 0, v114
	v_lshlrev_b32_e32 v114, 10, v115
	v_lshlrev_b32_e32 v116, 2, v115
	v_lshrrev_b32_e32 v117, 5, v115
	v_bfe_u32 v115, v115, 11, 3
	v_and_b32_e32 v114, 0x3c00, v114
	v_and_b32_e32 v116, 0x3c0, v116
	v_and_or_b32 v115, v117, 56, v115
	v_or3_b32 v114, v115, v116, v114
	v_mul_u32_u24_e32 v114, 9, v114
	v_and_b32_e32 v114, 0x3fff8, v114
	v_add_u32_e32 v127, 0, v114
	ds_read_b64 v[114:115], v126
	ds_read_b64 v[116:117], v127
	v_pk_mul_f32 v[118:119], v[162:163], s[66:67] op_sel_hi:[0,1]
	v_pk_fma_f32 v[120:121], v[38:39], s[68:69], v[118:119] neg_lo:[0,0,1] neg_hi:[0,0,1]
	v_pk_fma_f32 v[118:119], v[158:159], s[68:69], v[118:119] op_sel_hi:[0,1,1]
	v_mov_b32_e32 v121, v119
	s_waitcnt lgkmcnt(0)
	v_pk_add_f32 v[118:119], v[114:115], v[116:117] neg_hi:[0,1]
	v_pk_add_f32 v[114:115], v[114:115], v[116:117] op_sel:[1,1] op_sel_hi:[0,0] neg_hi:[1,0]
	v_pk_add_f32 v[116:117], v[110:111], v[112:113] neg_hi:[0,1]
	v_pk_add_f32 v[110:111], v[110:111], v[112:113] op_sel:[1,1] op_sel_hi:[0,0] neg_hi:[1,0]
	v_pk_mul_f32 v[112:113], v[118:119], v[116:117] op_sel_hi:[1,0]
	v_pk_mul_f32 v[122:123], v[114:115], v[110:111] op_sel_hi:[1,0]
	v_pk_fma_f32 v[112:113], v[118:119], v[116:117], v[112:113] op_sel:[1,1,0] op_sel_hi:[0,1,1] neg_lo:[1,0,0]
	v_pk_fma_f32 v[122:123], v[114:115], v[110:111], v[122:123] op_sel:[1,1,0] op_sel_hi:[0,1,1] neg_lo:[1,0,0]
	v_pk_mul_f32 v[124:125], v[122:123], v[120:121] op_sel_hi:[1,0]
	v_pk_fma_f32 v[120:121], v[122:123], v[120:121], v[124:125] op_sel:[1,1,0] op_sel_hi:[0,1,1] neg_hi:[1,0,0]
	v_pk_add_f32 v[112:113], v[112:113], v[120:121]
	v_pk_mul_f32 v[120:121], v[118:119], v[110:111] op_sel_hi:[1,0]
	v_pk_fma_f32 v[110:111], v[118:119], v[110:111], v[120:121] op_sel:[1,1,0] op_sel_hi:[0,1,1] neg_lo:[1,0,0]
	v_pk_mul_f32 v[118:119], v[114:115], v[116:117] op_sel_hi:[1,0]
	v_pk_fma_f32 v[114:115], v[114:115], v[116:117], v[118:119] op_sel:[1,1,0] op_sel_hi:[0,1,1] neg_lo:[1,0,0]
	v_pk_add_f32 v[110:111], v[110:111], v[114:115]
	s_nop 0
	v_pk_add_f32 v[114:115], v[112:113], v[110:111] op_sel:[0,1] op_sel_hi:[1,0] neg_lo:[0,1]
	v_pk_add_f32 v[110:111], v[112:113], v[110:111] op_sel:[0,1] op_sel_hi:[1,0] neg_hi:[1,0]
	ds_write_b64 v126, v[114:115]
	ds_write_b64 v127, v[110:111]
	v_add_u32_e32 v110, 13, v209
	v_lshlrev_b32_e32 v112, 10, v110
	v_lshlrev_b32_e32 v113, 2, v110
	v_lshrrev_b32_e32 v114, 5, v110
	v_ashrrev_i32_e32 v110, 11, v110
	v_and_b32_e32 v112, 0x3c00, v112
	v_and_b32_e32 v114, 56, v114
	v_and_or_b32 v110, v113, s9, v110
	v_or3_b32 v110, v110, v112, v114
	v_mul_i32_i24_e32 v110, 9, v110
	v_sub_u32_e32 v111, -13, v209
	v_and_b32_e32 v110, -8, v110
	v_add_u32_e32 v122, 0, v110
	v_lshlrev_b32_e32 v110, 10, v111
	v_lshlrev_b32_e32 v112, 2, v111
	v_lshrrev_b32_e32 v113, 5, v111
	v_bfe_u32 v111, v111, 11, 3
	v_and_b32_e32 v110, 0x3c00, v110
	v_and_b32_e32 v112, 0x3c0, v112
	v_and_or_b32 v111, v113, 56, v111
	v_or3_b32 v110, v111, v112, v110
	v_mul_u32_u24_e32 v110, 9, v110
	v_and_b32_e32 v110, 0x3fff8, v110
	v_add_u32_e32 v123, 0, v110
	ds_read_b64 v[110:111], v122
	ds_read_b64 v[112:113], v123
	v_pk_mul_f32 v[114:115], v[162:163], s[70:71] op_sel_hi:[0,1]
	v_pk_fma_f32 v[116:117], v[38:39], s[72:73], v[114:115] neg_lo:[0,0,1] neg_hi:[0,0,1]
	v_pk_fma_f32 v[114:115], v[158:159], s[72:73], v[114:115] op_sel_hi:[0,1,1]
	v_mov_b32_e32 v117, v115
	s_waitcnt lgkmcnt(0)
	v_pk_add_f32 v[114:115], v[110:111], v[112:113] neg_hi:[0,1]
	v_pk_add_f32 v[110:111], v[110:111], v[112:113] op_sel:[1,1] op_sel_hi:[0,0] neg_hi:[1,0]
	v_pk_add_f32 v[112:113], v[106:107], v[108:109] neg_hi:[0,1]
	v_pk_add_f32 v[106:107], v[106:107], v[108:109] op_sel:[1,1] op_sel_hi:[0,0] neg_hi:[1,0]
	v_pk_mul_f32 v[108:109], v[114:115], v[112:113] op_sel_hi:[1,0]
	v_pk_mul_f32 v[118:119], v[110:111], v[106:107] op_sel_hi:[1,0]
	v_pk_fma_f32 v[108:109], v[114:115], v[112:113], v[108:109] op_sel:[1,1,0] op_sel_hi:[0,1,1] neg_lo:[1,0,0]
	v_pk_fma_f32 v[118:119], v[110:111], v[106:107], v[118:119] op_sel:[1,1,0] op_sel_hi:[0,1,1] neg_lo:[1,0,0]
	v_pk_mul_f32 v[120:121], v[118:119], v[116:117] op_sel_hi:[1,0]
	v_pk_fma_f32 v[116:117], v[118:119], v[116:117], v[120:121] op_sel:[1,1,0] op_sel_hi:[0,1,1] neg_hi:[1,0,0]
	v_pk_add_f32 v[108:109], v[108:109], v[116:117]
	v_pk_mul_f32 v[116:117], v[114:115], v[106:107] op_sel_hi:[1,0]
	v_pk_fma_f32 v[106:107], v[114:115], v[106:107], v[116:117] op_sel:[1,1,0] op_sel_hi:[0,1,1] neg_lo:[1,0,0]
	v_pk_mul_f32 v[114:115], v[110:111], v[112:113] op_sel_hi:[1,0]
	v_pk_fma_f32 v[110:111], v[110:111], v[112:113], v[114:115] op_sel:[1,1,0] op_sel_hi:[0,1,1] neg_lo:[1,0,0]
	v_pk_add_f32 v[106:107], v[106:107], v[110:111]
	s_nop 0
	v_pk_add_f32 v[110:111], v[108:109], v[106:107] op_sel:[0,1] op_sel_hi:[1,0] neg_lo:[0,1]
	v_pk_add_f32 v[106:107], v[108:109], v[106:107] op_sel:[0,1] op_sel_hi:[1,0] neg_hi:[1,0]
	ds_write_b64 v122, v[110:111]
	ds_write_b64 v123, v[106:107]
	v_add_u32_e32 v106, 14, v209
	v_lshlrev_b32_e32 v108, 10, v106
	v_lshlrev_b32_e32 v109, 2, v106
	v_lshrrev_b32_e32 v110, 5, v106
	v_ashrrev_i32_e32 v106, 11, v106
	v_and_b32_e32 v108, 0x3c00, v108
	v_and_b32_e32 v110, 56, v110
	v_and_or_b32 v106, v109, s9, v106
	v_or3_b32 v106, v106, v108, v110
	v_mul_i32_i24_e32 v106, 9, v106
	v_sub_u32_e32 v107, -14, v209
	v_and_b32_e32 v106, -8, v106
	v_add_u32_e32 v118, 0, v106
	v_lshlrev_b32_e32 v106, 10, v107
	v_lshlrev_b32_e32 v108, 2, v107
	v_lshrrev_b32_e32 v109, 5, v107
	v_bfe_u32 v107, v107, 11, 3
	v_and_b32_e32 v106, 0x3c00, v106
	v_and_b32_e32 v108, 0x3c0, v108
	v_and_or_b32 v107, v109, 56, v107
	v_or3_b32 v106, v107, v108, v106
	v_mul_u32_u24_e32 v106, 9, v106
	v_and_b32_e32 v106, 0x3fff8, v106
	v_add_u32_e32 v119, 0, v106
	ds_read_b64 v[106:107], v118
	ds_read_b64 v[108:109], v119
	v_pk_mul_f32 v[110:111], v[162:163], s[74:75] op_sel_hi:[0,1]
	v_pk_fma_f32 v[112:113], v[38:39], s[76:77], v[110:111] neg_lo:[0,0,1] neg_hi:[0,0,1]
	v_pk_fma_f32 v[110:111], v[158:159], s[76:77], v[110:111] op_sel_hi:[0,1,1]
	v_mov_b32_e32 v113, v111
	s_waitcnt lgkmcnt(0)
	v_pk_add_f32 v[110:111], v[106:107], v[108:109] neg_hi:[0,1]
	v_pk_add_f32 v[106:107], v[106:107], v[108:109] op_sel:[1,1] op_sel_hi:[0,0] neg_hi:[1,0]
	v_pk_add_f32 v[108:109], v[102:103], v[104:105] neg_hi:[0,1]
	v_pk_add_f32 v[102:103], v[102:103], v[104:105] op_sel:[1,1] op_sel_hi:[0,0] neg_hi:[1,0]
	v_pk_mul_f32 v[104:105], v[110:111], v[108:109] op_sel_hi:[1,0]
	v_pk_mul_f32 v[114:115], v[106:107], v[102:103] op_sel_hi:[1,0]
	v_pk_fma_f32 v[104:105], v[110:111], v[108:109], v[104:105] op_sel:[1,1,0] op_sel_hi:[0,1,1] neg_lo:[1,0,0]
	v_pk_fma_f32 v[114:115], v[106:107], v[102:103], v[114:115] op_sel:[1,1,0] op_sel_hi:[0,1,1] neg_lo:[1,0,0]
	v_pk_mul_f32 v[116:117], v[114:115], v[112:113] op_sel_hi:[1,0]
	v_pk_fma_f32 v[112:113], v[114:115], v[112:113], v[116:117] op_sel:[1,1,0] op_sel_hi:[0,1,1] neg_hi:[1,0,0]
	v_pk_add_f32 v[104:105], v[104:105], v[112:113]
	v_pk_mul_f32 v[112:113], v[110:111], v[102:103] op_sel_hi:[1,0]
	v_pk_fma_f32 v[102:103], v[110:111], v[102:103], v[112:113] op_sel:[1,1,0] op_sel_hi:[0,1,1] neg_lo:[1,0,0]
	v_pk_mul_f32 v[110:111], v[106:107], v[108:109] op_sel_hi:[1,0]
	v_pk_fma_f32 v[106:107], v[106:107], v[108:109], v[110:111] op_sel:[1,1,0] op_sel_hi:[0,1,1] neg_lo:[1,0,0]
	v_pk_add_f32 v[102:103], v[102:103], v[106:107]
	s_nop 0
	v_pk_add_f32 v[106:107], v[104:105], v[102:103] op_sel:[0,1] op_sel_hi:[1,0] neg_lo:[0,1]
	v_pk_add_f32 v[102:103], v[104:105], v[102:103] op_sel:[0,1] op_sel_hi:[1,0] neg_hi:[1,0]
	ds_write_b64 v118, v[106:107]
	ds_write_b64 v119, v[102:103]
	v_add_u32_e32 v102, 15, v209
	v_lshlrev_b32_e32 v104, 10, v102
	v_lshlrev_b32_e32 v105, 2, v102
	v_lshrrev_b32_e32 v106, 5, v102
	v_ashrrev_i32_e32 v102, 11, v102
	v_and_b32_e32 v104, 0x3c00, v104
	v_and_b32_e32 v106, 56, v106
	v_and_or_b32 v102, v105, s9, v102
	v_or3_b32 v102, v102, v104, v106
	v_mul_i32_i24_e32 v102, 9, v102
	v_sub_u32_e32 v103, -15, v209
	v_and_b32_e32 v102, -8, v102
	v_add_u32_e32 v114, 0, v102
	v_lshlrev_b32_e32 v102, 10, v103
	v_lshlrev_b32_e32 v104, 2, v103
	v_lshrrev_b32_e32 v105, 5, v103
	v_bfe_u32 v103, v103, 11, 3
	v_and_b32_e32 v102, 0x3c00, v102
	v_and_b32_e32 v104, 0x3c0, v104
	v_and_or_b32 v103, v105, 56, v103
	v_or3_b32 v102, v103, v104, v102
	v_mul_u32_u24_e32 v102, 9, v102
	v_and_b32_e32 v102, 0x3fff8, v102
	v_add_u32_e32 v115, 0, v102
	ds_read_b64 v[102:103], v114
	ds_read_b64 v[104:105], v115
	v_pk_mul_f32 v[106:107], v[162:163], s[78:79] op_sel_hi:[0,1]
	v_pk_fma_f32 v[108:109], v[38:39], s[80:81], v[106:107] neg_lo:[0,0,1] neg_hi:[0,0,1]
	v_pk_fma_f32 v[106:107], v[158:159], s[80:81], v[106:107] op_sel_hi:[0,1,1]
	v_mov_b32_e32 v109, v107
	s_waitcnt lgkmcnt(0)
	v_pk_add_f32 v[106:107], v[102:103], v[104:105] neg_hi:[0,1]
	v_pk_add_f32 v[102:103], v[102:103], v[104:105] op_sel:[1,1] op_sel_hi:[0,0] neg_hi:[1,0]
	v_pk_add_f32 v[104:105], v[2:3], v[4:5] neg_hi:[0,1]
	v_pk_add_f32 v[2:3], v[2:3], v[4:5] op_sel:[1,1] op_sel_hi:[0,0] neg_hi:[1,0]
	v_pk_mul_f32 v[4:5], v[106:107], v[104:105] op_sel_hi:[1,0]
	v_pk_mul_f32 v[110:111], v[102:103], v[2:3] op_sel_hi:[1,0]
	v_pk_fma_f32 v[4:5], v[106:107], v[104:105], v[4:5] op_sel:[1,1,0] op_sel_hi:[0,1,1] neg_lo:[1,0,0]
	v_pk_fma_f32 v[110:111], v[102:103], v[2:3], v[110:111] op_sel:[1,1,0] op_sel_hi:[0,1,1] neg_lo:[1,0,0]
	v_pk_mul_f32 v[112:113], v[110:111], v[108:109] op_sel_hi:[1,0]
	v_pk_fma_f32 v[108:109], v[110:111], v[108:109], v[112:113] op_sel:[1,1,0] op_sel_hi:[0,1,1] neg_hi:[1,0,0]
	v_pk_add_f32 v[4:5], v[4:5], v[108:109]
	v_pk_mul_f32 v[108:109], v[106:107], v[2:3] op_sel_hi:[1,0]
	v_pk_fma_f32 v[2:3], v[106:107], v[2:3], v[108:109] op_sel:[1,1,0] op_sel_hi:[0,1,1] neg_lo:[1,0,0]
	v_pk_mul_f32 v[106:107], v[102:103], v[104:105] op_sel_hi:[1,0]
	v_pk_fma_f32 v[102:103], v[102:103], v[104:105], v[106:107] op_sel:[1,1,0] op_sel_hi:[0,1,1] neg_lo:[1,0,0]
	v_pk_add_f32 v[2:3], v[2:3], v[102:103]
	s_nop 0
	v_pk_add_f32 v[102:103], v[4:5], v[2:3] op_sel:[0,1] op_sel_hi:[1,0] neg_lo:[0,1]
	ds_write_b64 v114, v[102:103]
	v_pk_add_f32 v[2:3], v[4:5], v[2:3] op_sel:[0,1] op_sel_hi:[1,0] neg_hi:[1,0]
	ds_write_b64 v115, v[2:3]
	s_and_saveexec_b64 s[84:85], s[0:1]
	s_cbranch_execz .LBB0_771
	v_mov_b32_e32 v4, s94
	ds_read_b64 v[2:3], v203 offset:32
	ds_read_b64 v[4:5], v4
	s_waitcnt lgkmcnt(1)
	v_pk_add_f32 v[102:103], v[2:3], v[2:3] neg_hi:[0,1]
	v_pk_add_f32 v[2:3], v[2:3], v[2:3] op_sel:[1,1] op_sel_hi:[0,0] neg_hi:[1,0]
	s_waitcnt lgkmcnt(0)
	v_pk_add_f32 v[104:105], v[4:5], v[4:5] neg_hi:[0,1]
	v_pk_add_f32 v[4:5], v[4:5], v[4:5] op_sel:[1,1] op_sel_hi:[0,0] neg_hi:[1,0]
	v_mov_b64_e32 v[110:111], s[2:3]
	v_pk_mul_f32 v[108:109], v[2:3], v[4:5] op_sel_hi:[1,0]
	v_pk_mul_f32 v[106:107], v[102:103], v[104:105] op_sel_hi:[1,0]
	v_pk_fma_f32 v[108:109], v[2:3], v[4:5], v[108:109] op_sel:[1,1,0] op_sel_hi:[0,1,1] neg_lo:[1,0,0]
	v_pk_fma_f32 v[106:107], v[102:103], v[104:105], v[106:107] op_sel:[1,1,0] op_sel_hi:[0,1,1] neg_lo:[1,0,0]
	v_pk_mul_f32 v[112:113], v[108:109], v[110:111] op_sel_hi:[1,0]
	v_pk_fma_f32 v[108:109], v[108:109], v[110:111], v[112:113] op_sel:[1,1,0] op_sel_hi:[0,1,1] neg_hi:[1,0,0]
	v_pk_add_f32 v[106:107], v[106:107], v[108:109]
	v_pk_mul_f32 v[108:109], v[102:103], v[4:5] op_sel_hi:[1,0]
	v_pk_fma_f32 v[4:5], v[102:103], v[4:5], v[108:109] op_sel:[1,1,0] op_sel_hi:[0,1,1] neg_lo:[1,0,0]
	v_pk_mul_f32 v[102:103], v[2:3], v[104:105] op_sel_hi:[1,0]
	v_pk_fma_f32 v[2:3], v[2:3], v[104:105], v[102:103] op_sel:[1,1,0] op_sel_hi:[0,1,1] neg_lo:[1,0,0]
	v_pk_add_f32 v[2:3], v[4:5], v[2:3]
	s_nop 0
	v_pk_add_f32 v[2:3], v[106:107], v[2:3] op_sel:[0,1] op_sel_hi:[1,0] neg_hi:[1,0]
	ds_write_b64 v203, v[2:3] offset:32

.LBB0_774:
	v_add_u32_e32 v248, 0, v2
	ds_read2_b64 v[230:233], v248 offset1:1
	ds_read2_b64 v[234:237], v248 offset0:2 offset1:3
	ds_read2_b64 v[238:241], v248 offset0:4 offset1:5
	ds_read2_b64 v[242:245], v248 offset0:6 offset1:7
	v_add_u32_e32 v3, 0x9000, v2
	ds_read2_b64 v[102:105], v3 offset1:1
	ds_read2_b64 v[106:109], v3 offset0:2 offset1:3
	ds_read2_b64 v[110:113], v3 offset0:4 offset1:5
	ds_read2_b64 v[114:117], v3 offset0:6 offset1:7
	s_waitcnt lgkmcnt(5)
	v_pk_add_f32 v[250:251], v[230:231], v[238:239]
	v_pk_add_f32 v[230:231], v[230:231], v[238:239] neg_lo:[0,1] neg_hi:[0,1]
	v_pk_add_f32 v[238:239], v[232:233], v[240:241]
	v_pk_add_f32 v[232:233], v[232:233], v[240:241] neg_lo:[0,1] neg_hi:[0,1]
	v_mov_b64_e32 v[240:241], s[6:7]
	v_pk_mul_f32 v[246:247], v[232:233], v[240:241] op_sel_hi:[1,0]
	v_pk_fma_f32 v[232:233], v[232:233], v[240:241], v[246:247] op_sel:[1,1,0] op_sel_hi:[0,1,1] neg_lo:[1,0,0]
	s_waitcnt lgkmcnt(4)
	v_pk_add_f32 v[240:241], v[234:235], v[242:243]
	v_pk_add_f32 v[234:235], v[234:235], v[242:243] op_sel:[1,1] op_sel_hi:[0,0] neg_lo:[1,0] neg_hi:[0,1]
	v_pk_add_f32 v[242:243], v[236:237], v[244:245]
	v_pk_add_f32 v[236:237], v[236:237], v[244:245] neg_lo:[0,1] neg_hi:[0,1]
	v_mov_b64_e32 v[244:245], s[14:15]
	v_pk_mul_f32 v[246:247], v[236:237], v[244:245] op_sel_hi:[1,0]
	v_pk_fma_f32 v[236:237], v[236:237], v[244:245], v[246:247] op_sel:[1,1,0] op_sel_hi:[0,1,1] neg_lo:[1,0,0]
	v_pk_add_f32 v[244:245], v[250:251], v[240:241]
	v_pk_add_f32 v[250:251], v[250:251], v[240:241] neg_lo:[0,1] neg_hi:[0,1]
	v_pk_add_f32 v[240:241], v[238:239], v[242:243]
	v_pk_add_f32 v[238:239], v[238:239], v[242:243] op_sel:[1,1] op_sel_hi:[0,0] neg_lo:[1,0] neg_hi:[0,1]
	v_pk_add_f32 v[242:243], v[230:231], v[234:235]
	v_pk_add_f32 v[230:231], v[230:231], v[234:235] neg_lo:[0,1] neg_hi:[0,1]
	v_pk_add_f32 v[234:235], v[232:233], v[236:237]
	v_pk_add_f32 v[232:233], v[232:233], v[236:237] op_sel:[1,1] op_sel_hi:[0,0] neg_lo:[1,0] neg_hi:[0,1]
	v_pk_add_f32 v[236:237], v[244:245], v[240:241]
	v_pk_add_f32 v[240:241], v[244:245], v[240:241] neg_lo:[0,1] neg_hi:[0,1]
	v_pk_add_f32 v[244:245], v[250:251], v[238:239]
	v_pk_add_f32 v[250:251], v[250:251], v[238:239] neg_lo:[0,1] neg_hi:[0,1]
	v_pk_add_f32 v[238:239], v[242:243], v[234:235]
	v_pk_add_f32 v[234:235], v[242:243], v[234:235] neg_lo:[0,1] neg_hi:[0,1]
	v_pk_add_f32 v[242:243], v[230:231], v[232:233]
	v_pk_add_f32 v[230:231], v[230:231], v[232:233] neg_lo:[0,1] neg_hi:[0,1]
	ds_write2_b64 v248, v[236:237], v[238:239] offset1:1
	ds_write2_b64 v248, v[244:245], v[242:243] offset0:2 offset1:3
	ds_write2_b64 v248, v[240:241], v[234:235] offset0:4 offset1:5
	ds_write2_b64 v248, v[250:251], v[230:231] offset0:6 offset1:7
	v_add_u32_e32 v248, 0x12000, v2
	ds_read2_b64 v[230:233], v248 offset1:1
	ds_read2_b64 v[234:237], v248 offset0:2 offset1:3
	ds_read2_b64 v[238:241], v248 offset0:4 offset1:5
	ds_read2_b64 v[242:245], v248 offset0:6 offset1:7
	s_waitcnt lgkmcnt(9)
	v_pk_add_f32 v[4:5], v[102:103], v[110:111]
	v_pk_add_f32 v[102:103], v[102:103], v[110:111] neg_lo:[0,1] neg_hi:[0,1]
	v_pk_add_f32 v[110:111], v[104:105], v[112:113]
	v_pk_add_f32 v[104:105], v[104:105], v[112:113] neg_lo:[0,1] neg_hi:[0,1]
	v_mov_b64_e32 v[112:113], s[6:7]
	v_pk_mul_f32 v[118:119], v[104:105], v[112:113] op_sel_hi:[1,0]
	v_pk_fma_f32 v[104:105], v[104:105], v[112:113], v[118:119] op_sel:[1,1,0] op_sel_hi:[0,1,1] neg_lo:[1,0,0]
	s_waitcnt lgkmcnt(8)
	v_pk_add_f32 v[112:113], v[106:107], v[114:115]
	v_pk_add_f32 v[106:107], v[106:107], v[114:115] op_sel:[1,1] op_sel_hi:[0,0] neg_lo:[1,0] neg_hi:[0,1]
	v_pk_add_f32 v[114:115], v[108:109], v[116:117]
	v_pk_add_f32 v[108:109], v[108:109], v[116:117] neg_lo:[0,1] neg_hi:[0,1]
	v_mov_b64_e32 v[116:117], s[14:15]
	v_pk_mul_f32 v[118:119], v[108:109], v[116:117] op_sel_hi:[1,0]
	v_pk_fma_f32 v[108:109], v[108:109], v[116:117], v[118:119] op_sel:[1,1,0] op_sel_hi:[0,1,1] neg_lo:[1,0,0]
	v_pk_add_f32 v[116:117], v[4:5], v[112:113]
	v_pk_add_f32 v[4:5], v[4:5], v[112:113] neg_lo:[0,1] neg_hi:[0,1]
	v_pk_add_f32 v[112:113], v[110:111], v[114:115]
	v_pk_add_f32 v[110:111], v[110:111], v[114:115] op_sel:[1,1] op_sel_hi:[0,0] neg_lo:[1,0] neg_hi:[0,1]
	v_pk_add_f32 v[114:115], v[102:103], v[106:107]
	v_pk_add_f32 v[102:103], v[102:103], v[106:107] neg_lo:[0,1] neg_hi:[0,1]
	v_pk_add_f32 v[106:107], v[104:105], v[108:109]
	v_pk_add_f32 v[104:105], v[104:105], v[108:109] op_sel:[1,1] op_sel_hi:[0,0] neg_lo:[1,0] neg_hi:[0,1]
	v_pk_add_f32 v[108:109], v[116:117], v[112:113]
	v_pk_add_f32 v[112:113], v[116:117], v[112:113] neg_lo:[0,1] neg_hi:[0,1]
	v_pk_add_f32 v[116:117], v[4:5], v[110:111]
	v_pk_add_f32 v[4:5], v[4:5], v[110:111] neg_lo:[0,1] neg_hi:[0,1]
	v_pk_add_f32 v[110:111], v[114:115], v[106:107]
	v_pk_add_f32 v[106:107], v[114:115], v[106:107] neg_lo:[0,1] neg_hi:[0,1]
	v_pk_add_f32 v[114:115], v[102:103], v[104:105]
	v_pk_add_f32 v[102:103], v[102:103], v[104:105] neg_lo:[0,1] neg_hi:[0,1]
	ds_write2_b64 v3, v[108:109], v[110:111] offset1:1
	ds_write2_b64 v3, v[116:117], v[114:115] offset0:2 offset1:3
	ds_write2_b64 v3, v[112:113], v[106:107] offset0:4 offset1:5
	ds_write2_b64 v3, v[4:5], v[102:103] offset0:6 offset1:7
	v_add_u32_e32 v3, 0x1b000, v2
	ds_read2_b64 v[102:105], v3 offset1:1
	ds_read2_b64 v[106:109], v3 offset0:2 offset1:3
	ds_read2_b64 v[110:113], v3 offset0:4 offset1:5
	ds_read2_b64 v[114:117], v3 offset0:6 offset1:7
	s_waitcnt lgkmcnt(9)
	v_pk_add_f32 v[250:251], v[230:231], v[238:239]
	v_pk_add_f32 v[230:231], v[230:231], v[238:239] neg_lo:[0,1] neg_hi:[0,1]
	v_pk_add_f32 v[238:239], v[232:233], v[240:241]
	v_pk_add_f32 v[232:233], v[232:233], v[240:241] neg_lo:[0,1] neg_hi:[0,1]
	v_mov_b64_e32 v[240:241], s[6:7]
	v_pk_mul_f32 v[246:247], v[232:233], v[240:241] op_sel_hi:[1,0]
	v_pk_fma_f32 v[232:233], v[232:233], v[240:241], v[246:247] op_sel:[1,1,0] op_sel_hi:[0,1,1] neg_lo:[1,0,0]
	s_waitcnt lgkmcnt(8)
	v_pk_add_f32 v[240:241], v[234:235], v[242:243]
	v_pk_add_f32 v[234:235], v[234:235], v[242:243] op_sel:[1,1] op_sel_hi:[0,0] neg_lo:[1,0] neg_hi:[0,1]
	v_pk_add_f32 v[242:243], v[236:237], v[244:245]
	v_pk_add_f32 v[236:237], v[236:237], v[244:245] neg_lo:[0,1] neg_hi:[0,1]
	v_mov_b64_e32 v[244:245], s[14:15]
	v_pk_mul_f32 v[246:247], v[236:237], v[244:245] op_sel_hi:[1,0]
	v_pk_fma_f32 v[236:237], v[236:237], v[244:245], v[246:247] op_sel:[1,1,0] op_sel_hi:[0,1,1] neg_lo:[1,0,0]
	v_pk_add_f32 v[244:245], v[250:251], v[240:241]
	v_pk_add_f32 v[250:251], v[250:251], v[240:241] neg_lo:[0,1] neg_hi:[0,1]
	v_pk_add_f32 v[240:241], v[238:239], v[242:243]
	v_pk_add_f32 v[238:239], v[238:239], v[242:243] op_sel:[1,1] op_sel_hi:[0,0] neg_lo:[1,0] neg_hi:[0,1]
	v_pk_add_f32 v[242:243], v[230:231], v[234:235]
	v_pk_add_f32 v[230:231], v[230:231], v[234:235] neg_lo:[0,1] neg_hi:[0,1]
	v_pk_add_f32 v[234:235], v[232:233], v[236:237]
	v_pk_add_f32 v[232:233], v[232:233], v[236:237] op_sel:[1,1] op_sel_hi:[0,0] neg_lo:[1,0] neg_hi:[0,1]
	v_pk_add_f32 v[236:237], v[244:245], v[240:241]
	v_pk_add_f32 v[240:241], v[244:245], v[240:241] neg_lo:[0,1] neg_hi:[0,1]
	v_pk_add_f32 v[244:245], v[250:251], v[238:239]
	v_pk_add_f32 v[250:251], v[250:251], v[238:239] neg_lo:[0,1] neg_hi:[0,1]
	v_pk_add_f32 v[238:239], v[242:243], v[234:235]
	v_pk_add_f32 v[234:235], v[242:243], v[234:235] neg_lo:[0,1] neg_hi:[0,1]
	v_pk_add_f32 v[242:243], v[230:231], v[232:233]
	v_pk_add_f32 v[230:231], v[230:231], v[232:233] neg_lo:[0,1] neg_hi:[0,1]
	ds_write2_b64 v248, v[236:237], v[238:239] offset1:1
	ds_write2_b64 v248, v[244:245], v[242:243] offset0:2 offset1:3
	ds_write2_b64 v248, v[240:241], v[234:235] offset0:4 offset1:5
	ds_write2_b64 v248, v[250:251], v[230:231] offset0:6 offset1:7
	s_waitcnt lgkmcnt(5)
	v_pk_add_f32 v[4:5], v[102:103], v[110:111]
	v_pk_add_f32 v[102:103], v[102:103], v[110:111] neg_lo:[0,1] neg_hi:[0,1]
	v_pk_add_f32 v[110:111], v[104:105], v[112:113]
	v_pk_add_f32 v[104:105], v[104:105], v[112:113] neg_lo:[0,1] neg_hi:[0,1]
	v_mov_b64_e32 v[112:113], s[6:7]
	v_pk_mul_f32 v[118:119], v[104:105], v[112:113] op_sel_hi:[1,0]
	v_pk_fma_f32 v[104:105], v[104:105], v[112:113], v[118:119] op_sel:[1,1,0] op_sel_hi:[0,1,1] neg_lo:[1,0,0]
	s_waitcnt lgkmcnt(4)
	v_pk_add_f32 v[112:113], v[106:107], v[114:115]
	v_pk_add_f32 v[106:107], v[106:107], v[114:115] op_sel:[1,1] op_sel_hi:[0,0] neg_lo:[1,0] neg_hi:[0,1]
	v_pk_add_f32 v[114:115], v[108:109], v[116:117]
	v_pk_add_f32 v[108:109], v[108:109], v[116:117] neg_lo:[0,1] neg_hi:[0,1]
	v_mov_b64_e32 v[116:117], s[14:15]
	v_pk_mul_f32 v[118:119], v[108:109], v[116:117] op_sel_hi:[1,0]
	v_pk_fma_f32 v[108:109], v[108:109], v[116:117], v[118:119] op_sel:[1,1,0] op_sel_hi:[0,1,1] neg_lo:[1,0,0]
	v_pk_add_f32 v[116:117], v[4:5], v[112:113]
	v_pk_add_f32 v[4:5], v[4:5], v[112:113] neg_lo:[0,1] neg_hi:[0,1]
	v_pk_add_f32 v[112:113], v[110:111], v[114:115]
	v_pk_add_f32 v[110:111], v[110:111], v[114:115] op_sel:[1,1] op_sel_hi:[0,0] neg_lo:[1,0] neg_hi:[0,1]
	v_pk_add_f32 v[114:115], v[102:103], v[106:107]
	v_pk_add_f32 v[102:103], v[102:103], v[106:107] neg_lo:[0,1] neg_hi:[0,1]
	v_pk_add_f32 v[106:107], v[104:105], v[108:109]
	v_pk_add_f32 v[104:105], v[104:105], v[108:109] op_sel:[1,1] op_sel_hi:[0,0] neg_lo:[1,0] neg_hi:[0,1]
	v_pk_add_f32 v[108:109], v[116:117], v[112:113]
	v_pk_add_f32 v[112:113], v[116:117], v[112:113] neg_lo:[0,1] neg_hi:[0,1]
	v_pk_add_f32 v[116:117], v[4:5], v[110:111]
	v_pk_add_f32 v[4:5], v[4:5], v[110:111] neg_lo:[0,1] neg_hi:[0,1]
	v_pk_add_f32 v[110:111], v[114:115], v[106:107]
	v_pk_add_f32 v[106:107], v[114:115], v[106:107] neg_lo:[0,1] neg_hi:[0,1]
	v_pk_add_f32 v[114:115], v[102:103], v[104:105]
	v_pk_add_f32 v[102:103], v[102:103], v[104:105] neg_lo:[0,1] neg_hi:[0,1]
	ds_write2_b64 v3, v[108:109], v[110:111] offset1:1
	ds_write2_b64 v3, v[116:117], v[114:115] offset0:2 offset1:3
	ds_write2_b64 v3, v[112:113], v[106:107] offset0:4 offset1:5
	ds_write2_b64 v3, v[4:5], v[102:103] offset0:6 offset1:7
	s_mov_b32 s85, 0x24000
	s_cmp_lg_u32 s85, 0x24000
	v_mov_b32_e32 v4, v204
	s_waitcnt lgkmcnt(0)
	s_barrier
	s_mov_b32 s85, 0
	v_and_b32_e32 v5, 7, v4
	v_cvt_f32_ubyte0_e32 v2, v5
	v_mul_f32_e32 v3, 0x3c800000, v2
	v_cos_f32_e32 v2, v3
	v_sin_f32_e32 v3, v3
	v_lshlrev_b32_e32 v4, 3, v4
	v_lshl_add_u32 v5, v5, 3, 0
